# adds: mlstm_D epilogue o-gate/gain/bcum loads hoisted; L0 A5 f32-residual epilogue loads of 5 row groups hoisted; xattn PV staging waits skip the younger stores; routing logits loop software-pipelined
# speedup vs baseline: 1.0110x; 1.0021x over previous
; #define LAS __attribute__((address_space(3)))
; __device__ __forceinline__ unsigned cvt_pk_bf16(float lo, float hi) { unsigned r; asm volatile("v_cvt_pk_bf16_f32 %0, %1, %2" : "=v"(r) : "v"(lo), "v"(hi)); return r; }
; __device__ __forceinline__ void mlstm_D(LAS unsigned char* lds, int c, int h, const bf16_t* Z, const float* gi, const float* bcum, const float* marr, const bf16_t* CST, const float* NST,
;                                         const float* hgain, bf16_t* YCAT) {
;     ...
;         u32x2 w; w.x = cvt_pk_bf16(pv[0], pv[1]); w.y = cvt_pk_bf16(pv[2], pv[3]);
;         *(LAS u32x2*)(Pw + fr * PRS + (16 * j + 4 * fq) * 2) = w; }
;     rsum += __shfl_xor(rsum, 16); rsum += __shfl_xor(rsum, 32);
;     const float den = wi * nq + rsum;
;     f32x4 acc[16];
; #pragma unroll
;     for (int j = 0; j < 16; ++j) acc[j] = (f32x4){0.f, 0.f, 0.f, 0.f};
;     const bf16_t* cst = CST + (size_t)(c * NH + h) * DH * DH;
; #pragma unroll
;     for (int half = 0; half < 2; ++half) {
;         __syncthreads();
;         stage_tile<DH, 128, 8>(X, cst + half * 128, DH, tid);
;         __syncthreads();
.LBB0_769:
	s_or_b64 exec, exec, s[2:3]
	v_cvt_pk_bf16_f32 v2, v59, v52
	v_cvt_pk_bf16_f32 v3, v55, v53
	ds_write_b64 v30, v[2:3] offset:224
	v_lshrrev_b32_e32 v2, 28, v122
	v_lshrrev_b32_e32 v6, 28, v124
	v_add_u32_e32 v2, v99, v2
	v_add_u32_e32 v6, v118, v6
	v_lshrrev_b32_e32 v10, 28, v126
	v_ashrrev_i32_e32 v16, 4, v2
	v_ashrrev_i32_e32 v20, 4, v6
	v_add_u32_e32 v10, v119, v10
	v_and_b32_e32 v2, -16, v2
	v_ashrrev_i32_e32 v17, 31, v16
	v_and_b32_e32 v6, -16, v6
	v_ashrrev_i32_e32 v21, 31, v20
	v_ashrrev_i32_e32 v64, 4, v10
	v_and_b32_e32 v10, -16, v10
	v_sub_u32_e32 v135, v99, v2
	v_lshlrev_b64 v[2:3], 9, v[16:17]
	v_sub_u32_e32 v17, v118, v6
	v_lshlrev_b64 v[6:7], 9, v[20:21]
	v_sub_u32_e32 v21, v119, v10
	v_lshrrev_b32_e32 v10, 28, v128
	v_add_u32_e32 v10, v120, v10
	v_ashrrev_i32_e32 v65, 31, v64
	v_ashrrev_i32_e32 v118, 4, v10
	v_and_b32_e32 v10, -16, v10
	v_lshlrev_b64 v[30:31], 9, v[64:65]
	v_sub_u32_e32 v65, v120, v10
	v_lshrrev_b32_e32 v10, 28, v130
	v_add_u32_e32 v10, v123, v10
	v_ashrrev_i32_e32 v119, 31, v118
	v_ashrrev_i32_e32 v136, 4, v10
	v_and_b32_e32 v10, -16, v10
	v_lshlrev_b64 v[34:35], 9, v[118:119]
	v_sub_u32_e32 v119, v123, v10
	v_lshrrev_b32_e32 v10, 28, v131
	v_add_u32_e32 v10, v125, v10
	v_ashrrev_i32_e32 v138, 4, v10
	v_and_b32_e32 v10, -16, v10
	v_sub_u32_e32 v120, v125, v10
	v_lshrrev_b32_e32 v10, 28, v132
	v_add_u32_e32 v10, v127, v10
	s_ashr_i32 s23, s22, 31
	v_ashrrev_i32_e32 v137, 31, v136
	v_ashrrev_i32_e32 v140, 4, v10
	v_and_b32_e32 v10, -16, v10
	s_lshl_b64 s[2:3], s[22:23], 17
	v_lshlrev_b64 v[60:61], 9, v[136:137]
	v_sub_u32_e32 v137, v127, v10
	v_lshrrev_b32_e32 v10, 28, v133
	s_add_u32 s2, s56, s2
	v_add_u32_e32 v10, v129, v10
	s_addc_u32 s3, s57, s3
	v_lshlrev_b32_e32 v4, 3, v135
	v_ashrrev_i32_e32 v139, 31, v138
	v_ashrrev_i32_e32 v141, 31, v140
	v_ashrrev_i32_e32 v142, 4, v10
	v_and_b32_e32 v10, -16, v10
	v_ashrrev_i32_e32 v5, 31, v4
	v_lshlrev_b32_e32 v32, 3, v21
	v_lshlrev_b32_e32 v62, 3, v119
	v_lshlrev_b64 v[122:123], 9, v[138:139]
	v_lshlrev_b64 v[126:127], 9, v[140:141]
	v_lshlrev_b32_e32 v130, 3, v137
	v_sub_u32_e32 v139, v129, v10
	v_ashrrev_i32_e32 v143, 31, v142
	v_lshl_add_u64 v[2:3], s[2:3], 0, v[2:3]
	v_lshlrev_b32_e32 v8, 3, v17
	v_ashrrev_i32_e32 v33, 31, v32
	v_lshlrev_b32_e32 v36, 3, v65
	v_ashrrev_i32_e32 v63, 31, v62
	v_lshlrev_b32_e32 v124, 3, v120
	v_ashrrev_i32_e32 v131, 31, v130
	v_lshlrev_b64 v[128:129], 9, v[142:143]
	v_lshlrev_b32_e32 v132, 3, v139
	v_lshl_add_u64 v[2:3], v[4:5], 1, v[2:3]
	v_lshl_add_u64 v[4:5], s[2:3], 0, v[6:7]
	v_lshl_add_u64 v[6:7], s[2:3], 0, v[30:31]
	v_lshl_add_u64 v[60:61], s[2:3], 0, v[60:61]
	v_lshl_add_u64 v[126:127], s[2:3], 0, v[126:127]
	v_ashrrev_i32_e32 v9, 31, v8
	v_ashrrev_i32_e32 v37, 31, v36
	v_ashrrev_i32_e32 v125, 31, v124
	v_ashrrev_i32_e32 v133, 31, v132
	v_lshl_add_u64 v[6:7], v[32:33], 1, v[6:7]
	v_lshl_add_u64 v[30:31], s[2:3], 0, v[34:35]
	v_lshl_add_u64 v[196:197], v[62:63], 1, v[60:61]
	v_lshl_add_u64 v[60:61], s[2:3], 0, v[122:123]
	v_lshl_add_u64 v[204:205], v[130:131], 1, v[126:127]
	v_lshl_add_u64 v[126:127], s[2:3], 0, v[128:129]
	s_waitcnt lgkmcnt(0)
	s_barrier
	v_lshl_add_u64 v[4:5], v[8:9], 1, v[4:5]
	global_load_dwordx4 v[8:11], v[2:3], off
	global_load_dwordx4 v[12:15], v[4:5], off
	v_lshl_add_u64 v[192:193], v[36:37], 1, v[30:31]
	global_load_dwordx4 v[30:33], v[6:7], off
	global_load_dwordx4 v[34:37], v[192:193], off
	v_lshl_add_u64 v[200:201], v[124:125], 1, v[60:61]
	global_load_dwordx4 v[60:63], v[196:197], off
	global_load_dwordx4 v[122:125], v[200:201], off
	v_lshl_add_u64 v[208:209], v[132:133], 1, v[126:127]
	global_load_dwordx4 v[126:129], v[204:205], off
	global_load_dwordx4 v[130:133], v[208:209], off
	v_mul_lo_u32 v20, v20, s74
	v_lshlrev_b32_e32 v17, 4, v17
	v_add3_u32 v17, s51, v20, v17
	v_mul_lo_u32 v20, v64, s74
	v_lshlrev_b32_e32 v21, 4, v21
	v_add3_u32 v20, s51, v20, v21
	v_mul_lo_u32 v21, v118, s74
	v_lshlrev_b32_e32 v64, 4, v65
	v_add3_u32 v21, s51, v21, v64
	v_mul_lo_u32 v64, v136, s74
	v_lshlrev_b32_e32 v65, 4, v119
	v_add3_u32 v64, s51, v64, v65
	v_mul_lo_u32 v65, v138, s74
	v_lshlrev_b32_e32 v118, 4, v120
	v_mul_lo_u32 v16, v16, s74
	v_lshlrev_b32_e32 v135, 4, v135
	v_add3_u32 v65, s51, v65, v118
	v_mul_lo_u32 v118, v140, s74
	v_lshlrev_b32_e32 v119, 4, v137
	v_add3_u32 v16, s51, v16, v135
	v_add3_u32 v119, s51, v118, v119
	v_mul_lo_u32 v118, v142, s74
	v_lshlrev_b32_e32 v120, 4, v139
	v_add3_u32 v135, s51, v118, v120
	s_waitcnt vmcnt(7)
	ds_write_b128 v16, v[8:11]
	s_waitcnt vmcnt(6)
	ds_write_b128 v17, v[12:15]
	s_waitcnt vmcnt(5)
	ds_write_b128 v20, v[30:33]
	s_waitcnt vmcnt(4)
	ds_write_b128 v21, v[34:37]
	s_waitcnt vmcnt(3)
	ds_write_b128 v64, v[60:63]
	s_waitcnt vmcnt(2)
	ds_write_b128 v65, v[122:125]
	s_waitcnt vmcnt(1)
	ds_write_b128 v119, v[126:129]
	s_waitcnt vmcnt(0)
	ds_write_b128 v135, v[130:133]
	s_waitcnt lgkmcnt(0)
	s_barrier
; #define MFMA16(b, a, c) __builtin_amdgcn_mfma_f32_16x16x32_bf16((b), (a), (c), 0, 0, 0)
; __device__ __forceinline__ void mlstm_D(LAS unsigned char* lds, int c, int h, const bf16_t* Z, const float* gi, const float* bcum, const float* marr, const bf16_t* CST, const float* NST,
;                                         const float* hgain, bf16_t* YCAT) {
;     ...
; #pragma unroll
;         for (int ks = 0; ks < 4; ++ks)
;             { const bf16x8 aqh = *(const bf16x8*)(Z + trow * EVN + 1024 + h * DH + 32 * (half * 4 + ks) + 8 * fq);
; #pragma unroll
;               for (int j = 0; j < 16; ++j) acc[j] = MFMA16(row_frag(X, (128 + 8) * 2, 16 * j, 32 * ks, lane), aqh, acc[j]);
;               asm volatile("" ::: "memory"); }
	global_load_dwordx4 v[8:11], v[90:91], off offset:2048
	v_mul_u32_u24_e32 v118, 0x110, v71
	v_add_u32_e32 v228, v121, v118
	ds_read_b128 v[12:15], v228
	ds_read_b128 v[30:33], v228 offset:4352
	ds_read_b128 v[34:37], v228 offset:8704
	ds_read_b128 v[60:63], v228 offset:13056
	ds_read_b128 v[120:123], v228 offset:17408
	ds_read_b128 v[124:127], v228 offset:21760
	ds_read_b128 v[128:131], v228 offset:26112
	ds_read_b128 v[136:139], v228 offset:30464
	ds_read_b128 v[140:143], v228 offset:34816
	ds_read_b128 v[144:147], v228 offset:39168
	ds_read_b128 v[148:151], v228 offset:43520
	ds_read_b128 v[152:155], v228 offset:47872
	ds_read_b128 v[156:159], v228 offset:52224
	ds_read_b128 v[160:163], v228 offset:56576
	ds_read_b128 v[164:167], v228 offset:60928
	ds_read_b128 v[168:171], v228 offset:65280
	global_load_dwordx4 v[172:175], v[90:91], off offset:2112
	s_waitcnt vmcnt(1) lgkmcnt(14)
	v_mfma_f32_16x16x32_bf16 v[12:15], v[12:15], v[8:11], 0
	ds_read_b128 v[176:179], v228 offset:64
	v_mad_i64_i32 v[132:133], s[2:3], v101, s68, 0
	v_mfma_f32_16x16x32_bf16 v[30:33], v[30:33], v[8:11], 0
	v_ashrrev_i32_e32 v71, 31, v70
	s_waitcnt lgkmcnt(14)
	v_mfma_f32_16x16x32_bf16 v[34:37], v[34:37], v[8:11], 0
	s_waitcnt lgkmcnt(13)
	v_mfma_f32_16x16x32_bf16 v[60:63], v[60:63], v[8:11], 0
	s_waitcnt lgkmcnt(12)
	v_mfma_f32_16x16x32_bf16 v[120:123], v[120:123], v[8:11], 0
	s_waitcnt lgkmcnt(11)
	v_mfma_f32_16x16x32_bf16 v[124:127], v[124:127], v[8:11], 0
	s_waitcnt lgkmcnt(10)
	v_mfma_f32_16x16x32_bf16 v[128:131], v[128:131], v[8:11], 0
	s_waitcnt lgkmcnt(9)
	v_mfma_f32_16x16x32_bf16 v[136:139], v[136:139], v[8:11], 0
	s_waitcnt lgkmcnt(8)
	v_mfma_f32_16x16x32_bf16 v[140:143], v[140:143], v[8:11], 0
	s_waitcnt lgkmcnt(7)
	v_mfma_f32_16x16x32_bf16 v[144:147], v[144:147], v[8:11], 0
	s_waitcnt lgkmcnt(6)
	v_mfma_f32_16x16x32_bf16 v[148:151], v[148:151], v[8:11], 0
	s_waitcnt lgkmcnt(5)
	v_mfma_f32_16x16x32_bf16 v[152:155], v[152:155], v[8:11], 0
	s_waitcnt lgkmcnt(4)
	v_mfma_f32_16x16x32_bf16 v[156:159], v[156:159], v[8:11], 0
	s_waitcnt lgkmcnt(3)
	v_mfma_f32_16x16x32_bf16 v[160:163], v[160:163], v[8:11], 0
	s_waitcnt lgkmcnt(2)
	v_mfma_f32_16x16x32_bf16 v[164:167], v[164:167], v[8:11], 0
	s_waitcnt lgkmcnt(1)
	v_mfma_f32_16x16x32_bf16 v[8:11], v[168:171], v[8:11], 0
	ds_read_b128 v[168:171], v228 offset:4416
	s_waitcnt vmcnt(0) lgkmcnt(1)
	v_mfma_f32_16x16x32_bf16 v[12:15], v[176:179], v[172:175], v[12:15]
	ds_read_b128 v[176:179], v228 offset:8768
	s_waitcnt lgkmcnt(1)
	v_mfma_f32_16x16x32_bf16 v[30:33], v[168:171], v[172:175], v[30:33]
	ds_read_b128 v[168:171], v228 offset:13120
	s_waitcnt lgkmcnt(1)
	v_mfma_f32_16x16x32_bf16 v[34:37], v[176:179], v[172:175], v[34:37]
	ds_read_b128 v[176:179], v228 offset:17472
	s_waitcnt lgkmcnt(1)
	v_mfma_f32_16x16x32_bf16 v[60:63], v[168:171], v[172:175], v[60:63]
	ds_read_b128 v[168:171], v228 offset:21824
	s_waitcnt lgkmcnt(1)
	v_mfma_f32_16x16x32_bf16 v[120:123], v[176:179], v[172:175], v[120:123]
	ds_read_b128 v[176:179], v228 offset:26176
	s_waitcnt lgkmcnt(1)
	v_mfma_f32_16x16x32_bf16 v[124:127], v[168:171], v[172:175], v[124:127]
	ds_read_b128 v[168:171], v228 offset:30528
	s_waitcnt lgkmcnt(1)
	v_mfma_f32_16x16x32_bf16 v[128:131], v[176:179], v[172:175], v[128:131]
	ds_read_b128 v[176:179], v228 offset:34880
	s_waitcnt lgkmcnt(1)
	v_mfma_f32_16x16x32_bf16 v[136:139], v[168:171], v[172:175], v[136:139]
	ds_read_b128 v[168:171], v228 offset:39232
	s_waitcnt lgkmcnt(1)
	v_mfma_f32_16x16x32_bf16 v[140:143], v[176:179], v[172:175], v[140:143]
	ds_read_b128 v[176:179], v228 offset:43584
	s_waitcnt lgkmcnt(1)
	v_mfma_f32_16x16x32_bf16 v[144:147], v[168:171], v[172:175], v[144:147]
	ds_read_b128 v[168:171], v228 offset:47936
	s_waitcnt lgkmcnt(1)
	v_mfma_f32_16x16x32_bf16 v[148:151], v[176:179], v[172:175], v[148:151]
	ds_read_b128 v[176:179], v228 offset:52288
	s_waitcnt lgkmcnt(1)
	v_mfma_f32_16x16x32_bf16 v[152:155], v[168:171], v[172:175], v[152:155]
	ds_read_b128 v[168:171], v228 offset:56640
	s_waitcnt lgkmcnt(1)
	v_mfma_f32_16x16x32_bf16 v[156:159], v[176:179], v[172:175], v[156:159]
	s_waitcnt lgkmcnt(0)
	v_mfma_f32_16x16x32_bf16 v[160:163], v[168:171], v[172:175], v[160:163]
	ds_read_b128 v[168:171], v228 offset:60992
	ds_read_b128 v[176:179], v228 offset:65344
	global_load_dwordx4 v[180:183], v[90:91], off offset:2176
	s_waitcnt lgkmcnt(1)
	v_mfma_f32_16x16x32_bf16 v[164:167], v[168:171], v[172:175], v[164:167]
	ds_read_b128 v[168:171], v228 offset:128
	s_waitcnt lgkmcnt(1)
	v_mfma_f32_16x16x32_bf16 v[8:11], v[176:179], v[172:175], v[8:11]
	ds_read_b128 v[172:175], v228 offset:4480
	s_waitcnt vmcnt(0) lgkmcnt(1)
	v_mfma_f32_16x16x32_bf16 v[12:15], v[168:171], v[180:183], v[12:15]
	ds_read_b128 v[168:171], v228 offset:8832
	s_waitcnt lgkmcnt(1)
	v_mfma_f32_16x16x32_bf16 v[30:33], v[172:175], v[180:183], v[30:33]
	ds_read_b128 v[172:175], v228 offset:13184
	s_waitcnt lgkmcnt(1)
	v_mfma_f32_16x16x32_bf16 v[34:37], v[168:171], v[180:183], v[34:37]
	ds_read_b128 v[168:171], v228 offset:17536
	s_waitcnt lgkmcnt(1)
	v_mfma_f32_16x16x32_bf16 v[60:63], v[172:175], v[180:183], v[60:63]
	ds_read_b128 v[172:175], v228 offset:21888
	s_waitcnt lgkmcnt(1)
	v_mfma_f32_16x16x32_bf16 v[120:123], v[168:171], v[180:183], v[120:123]
	ds_read_b128 v[168:171], v228 offset:26240
	s_waitcnt lgkmcnt(1)
	v_mfma_f32_16x16x32_bf16 v[124:127], v[172:175], v[180:183], v[124:127]
	ds_read_b128 v[172:175], v228 offset:30592
	s_waitcnt lgkmcnt(1)
	v_mfma_f32_16x16x32_bf16 v[128:131], v[168:171], v[180:183], v[128:131]
	ds_read_b128 v[168:171], v228 offset:34944
	s_waitcnt lgkmcnt(1)
; #define MFMA16(b, a, c) __builtin_amdgcn_mfma_f32_16x16x32_bf16((b), (a), (c), 0, 0, 0)
; __device__ __forceinline__ void mlstm_D(LAS unsigned char* lds, int c, int h, const bf16_t* Z, const float* gi, const float* bcum, const float* marr, const bf16_t* CST, const float* NST,
;                                         const float* hgain, bf16_t* YCAT) {
;     ...
;     for (int half = 0; half < 2; ++half) {
;         __syncthreads();
;         stage_tile<DH, 128, 8>(X, cst + half * 128, DH, tid);
;         __syncthreads();
; #pragma unroll
;         for (int ks = 0; ks < 4; ++ks)
;             { const bf16x8 aqh = *(const bf16x8*)(Z + trow * EVN + 1024 + h * DH + 32 * (half * 4 + ks) + 8 * fq);
; #pragma unroll
;               for (int j = 0; j < 16; ++j) acc[j] = MFMA16(row_frag(X, (128 + 8) * 2, 16 * j, 32 * ks, lane), aqh, acc[j]);
;               asm volatile("" ::: "memory"); }
	v_mfma_f32_16x16x32_bf16 v[136:139], v[172:175], v[180:183], v[136:139]
	ds_read_b128 v[172:175], v228 offset:39296
	s_waitcnt lgkmcnt(1)
	v_mfma_f32_16x16x32_bf16 v[140:143], v[168:171], v[180:183], v[140:143]
	ds_read_b128 v[168:171], v228 offset:43648
	s_waitcnt lgkmcnt(1)
	v_mfma_f32_16x16x32_bf16 v[144:147], v[172:175], v[180:183], v[144:147]
	ds_read_b128 v[172:175], v228 offset:48000
	s_waitcnt lgkmcnt(1)
	v_mfma_f32_16x16x32_bf16 v[148:151], v[168:171], v[180:183], v[148:151]
	ds_read_b128 v[168:171], v228 offset:52352
	s_waitcnt lgkmcnt(1)
	v_mfma_f32_16x16x32_bf16 v[152:155], v[172:175], v[180:183], v[152:155]
	ds_read_b128 v[172:175], v228 offset:56704
	s_waitcnt lgkmcnt(1)
	v_mfma_f32_16x16x32_bf16 v[156:159], v[168:171], v[180:183], v[156:159]
	s_waitcnt lgkmcnt(0)
	v_mfma_f32_16x16x32_bf16 v[160:163], v[172:175], v[180:183], v[160:163]
	ds_read_b128 v[168:171], v228 offset:61056
	ds_read_b128 v[172:175], v228 offset:65408
	global_load_dwordx4 v[176:179], v[90:91], off offset:2240
	s_waitcnt lgkmcnt(1)
	v_mfma_f32_16x16x32_bf16 v[164:167], v[168:171], v[180:183], v[164:167]
	ds_read_b128 v[168:171], v228 offset:192
	s_waitcnt lgkmcnt(1)
	v_mfma_f32_16x16x32_bf16 v[8:11], v[172:175], v[180:183], v[8:11]
	ds_read_b128 v[172:175], v228 offset:4544
	s_waitcnt vmcnt(0) lgkmcnt(1)
	v_mfma_f32_16x16x32_bf16 v[12:15], v[168:171], v[176:179], v[12:15]
	ds_read_b128 v[168:171], v228 offset:8896
	s_waitcnt lgkmcnt(1)
	v_mfma_f32_16x16x32_bf16 v[30:33], v[172:175], v[176:179], v[30:33]
	ds_read_b128 v[172:175], v228 offset:13248
	s_waitcnt lgkmcnt(1)
	v_mfma_f32_16x16x32_bf16 v[34:37], v[168:171], v[176:179], v[34:37]
	ds_read_b128 v[168:171], v228 offset:17600
	s_waitcnt lgkmcnt(1)
	v_mfma_f32_16x16x32_bf16 v[60:63], v[172:175], v[176:179], v[60:63]
	ds_read_b128 v[172:175], v228 offset:21952
	s_waitcnt lgkmcnt(1)
	v_mfma_f32_16x16x32_bf16 v[120:123], v[168:171], v[176:179], v[120:123]
	ds_read_b128 v[168:171], v228 offset:26304
	s_waitcnt lgkmcnt(1)
	v_mfma_f32_16x16x32_bf16 v[124:127], v[172:175], v[176:179], v[124:127]
	ds_read_b128 v[172:175], v228 offset:30656
	s_waitcnt lgkmcnt(1)
	v_mfma_f32_16x16x32_bf16 v[128:131], v[168:171], v[176:179], v[128:131]
	ds_read_b128 v[168:171], v228 offset:35008
	s_waitcnt lgkmcnt(1)
	v_mfma_f32_16x16x32_bf16 v[136:139], v[172:175], v[176:179], v[136:139]
	ds_read_b128 v[172:175], v228 offset:39360
	s_waitcnt lgkmcnt(1)
	v_mfma_f32_16x16x32_bf16 v[140:143], v[168:171], v[176:179], v[140:143]
	ds_read_b128 v[168:171], v228 offset:43712
	s_waitcnt lgkmcnt(1)
	v_mfma_f32_16x16x32_bf16 v[144:147], v[172:175], v[176:179], v[144:147]
	ds_read_b128 v[172:175], v228 offset:48064
	s_waitcnt lgkmcnt(1)
	v_mfma_f32_16x16x32_bf16 v[148:151], v[168:171], v[176:179], v[148:151]
	s_waitcnt lgkmcnt(0)
	v_mfma_f32_16x16x32_bf16 v[152:155], v[172:175], v[176:179], v[152:155]
	ds_read_b128 v[168:171], v228 offset:52416
	ds_read_b128 v[172:175], v228 offset:56768
	s_waitcnt lgkmcnt(1)
	v_mfma_f32_16x16x32_bf16 v[156:159], v[168:171], v[176:179], v[156:159]
	ds_read_b128 v[168:171], v228 offset:61120
	ds_read_b128 v[180:183], v228 offset:65472
	s_waitcnt lgkmcnt(0)
	s_barrier
	global_load_dwordx4 v[184:187], v[2:3], off offset:256
	s_nop 0
	global_load_dwordx4 v[2:5], v[4:5], off offset:256
	s_nop 0
	global_load_dwordx4 v[188:191], v[6:7], off offset:256
	s_nop 0
	global_load_dwordx4 v[192:195], v[192:193], off offset:256
	s_nop 0
	global_load_dwordx4 v[196:199], v[196:197], off offset:256
	s_nop 0
	global_load_dwordx4 v[200:203], v[200:201], off offset:256
	s_nop 0
	global_load_dwordx4 v[204:207], v[204:205], off offset:256
	s_nop 0
	global_load_dwordx4 v[208:211], v[208:209], off offset:256
	s_waitcnt vmcnt(7)
	ds_write_b128 v16, v[184:187]
	s_waitcnt vmcnt(6)
	ds_write_b128 v17, v[2:5]
	s_waitcnt vmcnt(5)
	ds_write_b128 v20, v[188:191]
	s_waitcnt vmcnt(4)
	ds_write_b128 v21, v[192:195]
	s_waitcnt vmcnt(3)
	ds_write_b128 v64, v[196:199]
	s_waitcnt vmcnt(2)
	ds_write_b128 v65, v[200:203]
	s_waitcnt vmcnt(1)
	ds_write_b128 v119, v[204:207]
	s_waitcnt vmcnt(0)
	ds_write_b128 v135, v[208:211]
	s_waitcnt lgkmcnt(0)
	s_barrier
	global_load_dwordx4 v[2:5], v[90:91], off offset:2304
	v_mfma_f32_16x16x32_bf16 v[164:167], v[168:171], v[176:179], v[164:167]
	ds_read_b128 v[168:171], v228
	v_mad_i64_i32 v[64:65], s[2:3], v93, s68, 0
	v_mfma_f32_16x16x32_bf16 v[160:163], v[172:175], v[176:179], v[160:163]
	ds_read_b128 v[172:175], v228 offset:4352
	v_and_b32_e32 v119, 63, v99
	v_mfma_f32_16x16x32_bf16 v[6:9], v[180:183], v[176:179], v[8:11]
	s_waitcnt vmcnt(0) lgkmcnt(1)
	v_mfma_f32_16x16x32_bf16 v[10:13], v[168:171], v[2:5], v[12:15]
	s_nop 2
	ds_read_b128 v[14:17], v228 offset:8704
	ds_read_b128 v[168:171], v228 offset:13056
	s_waitcnt lgkmcnt(1)
	v_mfma_f32_16x16x32_bf16 v[14:17], v[14:17], v[2:5], v[34:37]
	s_nop 2
	ds_read_b128 v[34:37], v228 offset:17408
	s_waitcnt lgkmcnt(1)
	v_mfma_f32_16x16x32_bf16 v[60:63], v[168:171], v[2:5], v[60:63]
	ds_read_b128 v[168:171], v228 offset:21760
	s_waitcnt lgkmcnt(1)
	v_mfma_f32_16x16x32_bf16 v[34:37], v[34:37], v[2:5], v[120:123]
	s_nop 2
	ds_read_b128 v[120:123], v228 offset:26112
	s_waitcnt lgkmcnt(1)
	v_mfma_f32_16x16x32_bf16 v[124:127], v[168:171], v[2:5], v[124:127]
	ds_read_b128 v[168:171], v228 offset:30464
	s_waitcnt lgkmcnt(1)
	v_mfma_f32_16x16x32_bf16 v[120:123], v[120:123], v[2:5], v[128:131]
	s_nop 2
	ds_read_b128 v[128:131], v228 offset:34816
	s_waitcnt lgkmcnt(1)
	v_mfma_f32_16x16x32_bf16 v[136:139], v[168:171], v[2:5], v[136:139]
	ds_read_b128 v[168:171], v228 offset:39168
	s_waitcnt lgkmcnt(1)
; #define MFMA16(b, a, c) __builtin_amdgcn_mfma_f32_16x16x32_bf16((b), (a), (c), 0, 0, 0)
; __device__ __forceinline__ void mlstm_D(LAS unsigned char* lds, int c, int h, const bf16_t* Z, const float* gi, const float* bcum, const float* marr, const bf16_t* CST, const float* NST,
;                                         const float* hgain, bf16_t* YCAT) {
;     ...
; #pragma unroll
;         for (int ks = 0; ks < 4; ++ks)
;             { const bf16x8 aqh = *(const bf16x8*)(Z + trow * EVN + 1024 + h * DH + 32 * (half * 4 + ks) + 8 * fq);
; #pragma unroll
;               for (int j = 0; j < 16; ++j) acc[j] = MFMA16(row_frag(X, (128 + 8) * 2, 16 * j, 32 * ks, lane), aqh, acc[j]);
;               asm volatile("" ::: "memory"); }
	v_mfma_f32_16x16x32_bf16 v[128:131], v[128:131], v[2:5], v[140:143]
	s_nop 2
	ds_read_b128 v[140:143], v228 offset:43520
	s_waitcnt lgkmcnt(1)
	v_mfma_f32_16x16x32_bf16 v[144:147], v[168:171], v[2:5], v[144:147]
	ds_read_b128 v[168:171], v228 offset:47872
	s_waitcnt lgkmcnt(1)
	v_mfma_f32_16x16x32_bf16 v[140:143], v[140:143], v[2:5], v[148:151]
	s_nop 2
	ds_read_b128 v[148:151], v228 offset:52224
	s_waitcnt lgkmcnt(1)
	v_mfma_f32_16x16x32_bf16 v[152:155], v[168:171], v[2:5], v[152:155]
	ds_read_b128 v[168:171], v228 offset:56576
	s_waitcnt lgkmcnt(1)
	v_mfma_f32_16x16x32_bf16 v[148:151], v[148:151], v[2:5], v[156:159]
	s_waitcnt lgkmcnt(0)
	v_mfma_f32_16x16x32_bf16 v[156:159], v[168:171], v[2:5], v[160:163]
	s_nop 2
	ds_read_b128 v[160:163], v228 offset:60928
	ds_read_b128 v[168:171], v228 offset:65280
	v_mfma_f32_16x16x32_bf16 v[30:33], v[172:175], v[2:5], v[30:33]
	global_load_dwordx4 v[172:175], v[90:91], off offset:2368
	s_waitcnt lgkmcnt(1)
	v_mfma_f32_16x16x32_bf16 v[160:163], v[160:163], v[2:5], v[164:167]
	s_nop 2
	ds_read_b128 v[164:167], v228 offset:64
	s_waitcnt lgkmcnt(1)
	v_mfma_f32_16x16x32_bf16 v[2:5], v[168:171], v[2:5], v[6:9]
	s_nop 2
	ds_read_b128 v[6:9], v228 offset:4416
	s_waitcnt vmcnt(0) lgkmcnt(1)
	v_mfma_f32_16x16x32_bf16 v[10:13], v[164:167], v[172:175], v[10:13]
	ds_read_b128 v[164:167], v228 offset:8768
	s_waitcnt lgkmcnt(1)
	v_mfma_f32_16x16x32_bf16 v[6:9], v[6:9], v[172:175], v[30:33]
	s_nop 2
	ds_read_b128 v[30:33], v228 offset:13120
	s_waitcnt lgkmcnt(1)
	v_mfma_f32_16x16x32_bf16 v[14:17], v[164:167], v[172:175], v[14:17]
	ds_read_b128 v[164:167], v228 offset:17472
	s_waitcnt lgkmcnt(1)
	v_mfma_f32_16x16x32_bf16 v[30:33], v[30:33], v[172:175], v[60:63]
	s_nop 2
	ds_read_b128 v[60:63], v228 offset:21824
	s_waitcnt lgkmcnt(1)
	v_mfma_f32_16x16x32_bf16 v[34:37], v[164:167], v[172:175], v[34:37]
	ds_read_b128 v[164:167], v228 offset:26176
	s_waitcnt lgkmcnt(1)
	v_mfma_f32_16x16x32_bf16 v[60:63], v[60:63], v[172:175], v[124:127]
	s_nop 2
	ds_read_b128 v[124:127], v228 offset:30528
	s_waitcnt lgkmcnt(1)
	v_mfma_f32_16x16x32_bf16 v[120:123], v[164:167], v[172:175], v[120:123]
	ds_read_b128 v[164:167], v228 offset:34880
	s_waitcnt lgkmcnt(1)
	v_mfma_f32_16x16x32_bf16 v[124:127], v[124:127], v[172:175], v[136:139]
	s_nop 2
	ds_read_b128 v[136:139], v228 offset:39232
	s_waitcnt lgkmcnt(1)
	v_mfma_f32_16x16x32_bf16 v[128:131], v[164:167], v[172:175], v[128:131]
	ds_read_b128 v[164:167], v228 offset:43584
	s_waitcnt lgkmcnt(1)
	v_mfma_f32_16x16x32_bf16 v[136:139], v[136:139], v[172:175], v[144:147]
	s_nop 2
	ds_read_b128 v[144:147], v228 offset:47936
	s_waitcnt lgkmcnt(1)
	v_mfma_f32_16x16x32_bf16 v[140:143], v[164:167], v[172:175], v[140:143]
	ds_read_b128 v[164:167], v228 offset:52288
	s_waitcnt lgkmcnt(1)
	v_mfma_f32_16x16x32_bf16 v[144:147], v[144:147], v[172:175], v[152:155]
	s_nop 2
	ds_read_b128 v[152:155], v228 offset:56640
	s_waitcnt lgkmcnt(1)
	v_mfma_f32_16x16x32_bf16 v[148:151], v[164:167], v[172:175], v[148:151]
	ds_read_b128 v[164:167], v228 offset:60992
	ds_read_b128 v[168:171], v228 offset:65344
	s_waitcnt lgkmcnt(2)
	v_mfma_f32_16x16x32_bf16 v[152:155], v[152:155], v[172:175], v[156:159]
	s_nop 2
	global_load_dwordx4 v[156:159], v[90:91], off offset:2432
	ds_read_b128 v[176:179], v228 offset:128
	ds_read_b128 v[180:183], v228 offset:4480
	s_waitcnt lgkmcnt(3)
	v_mfma_f32_16x16x32_bf16 v[160:163], v[164:167], v[172:175], v[160:163]
	ds_read_b128 v[164:167], v228 offset:8832
	ds_read_b128 v[184:187], v228 offset:13184
	ds_read_b128 v[188:191], v228 offset:17536
	ds_read_b128 v[192:195], v228 offset:21888
	s_waitcnt lgkmcnt(6)
	v_mfma_f32_16x16x32_bf16 v[168:171], v[168:171], v[172:175], v[2:5]
	ds_read_b128 v[172:175], v228 offset:26240
	ds_read_b128 v[196:199], v228 offset:30592
	ds_read_b128 v[200:203], v228 offset:34944
	ds_read_b128 v[204:207], v228 offset:39296
	s_waitcnt vmcnt(0) lgkmcnt(9)
	v_mfma_f32_16x16x32_bf16 v[176:179], v[176:179], v[156:159], v[10:13]
	s_nop 2
	ds_read_b128 v[10:13], v228 offset:43648
	ds_read_b128 v[208:211], v228 offset:48000
	ds_read_b128 v[212:215], v228 offset:52352
	ds_read_b128 v[216:219], v228 offset:56704
	ds_read_b128 v[220:223], v228 offset:61056
	ds_read_b128 v[224:227], v228 offset:65408
	global_load_dwordx4 v[2:5], v[90:91], off offset:2496
	s_waitcnt lgkmcnt(14)
	v_mfma_f32_16x16x32_bf16 v[180:183], v[180:183], v[156:159], v[6:9]
	v_mad_i64_i32 v[90:91], s[2:3], v100, s68, 0
	s_nop 1
	v_add_f32_e32 v6, 0, v39
	v_add_f32_e32 v6, v6, v38
	v_add_f32_e32 v6, v6, v41
	v_add_f32_e32 v6, v6, v40
	v_add_f32_e32 v6, v6, v43
	v_add_f32_e32 v6, v6, v42
	s_waitcnt lgkmcnt(13)
	v_mfma_f32_16x16x32_bf16 v[164:167], v[164:167], v[156:159], v[14:17]
	s_nop 2
	v_add_f32_e32 v14, v6, v27
	s_waitcnt lgkmcnt(5)
	v_mfma_f32_16x16x32_bf16 v[6:9], v[10:13], v[156:159], v[140:143]
	v_add_f32_e32 v10, v14, v26
	v_add_f32_e32 v10, v10, v29
	v_add_f32_e32 v14, v10, v28
	v_add_f32_e32 v14, v14, v23
	v_add_f32_e32 v14, v14, v22
	v_add_f32_e32 v20, v14, v25
	v_add_f32_e32 v20, v20, v24
	v_add_f32_e32 v19, v20, v19
	v_add_f32_e32 v22, v19, v18
	v_add_f32_e32 v22, v22, v45
	v_add_f32_e32 v26, v22, v44
	v_add_f32_e32 v26, v26, v47
	v_add_f32_e32 v46, v26, v46
	v_add_f32_e32 v46, v46, v49
	v_add_f32_e32 v135, v46, v48
	v_add_f32_e32 v51, v135, v51
	v_add_f32_e32 v50, v51, v50
	v_add_f32_e32 v50, v50, v56
	v_add_f32_e32 v50, v50, v54
	s_waitcnt lgkmcnt(4)
	v_mfma_f32_16x16x32_bf16 v[10:13], v[208:211], v[156:159], v[144:147]
	ds_read_b128 v[42:45], v228 offset:192
	ds_read_b128 v[46:49], v228 offset:8896
	ds_read_b128 v[140:143], v228 offset:13248
	s_waitcnt lgkmcnt(6)
; #define MFMA16(b, a, c) __builtin_amdgcn_mfma_f32_16x16x32_bf16((b), (a), (c), 0, 0, 0)
; __device__ __forceinline__ void mlstm_D(LAS unsigned char* lds, int c, int h, const bf16_t* Z, const float* gi, const float* bcum, const float* marr, const bf16_t* CST, const float* NST,
;                                         const float* hgain, bf16_t* YCAT) {
;     ...
; #pragma unroll
;         for (int ks = 0; ks < 4; ++ks)
;             { const bf16x8 aqh = *(const bf16x8*)(Z + trow * EVN + 1024 + h * DH + 32 * (half * 4 + ks) + 8 * fq);
; #pragma unroll
;               for (int j = 0; j < 16; ++j) acc[j] = MFMA16(row_frag(X, (128 + 8) * 2, 16 * j, 32 * ks, lane), aqh, acc[j]);
;               asm volatile("" ::: "memory"); }
;     }
; #pragma unroll
;     for (int j = 0; j < 16; ++j) acc[j] = acc[j] * wi;
;     __syncthreads();
;     stage_tile<CH, DH, 16>(X, Z + (size_t)t0 * EVN + 3072 + h * DH, EVN, tid);
;     __syncthreads();
;     ...
;     const float mt = bcum[trow * 4 + h] + Mt; const float inv = 1.0f / fmaxf(fabsf(den), expf(-mt));
;     float ss = 0.f;
; #pragma unroll
;     for (int j = 0; j < 16; ++j) { acc[j] = acc[j] * inv; ss += (acc[j][0] * acc[j][0] + acc[j][1] * acc[j][1]) + (acc[j][2] * acc[j][2] + acc[j][3] * acc[j][3]); }
;     ss += __shfl_xor(ss, 16); ss += __shfl_xor(ss, 32);
;     const float rs = rsqrtf(ss * (1.0f / DH) + EPS);
; #pragma unroll
;     for (int j = 0; j < 16; j += 2) { u32x2 ab[2];
; #pragma unroll
;         for (int n = 0; n < 2; ++n) { const int col = h * DH + 16 * (j + n) + 4 * fq;
;             const f32x4 gn = *(const f32x4*)(hgain + col); const u32x2 ov = *(const u32x2*)(Z + trow * EVN + 4096 + col);
	v_mfma_f32_16x16x32_bf16 v[14:17], v[212:215], v[156:159], v[148:151]
	ds_read_b128 v[144:147], v228 offset:17600
	v_add_f32_e32 v50, v50, v58
	v_add_f32_e32 v50, v50, v57
	ds_read_b128 v[148:151], v228 offset:21952
	v_mfma_f32_16x16x32_bf16 v[184:187], v[184:187], v[156:159], v[30:33]
	v_add_f32_e32 v50, v50, v59
	v_sub_f32_e32 v51, v95, v116
	v_mul_f32_e32 v54, 0x3fb8aa3b, v51
	v_mfma_f32_16x16x32_bf16 v[188:191], v[188:191], v[156:159], v[34:37]
	v_mad_i64_i32 v[32:33], s[2:3], v105, s68, 0
	v_mad_i64_i32 v[30:31], s[2:3], v106, s68, 0
	v_mfma_f32_16x16x32_bf16 v[60:63], v[192:195], v[156:159], v[60:63]
	v_mad_i64_i32 v[192:193], s[2:3], v102, s68, 0
	v_mad_i64_i32 v[36:37], s[2:3], v103, s68, 0
	v_mad_i64_i32 v[34:35], s[2:3], v104, s68, 0
	v_mfma_f32_16x16x32_bf16 v[120:123], v[172:175], v[156:159], v[120:123]
	s_lshl_b32 s2, s5, 1
	s_add_u32 s3, s37, s2
	s_addc_u32 s7, s66, 0
	v_mfma_f32_16x16x32_bf16 v[124:127], v[196:199], v[156:159], v[124:127]
	s_add_u32 s6, s3, 0x1800
	s_addc_u32 s7, s7, 0
	v_lshl_add_u64 v[36:37], s[6:7], 0, v[36:37]
	v_mfma_f32_16x16x32_bf16 v[128:131], v[200:203], v[156:159], v[128:131]
	v_lshl_add_u64 v[36:37], v[82:83], 1, v[36:37]
	v_lshl_add_u64 v[34:35], s[6:7], 0, v[34:35]
	v_lshl_add_u64 v[34:35], v[84:85], 1, v[34:35]
	v_mfma_f32_16x16x32_bf16 v[38:41], v[204:207], v[156:159], v[136:139]
	v_lshl_add_u64 v[32:33], s[6:7], 0, v[32:33]
	v_lshl_add_u64 v[32:33], v[86:87], 1, v[32:33]
	v_lshl_add_u64 v[30:31], s[6:7], 0, v[30:31]
	s_waitcnt lgkmcnt(7)
	v_mfma_f32_16x16x32_bf16 v[18:21], v[216:219], v[156:159], v[152:155]
	ds_read_b128 v[136:139], v228 offset:4544
	v_lshl_add_u64 v[30:31], v[88:89], 1, v[30:31]
	v_cmp_ngt_f32_e32 vcc, s71, v51
	s_waitcnt lgkmcnt(7)
	v_mfma_f32_16x16x32_bf16 v[22:25], v[220:223], v[156:159], v[160:163]
	s_mov_b32 s3, 4
	s_waitcnt lgkmcnt(6)
	v_mfma_f32_16x16x32_bf16 v[26:29], v[224:227], v[156:159], v[168:171]
	ds_read_b128 v[56:59], v228 offset:26304
	ds_read_b128 v[152:155], v228 offset:30656
	ds_read_b128 v[156:159], v228 offset:35008
	ds_read_b128 v[160:163], v228 offset:39360
	s_waitcnt vmcnt(0) lgkmcnt(2)
	v_mfma_f32_16x16x32_bf16 v[124:127], v[152:155], v[2:5], v[124:127]
	s_waitcnt lgkmcnt(0)
	v_mfma_f32_16x16x32_bf16 v[152:155], v[160:163], v[2:5], v[38:41]
	s_nop 2
	v_lshl_add_u64 v[38:39], s[6:7], 0, v[64:65]
	v_lshl_add_u64 v[38:39], v[74:75], 1, v[38:39]
	v_mfma_f32_16x16x32_bf16 v[42:45], v[42:45], v[2:5], v[176:179]
	v_mfma_f32_16x16x32_bf16 v[46:49], v[46:49], v[2:5], v[164:167]
	v_mfma_f32_16x16x32_bf16 v[148:151], v[148:151], v[2:5], v[60:63]
	s_nop 2
	ds_read_b128 v[60:63], v228 offset:43712
	ds_read_b128 v[164:167], v228 offset:48064
	ds_read_b128 v[168:171], v228 offset:52416
	ds_read_b128 v[172:175], v228 offset:56768
	v_mfma_f32_16x16x32_bf16 v[120:123], v[56:59], v[2:5], v[120:123]
	ds_read_b128 v[56:59], v228 offset:61120
	ds_read_b128 v[176:179], v228 offset:65472
	v_or_b32_e32 v230, s5, v117
	v_lshlrev_b32_e32 v230, 1, v230
	v_mov_b32_e32 v231, 0
	v_lshl_add_u64 v[232:233], v[72:73], 0, s[44:45]
	v_lshlrev_b32_e32 v236, 4, v70
	v_mov_b32_e32 v237, s36
	v_lshl_add_u64 v[232:233], v[232:233], 0, v[230:231]
	v_lshl_add_u32 v236, v237, 2, v236
	global_load_dwordx2 v[194:195], v[232:233], off
	global_load_dwordx2 v[196:197], v[232:233], off offset:32
	global_load_dwordx2 v[198:199], v[232:233], off offset:64
	global_load_dwordx2 v[200:201], v[232:233], off offset:96
	global_load_dwordx2 v[202:203], v[232:233], off offset:128
	global_load_dwordx2 v[204:205], v[232:233], off offset:160
	global_load_dwordx2 v[206:207], v[232:233], off offset:192
	global_load_dwordx2 v[208:209], v[232:233], off offset:224
	global_load_dwordx2 v[210:211], v[232:233], off offset:256
	global_load_dwordx2 v[212:213], v[232:233], off offset:288
	global_load_dwordx2 v[214:215], v[232:233], off offset:320
	global_load_dwordx2 v[216:217], v[232:233], off offset:352
	global_load_dwordx2 v[218:219], v[232:233], off offset:384
	global_load_dwordx2 v[220:221], v[232:233], off offset:416
	global_load_dwordx2 v[222:223], v[232:233], off offset:448
	global_load_dwordx2 v[224:225], v[232:233], off offset:480
	global_load_dword v226, v236, s[34:35]
	s_waitcnt lgkmcnt(0)
	s_barrier
	v_mfma_f32_16x16x32_bf16 v[128:131], v[156:159], v[2:5], v[128:131]
	global_load_dwordx4 v[156:159], v[38:39], off
	v_lshl_add_u64 v[38:39], s[6:7], 0, v[90:91]
	v_lshl_add_u64 v[38:39], v[76:77], 1, v[38:39]
	global_load_dwordx4 v[160:163], v[38:39], off
	v_lshl_add_u64 v[38:39], s[6:7], 0, v[132:133]
	v_lshl_add_u64 v[38:39], v[78:79], 1, v[38:39]
	v_mfma_f32_16x16x32_bf16 v[136:139], v[136:139], v[2:5], v[180:183]
	global_load_dwordx4 v[82:85], v[34:35], off
	global_load_dwordx4 v[86:89], v[30:31], off
	v_mul_lo_u32 v77, v93, s75
	global_load_dwordx4 v[180:183], v[38:39], off
	v_lshl_add_u64 v[38:39], s[6:7], 0, v[192:193]
	v_lshl_add_u64 v[38:39], v[80:81], 1, v[38:39]
	global_load_dwordx4 v[78:81], v[38:39], off
	v_mfma_f32_16x16x32_bf16 v[140:143], v[140:143], v[2:5], v[184:187]
	v_add3_u32 v77, s51, v77, v107
	v_fma_f32 v30, v51, s70, -v54
	v_rndne_f32_e32 v31, v54
	global_load_dwordx4 v[184:187], v[36:37], off
	v_mfma_f32_16x16x32_bf16 v[144:147], v[144:147], v[2:5], v[188:191]
	v_fmac_f32_e32 v30, 0x32a5705f, v51
	s_waitcnt vmcnt(6)
	ds_write_b128 v77, v[156:159]
	global_load_dwordx4 v[188:191], v[32:33], off
	v_mul_lo_u32 v77, v100, s75
	v_add3_u32 v77, s51, v77, v108
	s_waitcnt vmcnt(6)
	ds_write_b128 v77, v[160:163]
	v_mul_lo_u32 v77, v101, s75
	v_add3_u32 v77, s51, v77, v109
	v_sub_f32_e32 v32, v54, v31
	v_add_f32_e32 v30, v32, v30
	v_exp_f32_e32 v30, v30
	s_waitcnt vmcnt(3)
; #define LAS __attribute__((address_space(3)))
; #define MFMA16(b, a, c) __builtin_amdgcn_mfma_f32_16x16x32_bf16((b), (a), (c), 0, 0, 0)
; __device__ __forceinline__ void mlstm_D(LAS unsigned char* lds, int c, int h, const bf16_t* Z, const float* gi, const float* bcum, const float* marr, const bf16_t* CST, const float* NST,
;                                         const float* hgain, bf16_t* YCAT) {
;     ...
;     for (int j = 0; j < 16; ++j) acc[j] = acc[j] * wi;
;     __syncthreads();
;     stage_tile<CH, DH, 16>(X, Z + (size_t)t0 * EVN + 3072 + h * DH, EVN, tid);
;     __syncthreads();
; #pragma unroll 1
;     for (int ks = 0; ks < 4; ++ks) { const bf16x8 ap = *(const LAS bf16x8*)(Pw + fr * PRS + (32 * ks + 8 * fq) * 2);
; #pragma unroll
;         for (int j = 0; j < 16; ++j) acc[j] = MFMA16(tr_frag(X, (DH + 16) * 2, 32 * ks, 16 * j, lane), ap, acc[j]); }
	ds_write_b128 v77, v[180:183]
	v_mul_lo_u32 v77, v102, s75
	v_add3_u32 v77, s51, v77, v110
	s_waitcnt vmcnt(2)
	ds_write_b128 v77, v[78:81]
	v_mul_lo_u32 v77, v103, s75
	v_add3_u32 v77, s51, v77, v111
	v_cvt_i32_f32_e32 v31, v31
	v_add_f32_e32 v32, v50, v52
	s_waitcnt vmcnt(1)
	ds_write_b128 v77, v[184:187]
	v_mul_lo_u32 v77, v104, s75
	v_add3_u32 v77, s51, v77, v112
	ds_write_b128 v77, v[82:85]
	v_mul_lo_u32 v77, v105, s75
	v_add_f32_e32 v32, v32, v55
	v_add3_u32 v77, s51, v77, v113
	v_add_f32_e32 v75, v32, v53
	v_mfma_f32_16x16x32_bf16 v[6:9], v[60:63], v[2:5], v[6:9]
	v_ldexp_f32 v30, v30, v31
	ds_bpermute_b32 v76, v98, v75
	v_cndmask_b32_e32 v30, 0, v30, vcc
	v_mfma_f32_16x16x32_bf16 v[10:13], v[164:167], v[2:5], v[10:13]
	v_cmp_nlt_f32_e32 vcc, s72, v51
	v_lshlrev_b32_e32 v78, 3, v119
	v_add_u32_e32 v79, s4, v118
	v_mfma_f32_16x16x32_bf16 v[14:17], v[168:171], v[2:5], v[14:17]
	v_add3_u32 v66, v79, v66, s53
	s_waitcnt vmcnt(0)
	ds_write_b128 v77, v[188:191]
	v_mul_lo_u32 v77, v106, s75
	v_mfma_f32_16x16x32_bf16 v[164:167], v[172:175], v[2:5], v[18:21]
	v_add3_u32 v77, s51, v77, v114
	ds_write_b128 v77, v[86:89]
	v_bfe_u32 v77, v99, 2, 2
	v_mfma_f32_16x16x32_bf16 v[168:171], v[56:59], v[2:5], v[22:25]
	v_cndmask_b32_e32 v18, v97, v30, vcc
	v_mul_u32_u24_e32 v77, 0x220, v77
	v_mul_f32_e32 v74, 0x3d800000, v18
	v_mfma_f32_16x16x32_bf16 v[2:5], v[176:179], v[2:5], v[26:29]
	v_mad_u32_u24 v77, v134, s73, v77
	v_pk_mul_f32 v[64:65], v[74:75], v[44:45] op_sel_hi:[0,1]
	v_pk_mul_f32 v[62:63], v[74:75], v[42:43] op_sel_hi:[0,1]
	v_pk_mul_f32 v[60:61], v[74:75], v[138:139] op_sel_hi:[0,1]
	v_pk_mul_f32 v[58:59], v[74:75], v[136:137] op_sel_hi:[0,1]
	v_pk_mul_f32 v[56:57], v[74:75], v[48:49] op_sel_hi:[0,1]
	v_pk_mul_f32 v[54:55], v[74:75], v[46:47] op_sel_hi:[0,1]
	v_pk_mul_f32 v[52:53], v[74:75], v[142:143] op_sel_hi:[0,1]
	v_pk_mul_f32 v[50:51], v[74:75], v[140:141] op_sel_hi:[0,1]
	v_pk_mul_f32 v[48:49], v[74:75], v[146:147] op_sel_hi:[0,1]
	v_pk_mul_f32 v[46:47], v[74:75], v[144:145] op_sel_hi:[0,1]
	v_pk_mul_f32 v[44:45], v[74:75], v[150:151] op_sel_hi:[0,1]
	v_pk_mul_f32 v[42:43], v[74:75], v[148:149] op_sel_hi:[0,1]
	v_pk_mul_f32 v[40:41], v[74:75], v[122:123] op_sel_hi:[0,1]
	v_pk_mul_f32 v[38:39], v[74:75], v[120:121] op_sel_hi:[0,1]
	v_pk_mul_f32 v[36:37], v[74:75], v[126:127] op_sel_hi:[0,1]
	v_pk_mul_f32 v[34:35], v[74:75], v[124:125] op_sel_hi:[0,1]
	v_pk_mul_f32 v[32:33], v[74:75], v[130:131] op_sel_hi:[0,1]
	v_pk_mul_f32 v[30:31], v[74:75], v[128:129] op_sel_hi:[0,1]
	v_pk_mul_f32 v[28:29], v[74:75], v[154:155] op_sel_hi:[0,1]
	v_pk_mul_f32 v[26:27], v[74:75], v[152:153] op_sel_hi:[0,1]
	v_pk_mul_f32 v[24:25], v[74:75], v[8:9] op_sel_hi:[0,1]
	v_pk_mul_f32 v[22:23], v[74:75], v[6:7] op_sel_hi:[0,1]
	v_pk_mul_f32 v[20:21], v[74:75], v[12:13] op_sel_hi:[0,1]
	v_pk_mul_f32 v[18:19], v[74:75], v[10:11] op_sel_hi:[0,1]
	v_pk_mul_f32 v[16:17], v[74:75], v[16:17] op_sel_hi:[0,1]
	v_pk_mul_f32 v[14:15], v[74:75], v[14:15] op_sel_hi:[0,1]
	v_pk_mul_f32 v[12:13], v[74:75], v[166:167] op_sel_hi:[0,1]
	v_pk_mul_f32 v[10:11], v[74:75], v[164:165] op_sel_hi:[0,1]
	v_pk_mul_f32 v[8:9], v[74:75], v[170:171] op_sel_hi:[0,1]
	v_pk_mul_f32 v[6:7], v[74:75], v[168:169] op_sel_hi:[0,1]
	v_pk_mul_f32 v[4:5], v[74:75], v[4:5] op_sel_hi:[0,1]
	v_pk_mul_f32 v[2:3], v[74:75], v[2:3] op_sel_hi:[0,1]
	v_and_or_b32 v77, v78, 24, v77
	s_waitcnt lgkmcnt(0)
	s_barrier
.LBB0_770:
	v_add_u32_e32 v82, s51, v66
	v_add_u32_e32 v90, s51, v77
	ds_read_b64_tr_b16 v[80:81], v90 offset:2176
	ds_read_b64_tr_b16 v[78:79], v90
	ds_read_b128 v[82:85], v82
	ds_read_b64_tr_b16 v[86:87], v90 offset:32
	ds_read_b64_tr_b16 v[88:89], v90 offset:2208
	ds_read_b64_tr_b16 v[102:103], v90 offset:2240
	ds_read_b64_tr_b16 v[100:101], v90 offset:64
	ds_read_b64_tr_b16 v[104:105], v90 offset:96
	ds_read_b64_tr_b16 v[108:109], v90 offset:480
	s_waitcnt lgkmcnt(6)
	v_mfma_f32_16x16x32_bf16 v[62:65], v[78:81], v[82:85], v[62:65]
	ds_read_b64_tr_b16 v[78:79], v90 offset:128
	ds_read_b64_tr_b16 v[106:107], v90 offset:2272
	ds_read_b64_tr_b16 v[80:81], v90 offset:2304
	s_add_i32 s3, s3, -1
	v_add_u32_e32 v66, 64, v66
	s_waitcnt lgkmcnt(7)
	v_mfma_f32_16x16x32_bf16 v[58:61], v[86:89], v[82:85], v[58:61]
	ds_read_b64_tr_b16 v[86:87], v90 offset:160
	ds_read_b64_tr_b16 v[88:89], v90 offset:2336
	s_cmp_lg_u32 s3, 0
	v_add_u32_e32 v77, 0x4400, v77
	s_waitcnt lgkmcnt(7)
	v_mfma_f32_16x16x32_bf16 v[54:57], v[100:103], v[82:85], v[54:57]
	s_waitcnt lgkmcnt(3)
	v_mfma_f32_16x16x32_bf16 v[50:53], v[104:107], v[82:85], v[50:53]
	ds_read_b64_tr_b16 v[102:103], v90 offset:2368
	ds_read_b64_tr_b16 v[100:101], v90 offset:192
	ds_read_b64_tr_b16 v[104:105], v90 offset:224
	s_waitcnt lgkmcnt(5)
	v_mfma_f32_16x16x32_bf16 v[46:49], v[78:81], v[82:85], v[46:49]
	ds_read_b64_tr_b16 v[78:79], v90 offset:256
	ds_read_b64_tr_b16 v[106:107], v90 offset:2400
	ds_read_b64_tr_b16 v[80:81], v90 offset:2432
	s_waitcnt lgkmcnt(6)
	v_mfma_f32_16x16x32_bf16 v[42:45], v[86:89], v[82:85], v[42:45]
	ds_read_b64_tr_b16 v[86:87], v90 offset:288
	ds_read_b64_tr_b16 v[88:89], v90 offset:2464
	s_waitcnt lgkmcnt(6)
	v_mfma_f32_16x16x32_bf16 v[38:41], v[100:103], v[82:85], v[38:41]
	s_waitcnt lgkmcnt(3)
	v_mfma_f32_16x16x32_bf16 v[34:37], v[104:107], v[82:85], v[34:37]
	ds_read_b64_tr_b16 v[102:103], v90 offset:2496
	ds_read_b64_tr_b16 v[100:101], v90 offset:320
	ds_read_b64_tr_b16 v[104:105], v90 offset:352
	s_waitcnt lgkmcnt(5)
	v_mfma_f32_16x16x32_bf16 v[30:33], v[78:81], v[82:85], v[30:33]
	ds_read_b64_tr_b16 v[78:79], v90 offset:384
	ds_read_b64_tr_b16 v[106:107], v90 offset:2528
	ds_read_b64_tr_b16 v[80:81], v90 offset:2560
	s_waitcnt lgkmcnt(6)
	v_mfma_f32_16x16x32_bf16 v[26:29], v[86:89], v[82:85], v[26:29]
	ds_read_b64_tr_b16 v[88:89], v90 offset:2592
	s_waitcnt lgkmcnt(5)
	v_mfma_f32_16x16x32_bf16 v[22:25], v[100:103], v[82:85], v[22:25]
	ds_read_b64_tr_b16 v[86:87], v90 offset:416
	ds_read_b64_tr_b16 v[100:101], v90 offset:448
	ds_read_b64_tr_b16 v[102:103], v90 offset:2624
	ds_read_b64_tr_b16 v[110:111], v90 offset:2656
	s_waitcnt lgkmcnt(6)
	v_mfma_f32_16x16x32_bf16 v[18:21], v[104:107], v[82:85], v[18:21]
	s_waitcnt lgkmcnt(5)
	v_mfma_f32_16x16x32_bf16 v[14:17], v[78:81], v[82:85], v[14:17]
	s_waitcnt lgkmcnt(3)
	v_mfma_f32_16x16x32_bf16 v[10:13], v[86:89], v[82:85], v[10:13]
	s_waitcnt lgkmcnt(1)
	v_mfma_f32_16x16x32_bf16 v[6:9], v[100:103], v[82:85], v[6:9]
	s_waitcnt lgkmcnt(0)
	v_mfma_f32_16x16x32_bf16 v[2:5], v[108:111], v[82:85], v[2:5]
	s_cbranch_scc1 .LBB0_770
; __device__ __forceinline__ void mlstm_D(LAS unsigned char* lds, int c, int h, const bf16_t* Z, const float* gi, const float* bcum, const float* marr, const bf16_t* CST, const float* NST,
;                                         const float* hgain, bf16_t* YCAT) {
;     ...
;     const float mt = bcum[trow * 4 + h] + Mt; const float inv = 1.0f / fmaxf(fabsf(den), expf(-mt));
;     float ss = 0.f;
; #pragma unroll
;     for (int j = 0; j < 16; ++j) { acc[j] = acc[j] * inv; ss += (acc[j][0] * acc[j][0] + acc[j][1] * acc[j][1]) + (acc[j][2] * acc[j][2] + acc[j][3] * acc[j][3]); }
;     ss += __shfl_xor(ss, 16); ss += __shfl_xor(ss, 32);
;     const float rs = rsqrtf(ss * (1.0f / DH) + EPS);
; #pragma unroll
;     for (int j = 0; j < 16; j += 2) { u32x2 ab[2];
; #pragma unroll
;         for (int n = 0; n < 2; ++n) { const int col = h * DH + 16 * (j + n) + 4 * fq;
;             const f32x4 gn = *(const f32x4*)(hgain + col); const u32x2 ov = *(const u32x2*)(Z + trow * EVN + 4096 + col);
	v_lshl_add_u64 v[78:79], v[70:71], 4, s[34:35]
	s_lshl_b32 s24, s36, 2
	v_lshl_add_u64 v[78:79], v[78:79], 0, s[24:25]
	s_nop 0
	v_add_f32_e32 v93, v75, v76
	ds_bpermute_b32 v95, v115, v93
	v_lshlrev_b64 v[70:71], 12, v[70:71]
	s_mov_b32 s3, s25
	v_lshl_add_u64 v[70:71], s[26:27], 0, v[70:71]
	v_lshl_add_u64 v[70:71], v[70:71], 0, s[2:3]
	v_and_b32_e32 v66, 8, v117
	v_or_b32_e32 v75, s5, v117
	v_lshlrev_b32_e32 v66, 1, v66
	v_lshl_add_u64 v[72:73], v[72:73], 0, s[44:45]
	v_lshl_add_u64 v[70:71], v[70:71], 0, v[66:67]
	v_lshlrev_b32_e32 v66, 1, v75
	s_add_i32 s22, s22, s52
	s_cmpk_gt_i32 s22, 0xff
	v_or_b32_e32 v118, s5, v117
	v_lshlrev_b32_e32 v118, 2, v118
	s_waitcnt vmcnt(0)
	global_load_dwordx4 v[120:123], v118, s[28:29]
	global_load_dwordx4 v[124:127], v118, s[28:29] offset:64
	global_load_dwordx4 v[128:131], v118, s[28:29] offset:128
	global_load_dwordx4 v[132:135], v118, s[28:29] offset:192
	global_load_dwordx4 v[136:139], v118, s[28:29] offset:256
	global_load_dwordx4 v[140:143], v118, s[28:29] offset:320
	global_load_dwordx4 v[144:147], v118, s[28:29] offset:384
	global_load_dwordx4 v[148:151], v118, s[28:29] offset:448
	global_load_dwordx4 v[152:155], v118, s[28:29] offset:512
	global_load_dwordx4 v[156:159], v118, s[28:29] offset:576
	global_load_dwordx4 v[160:163], v118, s[28:29] offset:640
	global_load_dwordx4 v[164:167], v118, s[28:29] offset:704
	global_load_dwordx4 v[168:171], v118, s[28:29] offset:768
	global_load_dwordx4 v[172:175], v118, s[28:29] offset:832
	global_load_dwordx4 v[176:179], v118, s[28:29] offset:896
	global_load_dwordx4 v[180:183], v118, s[28:29] offset:960
	v_mov_b32_e32 v77, v226
	v_add_f32_e32 v80, v116, v77
	v_mul_f32_e32 v76, 0xbfb8aa3b, v80
	v_fma_f32 v77, v80, s76, -v76
	v_rndne_f32_e32 v78, v76
	v_fmac_f32_e32 v77, 0xb2a5705f, v80
	v_sub_f32_e32 v76, v76, v78
	v_add_f32_e32 v76, v76, v77
	v_cvt_i32_f32_e32 v81, v78
	v_exp_f32_e32 v82, v76
	s_waitcnt lgkmcnt(0)
	v_pk_add_f32 v[78:79], v[92:93], v[94:95]
	v_cmp_nlt_f32_e32 vcc, s77, v80
	v_fmac_f32_e32 v79, v78, v74
	v_ldexp_f32 v74, v82, v81
	v_cndmask_b32_e32 v74, 0, v74, vcc
	v_cmp_ngt_f32_e32 vcc, s78, v80
	v_lshl_add_u64 v[76:77], v[72:73], 0, v[66:67]
	v_mov_b32_e32 v80, v194
	v_mov_b32_e32 v81, v195
	v_cndmask_b32_e32 v74, v97, v74, vcc
	v_max_f32_e64 v74, |v79|, v74
	v_div_scale_f32 v78, s[2:3], v74, v74, 1.0
	v_rcp_f32_e32 v79, v78
	v_div_scale_f32 v76, vcc, 1.0, v74, 1.0
	v_fma_f32 v77, -v78, v79, 1.0
	v_fmac_f32_e32 v79, v77, v79
	v_mul_f32_e32 v77, v76, v79
	v_fma_f32 v82, -v78, v77, v76
	v_fmac_f32_e32 v77, v82, v79
	v_fma_f32 v76, -v78, v77, v76
	v_div_fmas_f32 v76, v76, v79, v77
	v_div_fixup_f32 v74, v76, v74, 1.0
	v_pk_mul_f32 v[64:65], v[64:65], v[74:75] op_sel_hi:[1,0]
	v_pk_mul_f32 v[82:83], v[62:63], v[74:75] op_sel_hi:[1,0]
	v_pk_mul_f32 v[60:61], v[60:61], v[74:75] op_sel_hi:[1,0]
	v_pk_mul_f32 v[62:63], v[58:59], v[74:75] op_sel_hi:[1,0]
	v_pk_mul_f32 v[58:59], v[54:55], v[74:75] op_sel_hi:[1,0]
	v_pk_mul_f32 v[54:55], v[50:51], v[74:75] op_sel_hi:[1,0]
	v_pk_mul_f32 v[50:51], v[46:47], v[74:75] op_sel_hi:[1,0]
	v_pk_mul_f32 v[46:47], v[42:43], v[74:75] op_sel_hi:[1,0]
	v_pk_mul_f32 v[42:43], v[38:39], v[74:75] op_sel_hi:[1,0]
	v_pk_mul_f32 v[38:39], v[34:35], v[74:75] op_sel_hi:[1,0]
	v_pk_mul_f32 v[34:35], v[30:31], v[74:75] op_sel_hi:[1,0]
	v_pk_mul_f32 v[30:31], v[26:27], v[74:75] op_sel_hi:[1,0]
	v_pk_mul_f32 v[26:27], v[64:65], v[64:65]
	v_pk_mul_f32 v[76:77], v[82:83], v[82:83]
	v_pk_mul_f32 v[78:79], v[60:61], v[60:61]
	v_pk_mul_f32 v[84:85], v[62:63], v[62:63]
	v_pk_mul_f32 v[56:57], v[56:57], v[74:75] op_sel_hi:[1,0]
	v_pk_mov_b32 v[110:111], v[76:77], v[26:27] op_sel:[1,0]
	v_mov_b32_e32 v77, v27
	v_pk_mov_b32 v[26:27], v[84:85], v[78:79] op_sel:[1,0]
	v_mov_b32_e32 v85, v79
	v_mul_f32_e32 v86, v58, v58
	v_mul_f32_e32 v88, v56, v56
	v_pk_add_f32 v[76:77], v[110:111], v[76:77]
	v_pk_add_f32 v[26:27], v[26:27], v[84:85]
	v_pk_mul_f32 v[52:53], v[52:53], v[74:75] op_sel_hi:[1,0]
	v_pk_mul_f32 v[48:49], v[48:49], v[74:75] op_sel_hi:[1,0]
	v_pk_fma_f32 v[78:79], v[58:59], v[58:59], v[86:87] op_sel_hi:[1,1,0]
	v_pk_fma_f32 v[86:87], v[56:57], v[56:57], v[88:89] op_sel_hi:[1,1,0]
	v_pk_add_f32 v[76:77], v[76:77], v[76:77] op_sel_hi:[0,1]
	v_pk_add_f32 v[26:27], v[26:27], v[26:27] op_sel_hi:[0,1]
	v_pk_mul_f32 v[90:91], v[48:49], v[48:49]
	v_pk_mul_f32 v[92:93], v[50:51], v[50:51]
	v_mul_f32_e32 v78, v54, v54
	v_mul_f32_e32 v86, v55, v55
	v_mul_f32_e32 v76, v52, v52
	v_mul_f32_e32 v26, v53, v53
	v_pk_mul_f32 v[44:45], v[44:45], v[74:75] op_sel_hi:[1,0]
	v_pk_mov_b32 v[88:89], v[92:93], v[90:91] op_sel:[1,0]
	v_mov_b32_e32 v93, v91
	v_pk_add_f32 v[78:79], v[78:79], v[86:87]
	v_pk_add_f32 v[26:27], v[76:77], v[26:27]
	v_mul_f32_e32 v94, v46, v46
	v_mul_f32_e32 v100, v44, v44
	v_pk_add_f32 v[84:85], v[88:89], v[92:93]
	v_pk_add_f32 v[26:27], v[78:79], v[26:27]
	v_pk_mul_f32 v[40:41], v[40:41], v[74:75] op_sel_hi:[1,0]
	v_pk_mul_f32 v[36:37], v[36:37], v[74:75] op_sel_hi:[1,0]
	v_pk_fma_f32 v[90:91], v[46:47], v[46:47], v[94:95] op_sel_hi:[1,1,0]
	v_pk_fma_f32 v[94:95], v[44:45], v[44:45], v[100:101] op_sel_hi:[1,1,0]
	v_pk_add_f32 v[84:85], v[84:85], v[84:85] op_sel_hi:[0,1]
	v_pk_add_f32 v[26:27], v[26:27], v[26:27] op_sel_hi:[0,1]
	v_pk_mul_f32 v[102:103], v[36:37], v[36:37]
	v_pk_mul_f32 v[104:105], v[38:39], v[38:39]
	v_mul_f32_e32 v90, v42, v42
	v_mul_f32_e32 v94, v43, v43
	v_mul_f32_e32 v84, v40, v40
	v_mul_f32_e32 v26, v41, v41
	v_pk_mul_f32 v[32:33], v[32:33], v[74:75] op_sel_hi:[1,0]
	v_pk_mov_b32 v[100:101], v[104:105], v[102:103] op_sel:[1,0]
	v_mov_b32_e32 v105, v103
	v_pk_add_f32 v[86:87], v[90:91], v[94:95]
	v_pk_add_f32 v[26:27], v[84:85], v[26:27]
	v_mul_f32_e32 v106, v34, v34
	v_mul_f32_e32 v108, v32, v32
	v_pk_add_f32 v[88:89], v[100:101], v[104:105]
	v_pk_add_f32 v[26:27], v[86:87], v[26:27]
	v_pk_mul_f32 v[28:29], v[28:29], v[74:75] op_sel_hi:[1,0]
	v_pk_fma_f32 v[102:103], v[34:35], v[34:35], v[106:107] op_sel_hi:[1,1,0]
	v_pk_fma_f32 v[106:107], v[32:33], v[32:33], v[108:109] op_sel_hi:[1,1,0]
	v_pk_add_f32 v[88:89], v[88:89], v[88:89] op_sel_hi:[0,1]
	v_pk_add_f32 v[26:27], v[26:27], v[26:27] op_sel_hi:[0,1]
	v_mul_f32_e32 v102, v30, v30
	v_mul_f32_e32 v106, v31, v31
	v_mul_f32_e32 v88, v28, v28
	v_mul_f32_e32 v26, v29, v29
	v_pk_add_f32 v[76:77], v[102:103], v[106:107]
	v_pk_add_f32 v[26:27], v[88:89], v[26:27]
	v_pk_mul_f32 v[24:25], v[24:25], v[74:75] op_sel_hi:[1,0]
	v_lshlrev_b32_e32 v75, 2, v75
	v_pk_add_f32 v[26:27], v[76:77], v[26:27]
	s_waitcnt vmcnt(15)
; __device__ __forceinline__ unsigned cvt_pk_bf16(float lo, float hi) { unsigned r; asm volatile("v_cvt_pk_bf16_f32 %0, %1, %2" : "=v"(r) : "v"(lo), "v"(hi)); return r; }
; __device__ __forceinline__ void mlstm_D(LAS unsigned char* lds, int c, int h, const bf16_t* Z, const float* gi, const float* bcum, const float* marr, const bf16_t* CST, const float* NST,
;                                         const float* hgain, bf16_t* YCAT) {
;     ...
;     const float mt = bcum[trow * 4 + h] + Mt; const float inv = 1.0f / fmaxf(fabsf(den), expf(-mt));
;     float ss = 0.f;
; #pragma unroll
;     for (int j = 0; j < 16; ++j) { acc[j] = acc[j] * inv; ss += (acc[j][0] * acc[j][0] + acc[j][1] * acc[j][1]) + (acc[j][2] * acc[j][2] + acc[j][3] * acc[j][3]); }
;     ss += __shfl_xor(ss, 16); ss += __shfl_xor(ss, 32);
;     const float rs = rsqrtf(ss * (1.0f / DH) + EPS);
; #pragma unroll
;     for (int j = 0; j < 16; j += 2) { u32x2 ab[2];
; #pragma unroll
;         for (int n = 0; n < 2; ++n) { const int col = h * DH + 16 * (j + n) + 4 * fq;
;             const f32x4 gn = *(const f32x4*)(hgain + col); const u32x2 ov = *(const u32x2*)(Z + trow * EVN + 4096 + col);
;             const float o0 = bf_lo(ov.x), o1 = bf_hi(ov.x), o2 = bf_lo(ov.y), o3 = bf_hi(ov.y);
;             const float y0 = acc[j + n][0] * rs * gn[0] / (1.0f + expf(-o0)), y1 = acc[j + n][1] * rs * gn[1] / (1.0f + expf(-o1));
;             const float y2 = acc[j + n][2] * rs * gn[2] / (1.0f + expf(-o2)), y3 = acc[j + n][3] * rs * gn[3] / (1.0f + expf(-o3));
;             ab[n].x = cvt_pk_bf16(y0, y1); ab[n].y = cvt_pk_bf16(y2, y3); }
;         const bool odd = fq & 1; const u32x2 give = odd ? ab[0] : ab[1];
;         u32x2 got; got.x = (unsigned)__shfl_xor((int)give.x, 16); got.y = (unsigned)__shfl_xor((int)give.y, 16);
;         u32x4 w; if (odd) { w.x = got.x; w.y = got.y; w.z = ab[1].x; w.w = ab[1].y; } else { w.x = ab[0].x; w.y = ab[0].y; w.z = got.x; w.w = got.y; }
;         *(u32x4*)(YCAT + trow * D + 1024 + h * DH + 16 * (j + (odd ? 1 : 0)) + 4 * (fq & 2)) = w; if ((j & 3) == 2) asm volatile("" ::: "memory"); }
	v_mov_b32_e32 v76, v120
	v_mov_b32_e32 v77, v121
	v_mov_b32_e32 v78, v122
	v_mov_b32_e32 v79, v123
	v_pk_add_f32 v[84:85], v[26:27], v[26:27] op_sel_hi:[0,1]
	v_pk_mul_f32 v[26:27], v[22:23], v[74:75] op_sel_hi:[1,0]
	v_pk_mul_f32 v[22:23], v[24:25], v[24:25]
	v_pk_mul_f32 v[86:87], v[26:27], v[26:27]
	v_pk_mul_f32 v[20:21], v[20:21], v[74:75] op_sel_hi:[1,0]
	v_pk_mov_b32 v[88:89], v[86:87], v[22:23] op_sel:[1,0]
	v_mov_b32_e32 v87, v23
	v_pk_add_f32 v[22:23], v[88:89], v[86:87]
	v_pk_mul_f32 v[16:17], v[16:17], v[74:75] op_sel_hi:[1,0]
	v_pk_add_f32 v[86:87], v[22:23], v[22:23] op_sel_hi:[0,1]
	v_pk_mul_f32 v[22:23], v[18:19], v[74:75] op_sel_hi:[1,0]
	v_pk_mul_f32 v[14:15], v[14:15], v[74:75] op_sel_hi:[1,0]
	v_mul_f32_e32 v18, v22, v22
	v_pk_fma_f32 v[18:19], v[22:23], v[22:23], v[18:19] op_sel_hi:[1,1,0]
	v_mul_f32_e32 v86, v16, v16
	v_mul_f32_e32 v18, v20, v20
	v_pk_fma_f32 v[88:89], v[20:21], v[20:21], v[18:19] op_sel_hi:[1,1,0]
	v_mul_f32_e32 v18, v14, v14
	v_mul_f32_e32 v88, v15, v15
	v_mul_f32_e32 v84, v17, v17
	v_pk_add_f32 v[18:19], v[18:19], v[88:89]
	v_pk_add_f32 v[84:85], v[86:87], v[84:85]
	v_pk_mul_f32 v[12:13], v[12:13], v[74:75] op_sel_hi:[1,0]
	v_pk_add_f32 v[18:19], v[18:19], v[84:85]
	v_pk_mul_f32 v[10:11], v[10:11], v[74:75] op_sel_hi:[1,0]
	v_pk_add_f32 v[18:19], v[18:19], v[18:19] op_sel_hi:[0,1]
	v_pk_mul_f32 v[84:85], v[12:13], v[12:13]
	v_pk_mul_f32 v[86:87], v[10:11], v[10:11]
	v_pk_mul_f32 v[6:7], v[6:7], v[74:75] op_sel_hi:[1,0]
	v_pk_mov_b32 v[88:89], v[86:87], v[84:85] op_sel:[1,0]
	v_mov_b32_e32 v87, v85
	v_pk_mul_f32 v[8:9], v[8:9], v[74:75] op_sel_hi:[1,0]
	v_mul_f32_e32 v18, v6, v6
	v_pk_add_f32 v[84:85], v[88:89], v[86:87]
	v_pk_fma_f32 v[86:87], v[6:7], v[6:7], v[18:19] op_sel_hi:[1,1,0]
	v_mul_f32_e32 v18, v8, v8
	v_pk_add_f32 v[84:85], v[84:85], v[84:85] op_sel_hi:[0,1]
	v_pk_fma_f32 v[88:89], v[8:9], v[8:9], v[18:19] op_sel_hi:[1,1,0]
	v_pk_mul_f32 v[4:5], v[4:5], v[74:75] op_sel_hi:[1,0]
	v_pk_mul_f32 v[2:3], v[2:3], v[74:75] op_sel_hi:[1,0]
	v_mul_f32_e32 v84, v4, v4
	v_mul_f32_e32 v86, v2, v2
	v_mul_f32_e32 v88, v3, v3
	v_mul_f32_e32 v18, v5, v5
	v_pk_add_f32 v[86:87], v[86:87], v[88:89]
	v_pk_add_f32 v[18:19], v[84:85], v[18:19]
	s_nop 0
	v_lshlrev_b32_e32 v84, 16, v80
	v_pk_add_f32 v[18:19], v[86:87], v[18:19]
	v_mul_f32_e32 v74, 0xbfb8aa3b, v84
	v_add_f32_e32 v18, v18, v19
	ds_bpermute_b32 v19, v98, v18
	v_fma_f32 v85, v84, s76, -v74
	v_rndne_f32_e32 v86, v74
	v_fmac_f32_e32 v85, 0xb2a5705f, v84
	v_sub_f32_e32 v74, v74, v86
	s_waitcnt lgkmcnt(0)
	v_add_f32_e32 v18, v18, v19
	ds_bpermute_b32 v19, v115, v18
	v_add_f32_e32 v74, v74, v85
	v_exp_f32_e32 v85, v74
	v_cvt_i32_f32_e32 v86, v86
	v_and_b32_e32 v80, 0xffff0000, v80
	s_waitcnt lgkmcnt(0)
	v_add_f32_e32 v18, v18, v19
	v_fmamk_f32 v18, v18, 0x3b800000, v1
	v_mul_f32_e32 v19, 0x4b800000, v18
	v_cmp_gt_f32_e32 vcc, s79, v18
	s_nop 1
	v_cndmask_b32_e32 v18, v18, v19, vcc
	v_rsq_f32_e32 v18, v18
	s_nop 0
	v_mul_f32_e32 v19, 0x45800000, v18
	v_cndmask_b32_e32 v74, v18, v19, vcc
	v_ldexp_f32 v19, v85, v86
	v_cmp_nlt_f32_e32 vcc, s77, v84
	v_mul_f32_e32 v18, v82, v74
	v_mul_f32_e32 v83, v83, v74
	v_cndmask_b32_e32 v19, 0, v19, vcc
	v_cmp_ngt_f32_e32 vcc, s78, v84
	s_nop 0
	v_mul_f32_e32 v18, v76, v18
	v_mul_f32_e32 v77, v77, v83
	v_cndmask_b32_e32 v19, v97, v19, vcc
	v_add_f32_e32 v19, 1.0, v19
	v_div_scale_f32 v76, s[2:3], v19, v19, v18
	v_rcp_f32_e32 v82, v76
	v_cmp_nlt_f32_e64 s[2:3], s77, v80
	v_lshlrev_b32_e32 v84, 16, v81
	v_mul_f32_e32 v64, v64, v74
	v_fma_f32 v85, -v76, v82, 1.0
	v_fmac_f32_e32 v82, v85, v82
	v_div_scale_f32 v85, vcc, v18, v19, v18
	v_mul_f32_e32 v86, v85, v82
	v_fma_f32 v87, -v76, v86, v85
	v_fmac_f32_e32 v86, v87, v82
	v_mul_f32_e32 v87, 0xbfb8aa3b, v80
	v_fma_f32 v88, v80, s76, -v87
	v_rndne_f32_e32 v89, v87
	v_fmac_f32_e32 v88, 0xb2a5705f, v80
	v_sub_f32_e32 v87, v87, v89
	v_add_f32_e32 v87, v87, v88
	v_exp_f32_e32 v87, v87
	v_cvt_i32_f32_e32 v88, v89
	v_fma_f32 v76, -v76, v86, v85
	v_div_fmas_f32 v76, v76, v82, v86
	v_div_fixup_f32 v18, v76, v19, v18
	v_ldexp_f32 v83, v87, v88
	v_cndmask_b32_e64 v83, 0, v83, s[2:3]
	v_cmp_ngt_f32_e64 s[2:3], s78, v80
	v_mul_f32_e32 v64, v78, v64
	v_and_b32_e32 v81, 0xffff0000, v81
	v_cndmask_b32_e64 v80, v97, v83, s[2:3]
	v_add_f32_e32 v80, 1.0, v80
	v_div_scale_f32 v83, s[2:3], v80, v80, v77
	v_rcp_f32_e32 v85, v83
	v_cmp_nlt_f32_e64 s[2:3], s77, v84
	v_mul_f32_e32 v65, v65, v74
	v_mul_f32_e32 v65, v79, v65
	v_fma_f32 v19, -v83, v85, 1.0
	v_fmac_f32_e32 v85, v19, v85
	v_div_scale_f32 v19, vcc, v77, v80, v77
	v_mul_f32_e32 v76, v19, v85
	v_fma_f32 v82, -v83, v76, v19
	v_fmac_f32_e32 v76, v82, v85
	v_mul_f32_e32 v82, 0xbfb8aa3b, v84
	v_fma_f32 v86, v84, s76, -v82
	v_rndne_f32_e32 v87, v82
	v_fmac_f32_e32 v86, 0xb2a5705f, v84
	v_sub_f32_e32 v82, v82, v87
	v_add_f32_e32 v82, v82, v86
	v_exp_f32_e32 v82, v82
	v_cvt_i32_f32_e32 v86, v87
	v_fma_f32 v19, -v83, v76, v19
	v_div_fmas_f32 v19, v19, v85, v76
	v_div_fixup_f32 v19, v19, v80, v77
	v_ldexp_f32 v78, v82, v86
	v_cndmask_b32_e64 v78, 0, v78, s[2:3]
	v_cmp_ngt_f32_e64 s[2:3], s78, v84
	v_mul_f32_e32 v62, v62, v74
	v_mul_f32_e32 v63, v63, v74
	v_cndmask_b32_e64 v78, v97, v78, s[2:3]
	v_add_f32_e32 v78, 1.0, v78
	v_div_scale_f32 v82, s[2:3], v78, v78, v64
	v_rcp_f32_e32 v83, v82
	v_cmp_nlt_f32_e64 s[2:3], s77, v81
	v_mul_f32_e32 v60, v60, v74
	v_mul_f32_e32 v61, v61, v74
	v_fma_f32 v76, -v82, v83, 1.0
	v_fmac_f32_e32 v83, v76, v83
	v_div_scale_f32 v76, vcc, v64, v78, v64
	v_mul_f32_e32 v77, v76, v83
	v_fma_f32 v80, -v82, v77, v76
	v_fmac_f32_e32 v77, v80, v83
	v_mul_f32_e32 v80, 0xbfb8aa3b, v81
	v_fma_f32 v84, v81, s76, -v80
	v_rndne_f32_e32 v85, v80
	v_fmac_f32_e32 v84, 0xb2a5705f, v81
	v_sub_f32_e32 v80, v80, v85
	v_add_f32_e32 v80, v80, v84
	v_exp_f32_e32 v80, v80
	v_cvt_i32_f32_e32 v84, v85
	v_fma_f32 v76, -v82, v77, v76
	v_div_fmas_f32 v76, v76, v83, v77
	v_div_fixup_f32 v64, v76, v78, v64
	v_ldexp_f32 v79, v80, v84
	v_cndmask_b32_e64 v79, 0, v79, s[2:3]
	v_cmp_ngt_f32_e64 s[2:3], s78, v81
	v_mul_f32_e32 v58, v58, v74
	v_mul_f32_e32 v59, v59, v74
	v_cndmask_b32_e64 v79, v97, v79, s[2:3]
	v_add_f32_e32 v79, 1.0, v79
	v_div_scale_f32 v80, s[2:3], v79, v79, v65
	v_rcp_f32_e32 v81, v80
	v_mul_f32_e32 v56, v56, v74
	v_mul_f32_e32 v57, v57, v74
	v_mul_f32_e32 v54, v54, v74
	v_fma_f32 v76, -v80, v81, 1.0
	v_fmac_f32_e32 v81, v76, v81
	v_div_scale_f32 v76, vcc, v65, v79, v65
	v_mul_f32_e32 v77, v76, v81
	v_fma_f32 v78, -v80, v77, v76
	v_fmac_f32_e32 v77, v78, v81
	v_fma_f32 v76, -v80, v77, v76
	v_cvt_pk_bf16_f32 v80, v18, v19
	v_or_b32_e32 v18, 32, v66
	v_mov_b32_e32 v19, v67
	v_div_fmas_f32 v76, v76, v81, v77
	v_lshl_add_u64 v[18:19], v[72:73], 0, v[18:19]
	v_div_fixup_f32 v65, v76, v79, v65
	v_cvt_pk_bf16_f32 v64, v64, v65
	v_mov_b32_e32 v18, v196
	v_mov_b32_e32 v19, v197
	s_nop 0
	s_waitcnt vmcnt(14)
; __device__ __forceinline__ unsigned cvt_pk_bf16(float lo, float hi) { unsigned r; asm volatile("v_cvt_pk_bf16_f32 %0, %1, %2" : "=v"(r) : "v"(lo), "v"(hi)); return r; }
; __device__ __forceinline__ void mlstm_D(LAS unsigned char* lds, int c, int h, const bf16_t* Z, const float* gi, const float* bcum, const float* marr, const bf16_t* CST, const float* NST,
;                                         const float* hgain, bf16_t* YCAT) {
;     ...
;     for (int j = 0; j < 16; ++j) { acc[j] = acc[j] * inv; ss += (acc[j][0] * acc[j][0] + acc[j][1] * acc[j][1]) + (acc[j][2] * acc[j][2] + acc[j][3] * acc[j][3]); }
;     ss += __shfl_xor(ss, 16); ss += __shfl_xor(ss, 32);
;     const float rs = rsqrtf(ss * (1.0f / DH) + EPS);
; #pragma unroll
;     for (int j = 0; j < 16; j += 2) { u32x2 ab[2];
; #pragma unroll
;         for (int n = 0; n < 2; ++n) { const int col = h * DH + 16 * (j + n) + 4 * fq;
;             const f32x4 gn = *(const f32x4*)(hgain + col); const u32x2 ov = *(const u32x2*)(Z + trow * EVN + 4096 + col);
;             const float o0 = bf_lo(ov.x), o1 = bf_hi(ov.x), o2 = bf_lo(ov.y), o3 = bf_hi(ov.y);
;             const float y0 = acc[j + n][0] * rs * gn[0] / (1.0f + expf(-o0)), y1 = acc[j + n][1] * rs * gn[1] / (1.0f + expf(-o1));
;             const float y2 = acc[j + n][2] * rs * gn[2] / (1.0f + expf(-o2)), y3 = acc[j + n][3] * rs * gn[3] / (1.0f + expf(-o3));
;             ab[n].x = cvt_pk_bf16(y0, y1); ab[n].y = cvt_pk_bf16(y2, y3); }
;         const bool odd = fq & 1; const u32x2 give = odd ? ab[0] : ab[1];
;         u32x2 got; got.x = (unsigned)__shfl_xor((int)give.x, 16); got.y = (unsigned)__shfl_xor((int)give.y, 16);
	v_mov_b32_e32 v76, v124
	v_mov_b32_e32 v77, v125
	v_mov_b32_e32 v78, v126
	v_mov_b32_e32 v79, v127
	v_mul_f32_e32 v55, v55, v74
	v_mul_f32_e32 v52, v52, v74
	v_mul_f32_e32 v53, v53, v74
	v_mul_f32_e32 v50, v50, v74
	v_mul_f32_e32 v51, v51, v74
	v_mul_f32_e32 v48, v48, v74
	v_mul_f32_e32 v49, v49, v74
	v_mul_f32_e32 v46, v46, v74
	v_mul_f32_e32 v47, v47, v74
	v_mul_f32_e32 v44, v44, v74
	v_mul_f32_e32 v45, v45, v74
	v_mul_f32_e32 v42, v42, v74
	v_mul_f32_e32 v43, v43, v74
	v_mul_f32_e32 v40, v40, v74
	v_mul_f32_e32 v41, v41, v74
	v_mul_f32_e32 v38, v38, v74
	v_mul_f32_e32 v39, v39, v74
	v_mul_f32_e32 v36, v36, v74
	v_mul_f32_e32 v37, v37, v74
	v_mul_f32_e32 v34, v34, v74
	v_mul_f32_e32 v35, v35, v74
	v_mul_f32_e32 v32, v32, v74
	v_mul_f32_e32 v33, v33, v74
	v_mul_f32_e32 v30, v30, v74
	v_mul_f32_e32 v31, v31, v74
	v_mul_f32_e32 v28, v28, v74
	v_mul_f32_e32 v29, v29, v74
	v_mul_f32_e32 v26, v26, v74
	v_mul_f32_e32 v27, v27, v74
	v_mul_f32_e32 v24, v24, v74
	v_mul_f32_e32 v25, v25, v74
	v_mul_f32_e32 v22, v22, v74
	v_mul_f32_e32 v23, v23, v74
	v_mul_f32_e32 v20, v20, v74
	v_mul_f32_e32 v21, v21, v74
	v_mul_f32_e32 v14, v14, v74
	v_mul_f32_e32 v15, v15, v74
	v_mul_f32_e32 v16, v16, v74
	v_mul_f32_e32 v17, v17, v74
	v_mul_f32_e32 v10, v10, v74
	v_mul_f32_e32 v11, v11, v74
	v_mul_f32_e32 v12, v12, v74
	v_mul_f32_e32 v13, v13, v74
	v_mul_f32_e32 v6, v6, v74
	v_mul_f32_e32 v7, v7, v74
	v_mul_f32_e32 v8, v8, v74
	v_mul_f32_e32 v9, v9, v74
	v_mul_f32_e32 v2, v2, v74
	v_mul_f32_e32 v3, v3, v74
	v_mul_f32_e32 v4, v4, v74
	v_mul_f32_e32 v5, v5, v74
	s_nop 0
	v_lshlrev_b32_e32 v65, 16, v18
	v_mul_f32_e32 v81, 0xbfb8aa3b, v65
	v_fma_f32 v82, v65, s76, -v81
	v_rndne_f32_e32 v83, v81
	v_fmac_f32_e32 v82, 0xb2a5705f, v65
	v_sub_f32_e32 v81, v81, v83
	v_add_f32_e32 v81, v81, v82
	v_exp_f32_e32 v81, v81
	v_cvt_i32_f32_e32 v82, v83
	s_nop 0
	v_mul_f32_e32 v62, v76, v62
	v_cmp_nlt_f32_e32 vcc, s77, v65
	v_and_b32_e32 v18, 0xffff0000, v18
	v_ldexp_f32 v76, v81, v82
	v_cndmask_b32_e32 v76, 0, v76, vcc
	v_cmp_ngt_f32_e32 vcc, s78, v65
	v_mul_f32_e32 v63, v77, v63
	v_lshlrev_b32_e32 v82, 16, v19
	v_cndmask_b32_e32 v65, v97, v76, vcc
	v_add_f32_e32 v65, 1.0, v65
	v_div_scale_f32 v76, s[2:3], v65, v65, v62
	v_rcp_f32_e32 v81, v76
	v_cmp_nlt_f32_e64 s[2:3], s77, v18
	v_mul_f32_e32 v60, v78, v60
	v_and_b32_e32 v19, 0xffff0000, v19
	v_fma_f32 v84, -v76, v81, 1.0
	v_fmac_f32_e32 v81, v84, v81
	v_div_scale_f32 v84, vcc, v62, v65, v62
	v_mul_f32_e32 v85, v84, v81
	v_fma_f32 v86, -v76, v85, v84
	v_fmac_f32_e32 v85, v86, v81
	v_mul_f32_e32 v86, 0xbfb8aa3b, v18
	v_fma_f32 v87, v18, s76, -v86
	v_rndne_f32_e32 v88, v86
	v_fmac_f32_e32 v87, 0xb2a5705f, v18
	v_sub_f32_e32 v86, v86, v88
	v_add_f32_e32 v86, v86, v87
	v_exp_f32_e32 v86, v86
	v_cvt_i32_f32_e32 v87, v88
	v_fma_f32 v76, -v76, v85, v84
	v_div_fmas_f32 v76, v76, v81, v85
	v_div_fixup_f32 v62, v76, v65, v62
	v_ldexp_f32 v77, v86, v87
	v_cndmask_b32_e64 v77, 0, v77, s[2:3]
	v_cmp_ngt_f32_e64 s[2:3], s78, v18
	v_mul_f32_e32 v61, v79, v61
	v_and_b32_e32 v83, 16, v99
	v_cndmask_b32_e64 v18, v97, v77, s[2:3]
	v_add_f32_e32 v18, 1.0, v18
	v_div_scale_f32 v77, s[2:3], v18, v18, v63
	v_rcp_f32_e32 v84, v77
	v_cmp_nlt_f32_e64 s[2:3], s77, v82
	v_fma_f32 v65, -v77, v84, 1.0
	v_fmac_f32_e32 v84, v65, v84
	v_div_scale_f32 v65, vcc, v63, v18, v63
	v_mul_f32_e32 v76, v65, v84
	v_fma_f32 v81, -v77, v76, v65
	v_fmac_f32_e32 v76, v81, v84
	v_mul_f32_e32 v81, 0xbfb8aa3b, v82
	v_fma_f32 v85, v82, s76, -v81
	v_rndne_f32_e32 v86, v81
	v_fmac_f32_e32 v85, 0xb2a5705f, v82
	v_sub_f32_e32 v81, v81, v86
	v_add_f32_e32 v81, v81, v85
	v_exp_f32_e32 v81, v81
	v_cvt_i32_f32_e32 v85, v86
	v_fma_f32 v65, -v77, v76, v65
	v_div_fmas_f32 v65, v65, v84, v76
	v_div_fixup_f32 v18, v65, v18, v63
	v_ldexp_f32 v77, v81, v85
	v_cndmask_b32_e64 v77, 0, v77, s[2:3]
	v_cmp_ngt_f32_e64 s[2:3], s78, v82
	v_cvt_pk_bf16_f32 v18, v62, v18
	s_nop 1
	v_cndmask_b32_e64 v77, v97, v77, s[2:3]
	v_add_f32_e32 v77, 1.0, v77
	v_div_scale_f32 v78, s[2:3], v77, v77, v60
	v_rcp_f32_e32 v81, v78
	v_cmp_nlt_f32_e64 s[2:3], s77, v19
	v_fma_f32 v63, -v78, v81, 1.0
	v_fmac_f32_e32 v81, v63, v81
	v_div_scale_f32 v63, vcc, v60, v77, v60
	v_mul_f32_e32 v65, v63, v81
	v_fma_f32 v76, -v78, v65, v63
	v_fmac_f32_e32 v65, v76, v81
	v_mul_f32_e32 v76, 0xbfb8aa3b, v19
	v_fma_f32 v82, v19, s76, -v76
	v_rndne_f32_e32 v84, v76
	v_fmac_f32_e32 v82, 0xb2a5705f, v19
	v_sub_f32_e32 v76, v76, v84
	v_add_f32_e32 v76, v76, v82
	v_exp_f32_e32 v76, v76
	v_cvt_i32_f32_e32 v82, v84
	v_fma_f32 v63, -v78, v65, v63
	v_div_fmas_f32 v63, v63, v81, v65
	v_div_fixup_f32 v60, v63, v77, v60
	v_ldexp_f32 v76, v76, v82
	v_cndmask_b32_e64 v76, 0, v76, s[2:3]
	v_cmp_ngt_f32_e64 s[2:3], s78, v19
	s_nop 1
	v_cndmask_b32_e64 v19, v97, v76, s[2:3]
	v_add_f32_e32 v19, 1.0, v19
	v_div_scale_f32 v76, s[2:3], v19, v19, v61
	v_rcp_f32_e32 v78, v76
	v_cmp_eq_u32_e64 s[2:3], 0, v83
	v_fma_f32 v63, -v76, v78, 1.0
	v_fmac_f32_e32 v78, v63, v78
	v_div_scale_f32 v63, vcc, v61, v19, v61
	v_mul_f32_e32 v65, v63, v78
	v_fma_f32 v77, -v76, v65, v63
	v_fmac_f32_e32 v65, v77, v78
	v_fma_f32 v63, -v76, v65, v63
	v_div_fmas_f32 v63, v63, v78, v65
	v_div_fixup_f32 v19, v63, v19, v61
	v_cvt_pk_bf16_f32 v19, v60, v19
	v_cndmask_b32_e64 v61, v80, v18, s[2:3]
	v_cndmask_b32_e64 v60, v64, v19, s[2:3]
	ds_bpermute_b32 v61, v98, v61
	ds_bpermute_b32 v65, v98, v60
	s_waitcnt lgkmcnt(1)
	v_cndmask_b32_e64 v62, v18, v61, s[2:3]
	s_waitcnt lgkmcnt(0)
; __device__ __forceinline__ unsigned cvt_pk_bf16(float lo, float hi) { unsigned r; asm volatile("v_cvt_pk_bf16_f32 %0, %1, %2" : "=v"(r) : "v"(lo), "v"(hi)); return r; }
; __device__ __forceinline__ void mlstm_D(LAS unsigned char* lds, int c, int h, const bf16_t* Z, const float* gi, const float* bcum, const float* marr, const bf16_t* CST, const float* NST,
;                                         const float* hgain, bf16_t* YCAT) {
;     ...
;         for (int n = 0; n < 2; ++n) { const int col = h * DH + 16 * (j + n) + 4 * fq;
;             const f32x4 gn = *(const f32x4*)(hgain + col); const u32x2 ov = *(const u32x2*)(Z + trow * EVN + 4096 + col);
;             const float o0 = bf_lo(ov.x), o1 = bf_hi(ov.x), o2 = bf_lo(ov.y), o3 = bf_hi(ov.y);
;             const float y0 = acc[j + n][0] * rs * gn[0] / (1.0f + expf(-o0)), y1 = acc[j + n][1] * rs * gn[1] / (1.0f + expf(-o1));
;             const float y2 = acc[j + n][2] * rs * gn[2] / (1.0f + expf(-o2)), y3 = acc[j + n][3] * rs * gn[3] / (1.0f + expf(-o3));
;             ab[n].x = cvt_pk_bf16(y0, y1); ab[n].y = cvt_pk_bf16(y2, y3); }
;         const bool odd = fq & 1; const u32x2 give = odd ? ab[0] : ab[1];
;         u32x2 got; got.x = (unsigned)__shfl_xor((int)give.x, 16); got.y = (unsigned)__shfl_xor((int)give.y, 16);
;         u32x4 w; if (odd) { w.x = got.x; w.y = got.y; w.z = ab[1].x; w.w = ab[1].y; } else { w.x = ab[0].x; w.y = ab[0].y; w.z = got.x; w.w = got.y; }
;         *(u32x4*)(YCAT + trow * D + 1024 + h * DH + 16 * (j + (odd ? 1 : 0)) + 4 * (fq & 2)) = w; if ((j & 3) == 2) asm volatile("" ::: "memory"); }
	v_cndmask_b32_e64 v63, v19, v65, s[2:3]
	v_lshlrev_b32_e32 v18, 1, v83
	v_mov_b32_e32 v19, v67
	v_lshl_add_u64 v[18:19], v[70:71], 0, v[18:19]
	v_cndmask_b32_e64 v60, v61, v80, s[2:3]
	v_cndmask_b32_e64 v61, v65, v64, s[2:3]
	v_add_co_u32_e32 v64, vcc, 4.0, v18
	s_nop 1
	v_addc_co_u32_e32 v65, vcc, 0, v19, vcc
	global_store_dwordx4 v[64:65], v[60:63], off offset:2048
	v_lshl_add_u64 v[18:19], v[18:19], 0, s[46:47]
	s_nop 0
	v_or_b32_e32 v60, 64, v66
	v_mov_b32_e32 v61, v67
	v_lshl_add_u64 v[60:61], v[72:73], 0, v[60:61]
	v_mov_b32_e32 v64, v198
	v_mov_b32_e32 v65, v199
	s_nop 0
	s_waitcnt vmcnt(14)
	v_mov_b32_e32 v60, v128
	v_mov_b32_e32 v61, v129
	v_mov_b32_e32 v62, v130
	v_mov_b32_e32 v63, v131
	s_nop 0
	v_lshlrev_b32_e32 v70, 16, v64
	v_mul_f32_e32 v71, 0xbfb8aa3b, v70
	v_fma_f32 v76, v70, s76, -v71
	v_rndne_f32_e32 v77, v71
	v_fmac_f32_e32 v76, 0xb2a5705f, v70
	v_sub_f32_e32 v71, v71, v77
	v_add_f32_e32 v71, v71, v76
	v_exp_f32_e32 v71, v71
	v_cvt_i32_f32_e32 v76, v77
	s_nop 0
	v_mul_f32_e32 v58, v60, v58
	v_cmp_nlt_f32_e32 vcc, s77, v70
	v_and_b32_e32 v64, 0xffff0000, v64
	v_ldexp_f32 v60, v71, v76
	v_cndmask_b32_e32 v60, 0, v60, vcc
	v_cmp_ngt_f32_e32 vcc, s78, v70
	v_mul_f32_e32 v59, v61, v59
	v_lshlrev_b32_e32 v76, 16, v65
	v_cndmask_b32_e32 v60, v97, v60, vcc
	v_add_f32_e32 v60, 1.0, v60
	v_div_scale_f32 v70, s[4:5], v60, v60, v58
	v_rcp_f32_e32 v71, v70
	v_cmp_nlt_f32_e64 s[4:5], s77, v64
	v_mul_f32_e32 v56, v62, v56
	v_and_b32_e32 v65, 0xffff0000, v65
	v_fma_f32 v77, -v70, v71, 1.0
	v_fmac_f32_e32 v71, v77, v71
	v_div_scale_f32 v77, vcc, v58, v60, v58
	v_mul_f32_e32 v78, v77, v71
	v_fma_f32 v79, -v70, v78, v77
	v_fmac_f32_e32 v78, v79, v71
	v_mul_f32_e32 v79, 0xbfb8aa3b, v64
	v_fma_f32 v80, v64, s76, -v79
	v_rndne_f32_e32 v81, v79
	v_fmac_f32_e32 v80, 0xb2a5705f, v64
	v_sub_f32_e32 v79, v79, v81
	v_add_f32_e32 v79, v79, v80
	v_exp_f32_e32 v79, v79
	v_cvt_i32_f32_e32 v80, v81
	v_fma_f32 v70, -v70, v78, v77
	v_div_fmas_f32 v70, v70, v71, v78
	v_div_fixup_f32 v58, v70, v60, v58
	v_ldexp_f32 v61, v79, v80
	v_cndmask_b32_e64 v61, 0, v61, s[4:5]
	v_cmp_ngt_f32_e64 s[4:5], s78, v64
	v_mul_f32_e32 v57, v63, v57
	s_nop 0
	v_cndmask_b32_e64 v61, v97, v61, s[4:5]
	v_add_f32_e32 v61, 1.0, v61
	v_div_scale_f32 v64, s[4:5], v61, v61, v59
	v_rcp_f32_e32 v77, v64
	v_cmp_nlt_f32_e64 s[4:5], s77, v76
	v_fma_f32 v60, -v64, v77, 1.0
	v_fmac_f32_e32 v77, v60, v77
	v_div_scale_f32 v60, vcc, v59, v61, v59
	v_mul_f32_e32 v70, v60, v77
	v_fma_f32 v71, -v64, v70, v60
	v_fmac_f32_e32 v70, v71, v77
	v_mul_f32_e32 v71, 0xbfb8aa3b, v76
	v_fma_f32 v78, v76, s76, -v71
	v_rndne_f32_e32 v79, v71
	v_fmac_f32_e32 v78, 0xb2a5705f, v76
	v_sub_f32_e32 v71, v71, v79
	v_add_f32_e32 v71, v71, v78
	v_exp_f32_e32 v71, v71
	v_cvt_i32_f32_e32 v78, v79
	v_fma_f32 v60, -v64, v70, v60
	v_div_fmas_f32 v60, v60, v77, v70
	v_div_fixup_f32 v59, v60, v61, v59
	v_ldexp_f32 v62, v71, v78
	v_cndmask_b32_e64 v62, 0, v62, s[4:5]
	v_cmp_ngt_f32_e64 s[4:5], s78, v76
	s_nop 1
	v_cndmask_b32_e64 v62, v97, v62, s[4:5]
	v_add_f32_e32 v62, 1.0, v62
	v_div_scale_f32 v64, s[4:5], v62, v62, v56
	v_rcp_f32_e32 v71, v64
	v_cmp_nlt_f32_e64 s[4:5], s77, v65
	v_fma_f32 v60, -v64, v71, 1.0
	v_fmac_f32_e32 v71, v60, v71
	v_div_scale_f32 v60, vcc, v56, v62, v56
	v_mul_f32_e32 v61, v60, v71
	v_fma_f32 v70, -v64, v61, v60
	v_fmac_f32_e32 v61, v70, v71
	v_mul_f32_e32 v70, 0xbfb8aa3b, v65
	v_fma_f32 v76, v65, s76, -v70
	v_rndne_f32_e32 v77, v70
	v_fmac_f32_e32 v76, 0xb2a5705f, v65
	v_sub_f32_e32 v70, v70, v77
	v_add_f32_e32 v70, v70, v76
	v_exp_f32_e32 v70, v70
	v_cvt_i32_f32_e32 v76, v77
	v_fma_f32 v60, -v64, v61, v60
	v_div_fmas_f32 v60, v60, v71, v61
	v_div_fixup_f32 v56, v60, v62, v56
	v_ldexp_f32 v63, v70, v76
	v_cndmask_b32_e64 v63, 0, v63, s[4:5]
	v_cmp_ngt_f32_e64 s[4:5], s78, v65
	s_nop 1
	v_cndmask_b32_e64 v63, v97, v63, s[4:5]
	v_add_f32_e32 v63, 1.0, v63
	v_div_scale_f32 v64, s[4:5], v63, v63, v57
	v_rcp_f32_e32 v65, v64
	s_nop 0
	v_fma_f32 v60, -v64, v65, 1.0
	v_fmac_f32_e32 v65, v60, v65
	v_div_scale_f32 v60, vcc, v57, v63, v57
	v_mul_f32_e32 v61, v60, v65
	v_fma_f32 v62, -v64, v61, v60
	v_fmac_f32_e32 v61, v62, v65
	v_fma_f32 v60, -v64, v61, v60
	v_div_fmas_f32 v60, v60, v65, v61
	v_div_fixup_f32 v57, v60, v63, v57
	v_cvt_pk_bf16_f32 v62, v58, v59
	v_cvt_pk_bf16_f32 v63, v56, v57
	v_or_b32_e32 v56, 0x60, v66
	v_mov_b32_e32 v57, v67
	v_lshl_add_u64 v[56:57], v[72:73], 0, v[56:57]
	v_mov_b32_e32 v60, v200
	v_mov_b32_e32 v61, v201
	s_nop 0
	s_waitcnt vmcnt(13)
; __device__ __forceinline__ unsigned cvt_pk_bf16(float lo, float hi) { unsigned r; asm volatile("v_cvt_pk_bf16_f32 %0, %1, %2" : "=v"(r) : "v"(lo), "v"(hi)); return r; }
; __device__ __forceinline__ void mlstm_D(LAS unsigned char* lds, int c, int h, const bf16_t* Z, const float* gi, const float* bcum, const float* marr, const bf16_t* CST, const float* NST,
;                                         const float* hgain, bf16_t* YCAT) {
;     ...
;         for (int n = 0; n < 2; ++n) { const int col = h * DH + 16 * (j + n) + 4 * fq;
;             const f32x4 gn = *(const f32x4*)(hgain + col); const u32x2 ov = *(const u32x2*)(Z + trow * EVN + 4096 + col);
;             const float o0 = bf_lo(ov.x), o1 = bf_hi(ov.x), o2 = bf_lo(ov.y), o3 = bf_hi(ov.y);
;             const float y0 = acc[j + n][0] * rs * gn[0] / (1.0f + expf(-o0)), y1 = acc[j + n][1] * rs * gn[1] / (1.0f + expf(-o1));
;             const float y2 = acc[j + n][2] * rs * gn[2] / (1.0f + expf(-o2)), y3 = acc[j + n][3] * rs * gn[3] / (1.0f + expf(-o3));
;             ab[n].x = cvt_pk_bf16(y0, y1); ab[n].y = cvt_pk_bf16(y2, y3); }
;         const bool odd = fq & 1; const u32x2 give = odd ? ab[0] : ab[1];
;         u32x2 got; got.x = (unsigned)__shfl_xor((int)give.x, 16); got.y = (unsigned)__shfl_xor((int)give.y, 16);
;         u32x4 w; if (odd) { w.x = got.x; w.y = got.y; w.z = ab[1].x; w.w = ab[1].y; } else { w.x = ab[0].x; w.y = ab[0].y; w.z = got.x; w.w = got.y; }
;         *(u32x4*)(YCAT + trow * D + 1024 + h * DH + 16 * (j + (odd ? 1 : 0)) + 4 * (fq & 2)) = w; if ((j & 3) == 2) asm volatile("" ::: "memory"); }
	v_mov_b32_e32 v56, v132
	v_mov_b32_e32 v57, v133
	v_mov_b32_e32 v58, v134
	v_mov_b32_e32 v59, v135
	s_nop 0
	v_lshlrev_b32_e32 v64, 16, v60
	v_mul_f32_e32 v65, 0xbfb8aa3b, v64
	v_fma_f32 v70, v64, s76, -v65
	v_rndne_f32_e32 v71, v65
	v_fmac_f32_e32 v70, 0xb2a5705f, v64
	v_sub_f32_e32 v65, v65, v71
	v_add_f32_e32 v65, v65, v70
	v_exp_f32_e32 v65, v65
	v_cvt_i32_f32_e32 v70, v71
	s_nop 0
	v_mul_f32_e32 v54, v56, v54
	v_cmp_nlt_f32_e32 vcc, s77, v64
	v_and_b32_e32 v60, 0xffff0000, v60
	v_ldexp_f32 v56, v65, v70
	v_cndmask_b32_e32 v56, 0, v56, vcc
	v_cmp_ngt_f32_e32 vcc, s78, v64
	v_mul_f32_e32 v55, v57, v55
	v_lshlrev_b32_e32 v70, 16, v61
	v_cndmask_b32_e32 v56, v97, v56, vcc
	v_add_f32_e32 v56, 1.0, v56
	v_div_scale_f32 v64, s[4:5], v56, v56, v54
	v_rcp_f32_e32 v65, v64
	v_cmp_nlt_f32_e64 s[4:5], s77, v60
	v_mul_f32_e32 v52, v58, v52
	v_and_b32_e32 v61, 0xffff0000, v61
	v_fma_f32 v71, -v64, v65, 1.0
	v_fmac_f32_e32 v65, v71, v65
	v_div_scale_f32 v71, vcc, v54, v56, v54
	v_mul_f32_e32 v76, v71, v65
	v_fma_f32 v77, -v64, v76, v71
	v_fmac_f32_e32 v76, v77, v65
	v_mul_f32_e32 v77, 0xbfb8aa3b, v60
	v_fma_f32 v78, v60, s76, -v77
	v_rndne_f32_e32 v79, v77
	v_fmac_f32_e32 v78, 0xb2a5705f, v60
	v_sub_f32_e32 v77, v77, v79
	v_add_f32_e32 v77, v77, v78
	v_exp_f32_e32 v77, v77
	v_cvt_i32_f32_e32 v78, v79
	v_fma_f32 v64, -v64, v76, v71
	v_div_fmas_f32 v64, v64, v65, v76
	v_div_fixup_f32 v54, v64, v56, v54
	v_ldexp_f32 v57, v77, v78
	v_cndmask_b32_e64 v57, 0, v57, s[4:5]
	v_cmp_ngt_f32_e64 s[4:5], s78, v60
	v_mul_f32_e32 v53, v59, v53
	s_nop 0
	v_cndmask_b32_e64 v57, v97, v57, s[4:5]
	v_add_f32_e32 v57, 1.0, v57
	v_div_scale_f32 v60, s[4:5], v57, v57, v55
	v_rcp_f32_e32 v71, v60
	v_cmp_nlt_f32_e64 s[4:5], s77, v70
	v_fma_f32 v56, -v60, v71, 1.0
	v_fmac_f32_e32 v71, v56, v71
	v_div_scale_f32 v56, vcc, v55, v57, v55
	v_mul_f32_e32 v64, v56, v71
	v_fma_f32 v65, -v60, v64, v56
	v_fmac_f32_e32 v64, v65, v71
	v_mul_f32_e32 v65, 0xbfb8aa3b, v70
	v_fma_f32 v76, v70, s76, -v65
	v_rndne_f32_e32 v77, v65
	v_fmac_f32_e32 v76, 0xb2a5705f, v70
	v_sub_f32_e32 v65, v65, v77
	v_add_f32_e32 v65, v65, v76
	v_exp_f32_e32 v65, v65
	v_cvt_i32_f32_e32 v76, v77
	v_fma_f32 v56, -v60, v64, v56
	v_div_fmas_f32 v56, v56, v71, v64
	v_div_fixup_f32 v55, v56, v57, v55
	v_ldexp_f32 v58, v65, v76
	v_cndmask_b32_e64 v58, 0, v58, s[4:5]
	v_cmp_ngt_f32_e64 s[4:5], s78, v70
	v_cvt_pk_bf16_f32 v54, v54, v55
	s_nop 1
	v_cndmask_b32_e64 v58, v97, v58, s[4:5]
	v_add_f32_e32 v58, 1.0, v58
	v_div_scale_f32 v60, s[4:5], v58, v58, v52
	v_rcp_f32_e32 v65, v60
	v_cmp_nlt_f32_e64 s[4:5], s77, v61
	v_fma_f32 v56, -v60, v65, 1.0
	v_fmac_f32_e32 v65, v56, v65
	v_div_scale_f32 v56, vcc, v52, v58, v52
	v_mul_f32_e32 v57, v56, v65
	v_fma_f32 v64, -v60, v57, v56
	v_fmac_f32_e32 v57, v64, v65
	v_mul_f32_e32 v64, 0xbfb8aa3b, v61
	v_fma_f32 v70, v61, s76, -v64
	v_rndne_f32_e32 v71, v64
	v_fmac_f32_e32 v70, 0xb2a5705f, v61
	v_sub_f32_e32 v64, v64, v71
	v_add_f32_e32 v64, v64, v70
	v_exp_f32_e32 v64, v64
	v_cvt_i32_f32_e32 v70, v71
	v_fma_f32 v56, -v60, v57, v56
	v_div_fmas_f32 v56, v56, v65, v57
	v_div_fixup_f32 v52, v56, v58, v52
	v_ldexp_f32 v59, v64, v70
	v_cndmask_b32_e64 v59, 0, v59, s[4:5]
	v_cmp_ngt_f32_e64 s[4:5], s78, v61
	s_nop 1
	v_cndmask_b32_e64 v59, v97, v59, s[4:5]
	v_add_f32_e32 v59, 1.0, v59
	v_div_scale_f32 v60, s[4:5], v59, v59, v53
	v_rcp_f32_e32 v61, v60
	s_nop 0
	v_fma_f32 v56, -v60, v61, 1.0
	v_fmac_f32_e32 v61, v56, v61
	v_div_scale_f32 v56, vcc, v53, v59, v53
	v_mul_f32_e32 v57, v56, v61
	v_fma_f32 v58, -v60, v57, v56
	v_fmac_f32_e32 v57, v58, v61
	v_fma_f32 v56, -v60, v57, v56
	v_div_fmas_f32 v56, v56, v61, v57
	v_div_fixup_f32 v53, v56, v59, v53
	v_cvt_pk_bf16_f32 v53, v52, v53
	v_cndmask_b32_e64 v52, v62, v54, s[2:3]
	v_cndmask_b32_e64 v55, v63, v53, s[2:3]
	ds_bpermute_b32 v52, v98, v52
	ds_bpermute_b32 v56, v98, v55
	s_waitcnt lgkmcnt(1)
	v_cndmask_b32_e64 v54, v54, v52, s[2:3]
	v_cndmask_b32_e64 v52, v52, v62, s[2:3]
	s_waitcnt lgkmcnt(0)
	v_cndmask_b32_e64 v55, v53, v56, s[2:3]
	v_cndmask_b32_e64 v53, v56, v63, s[2:3]
	global_store_dwordx4 v[18:19], v[52:55], off offset:64
	s_nop 1
	v_or_b32_e32 v52, 0x80, v66
	v_mov_b32_e32 v53, v67
	v_lshl_add_u64 v[52:53], v[72:73], 0, v[52:53]
	v_mov_b32_e32 v56, v202
	v_mov_b32_e32 v57, v203
	s_nop 0
	s_waitcnt vmcnt(13)
; __device__ __forceinline__ unsigned cvt_pk_bf16(float lo, float hi) { unsigned r; asm volatile("v_cvt_pk_bf16_f32 %0, %1, %2" : "=v"(r) : "v"(lo), "v"(hi)); return r; }
; __device__ __forceinline__ void mlstm_D(LAS unsigned char* lds, int c, int h, const bf16_t* Z, const float* gi, const float* bcum, const float* marr, const bf16_t* CST, const float* NST,
;                                         const float* hgain, bf16_t* YCAT) {
;     ...
;         for (int n = 0; n < 2; ++n) { const int col = h * DH + 16 * (j + n) + 4 * fq;
;             const f32x4 gn = *(const f32x4*)(hgain + col); const u32x2 ov = *(const u32x2*)(Z + trow * EVN + 4096 + col);
;             const float o0 = bf_lo(ov.x), o1 = bf_hi(ov.x), o2 = bf_lo(ov.y), o3 = bf_hi(ov.y);
;             const float y0 = acc[j + n][0] * rs * gn[0] / (1.0f + expf(-o0)), y1 = acc[j + n][1] * rs * gn[1] / (1.0f + expf(-o1));
;             const float y2 = acc[j + n][2] * rs * gn[2] / (1.0f + expf(-o2)), y3 = acc[j + n][3] * rs * gn[3] / (1.0f + expf(-o3));
;             ab[n].x = cvt_pk_bf16(y0, y1); ab[n].y = cvt_pk_bf16(y2, y3); }
;         const bool odd = fq & 1; const u32x2 give = odd ? ab[0] : ab[1];
;         u32x2 got; got.x = (unsigned)__shfl_xor((int)give.x, 16); got.y = (unsigned)__shfl_xor((int)give.y, 16);
;         u32x4 w; if (odd) { w.x = got.x; w.y = got.y; w.z = ab[1].x; w.w = ab[1].y; } else { w.x = ab[0].x; w.y = ab[0].y; w.z = got.x; w.w = got.y; }
;         *(u32x4*)(YCAT + trow * D + 1024 + h * DH + 16 * (j + (odd ? 1 : 0)) + 4 * (fq & 2)) = w; if ((j & 3) == 2) asm volatile("" ::: "memory"); }
	v_mov_b32_e32 v52, v136
	v_mov_b32_e32 v53, v137
	v_mov_b32_e32 v54, v138
	v_mov_b32_e32 v55, v139
	s_nop 0
	v_lshlrev_b32_e32 v58, 16, v56
	v_mul_f32_e32 v59, 0xbfb8aa3b, v58
	v_fma_f32 v60, v58, s76, -v59
	v_rndne_f32_e32 v61, v59
	v_fmac_f32_e32 v60, 0xb2a5705f, v58
	v_sub_f32_e32 v59, v59, v61
	v_add_f32_e32 v59, v59, v60
	v_exp_f32_e32 v59, v59
	v_cvt_i32_f32_e32 v60, v61
	s_nop 0
	v_mul_f32_e32 v50, v52, v50
	v_cmp_nlt_f32_e32 vcc, s77, v58
	v_and_b32_e32 v56, 0xffff0000, v56
	v_ldexp_f32 v52, v59, v60
	v_cndmask_b32_e32 v52, 0, v52, vcc
	v_cmp_ngt_f32_e32 vcc, s78, v58
	v_mul_f32_e32 v51, v53, v51
	v_lshlrev_b32_e32 v60, 16, v57
	v_cndmask_b32_e32 v52, v97, v52, vcc
	v_add_f32_e32 v52, 1.0, v52
	v_div_scale_f32 v58, s[4:5], v52, v52, v50
	v_rcp_f32_e32 v59, v58
	v_cmp_nlt_f32_e64 s[4:5], s77, v56
	v_mul_f32_e32 v48, v54, v48
	v_and_b32_e32 v57, 0xffff0000, v57
	v_fma_f32 v61, -v58, v59, 1.0
	v_fmac_f32_e32 v59, v61, v59
	v_div_scale_f32 v61, vcc, v50, v52, v50
	v_mul_f32_e32 v62, v61, v59
	v_fma_f32 v63, -v58, v62, v61
	v_fmac_f32_e32 v62, v63, v59
	v_mul_f32_e32 v63, 0xbfb8aa3b, v56
	v_fma_f32 v64, v56, s76, -v63
	v_rndne_f32_e32 v65, v63
	v_fmac_f32_e32 v64, 0xb2a5705f, v56
	v_sub_f32_e32 v63, v63, v65
	v_add_f32_e32 v63, v63, v64
	v_exp_f32_e32 v63, v63
	v_cvt_i32_f32_e32 v64, v65
	v_fma_f32 v58, -v58, v62, v61
	v_div_fmas_f32 v58, v58, v59, v62
	v_div_fixup_f32 v50, v58, v52, v50
	v_ldexp_f32 v53, v63, v64
	v_cndmask_b32_e64 v53, 0, v53, s[4:5]
	v_cmp_ngt_f32_e64 s[4:5], s78, v56
	v_mul_f32_e32 v49, v55, v49
	s_nop 0
	v_cndmask_b32_e64 v53, v97, v53, s[4:5]
	v_add_f32_e32 v53, 1.0, v53
	v_div_scale_f32 v56, s[4:5], v53, v53, v51
	v_rcp_f32_e32 v61, v56
	v_cmp_nlt_f32_e64 s[4:5], s77, v60
	v_fma_f32 v52, -v56, v61, 1.0
	v_fmac_f32_e32 v61, v52, v61
	v_div_scale_f32 v52, vcc, v51, v53, v51
	v_mul_f32_e32 v58, v52, v61
	v_fma_f32 v59, -v56, v58, v52
	v_fmac_f32_e32 v58, v59, v61
	v_mul_f32_e32 v59, 0xbfb8aa3b, v60
	v_fma_f32 v62, v60, s76, -v59
	v_rndne_f32_e32 v63, v59
	v_fmac_f32_e32 v62, 0xb2a5705f, v60
	v_sub_f32_e32 v59, v59, v63
	v_add_f32_e32 v59, v59, v62
	v_exp_f32_e32 v59, v59
	v_cvt_i32_f32_e32 v62, v63
	v_fma_f32 v52, -v56, v58, v52
	v_div_fmas_f32 v52, v52, v61, v58
	v_div_fixup_f32 v51, v52, v53, v51
	v_ldexp_f32 v54, v59, v62
	v_cndmask_b32_e64 v54, 0, v54, s[4:5]
	v_cmp_ngt_f32_e64 s[4:5], s78, v60
	s_nop 1
	v_cndmask_b32_e64 v54, v97, v54, s[4:5]
	v_add_f32_e32 v54, 1.0, v54
	v_div_scale_f32 v56, s[4:5], v54, v54, v48
	v_rcp_f32_e32 v59, v56
	v_cmp_nlt_f32_e64 s[4:5], s77, v57
	v_fma_f32 v52, -v56, v59, 1.0
	v_fmac_f32_e32 v59, v52, v59
	v_div_scale_f32 v52, vcc, v48, v54, v48
	v_mul_f32_e32 v53, v52, v59
	v_fma_f32 v58, -v56, v53, v52
	v_fmac_f32_e32 v53, v58, v59
	v_mul_f32_e32 v58, 0xbfb8aa3b, v57
	v_fma_f32 v60, v57, s76, -v58
	v_rndne_f32_e32 v61, v58
	v_fmac_f32_e32 v60, 0xb2a5705f, v57
	v_sub_f32_e32 v58, v58, v61
	v_add_f32_e32 v58, v58, v60
	v_exp_f32_e32 v58, v58
	v_cvt_i32_f32_e32 v60, v61
	v_fma_f32 v52, -v56, v53, v52
	v_div_fmas_f32 v52, v52, v59, v53
	v_div_fixup_f32 v48, v52, v54, v48
	v_ldexp_f32 v55, v58, v60
	v_cndmask_b32_e64 v55, 0, v55, s[4:5]
	v_cmp_ngt_f32_e64 s[4:5], s78, v57
	s_nop 1
	v_cndmask_b32_e64 v55, v97, v55, s[4:5]
	v_add_f32_e32 v55, 1.0, v55
	v_div_scale_f32 v56, s[4:5], v55, v55, v49
	v_rcp_f32_e32 v57, v56
	s_nop 0
	v_fma_f32 v52, -v56, v57, 1.0
	v_fmac_f32_e32 v57, v52, v57
	v_div_scale_f32 v52, vcc, v49, v55, v49
	v_mul_f32_e32 v53, v52, v57
	v_fma_f32 v54, -v56, v53, v52
	v_fmac_f32_e32 v53, v54, v57
	v_fma_f32 v52, -v56, v53, v52
	v_div_fmas_f32 v52, v52, v57, v53
	v_div_fixup_f32 v49, v52, v55, v49
	v_cvt_pk_bf16_f32 v54, v50, v51
	v_cvt_pk_bf16_f32 v55, v48, v49
	v_or_b32_e32 v48, 0xa0, v66
	v_mov_b32_e32 v49, v67
	v_lshl_add_u64 v[48:49], v[72:73], 0, v[48:49]
	v_mov_b32_e32 v52, v204
	v_mov_b32_e32 v53, v205
	s_nop 0
	s_waitcnt vmcnt(12)
	v_mov_b32_e32 v48, v140
	v_mov_b32_e32 v49, v141
	v_mov_b32_e32 v50, v142
	v_mov_b32_e32 v51, v143
	s_nop 0
	v_lshlrev_b32_e32 v56, 16, v52
	v_mul_f32_e32 v57, 0xbfb8aa3b, v56
	v_fma_f32 v58, v56, s76, -v57
	v_rndne_f32_e32 v59, v57
	v_fmac_f32_e32 v58, 0xb2a5705f, v56
	v_sub_f32_e32 v57, v57, v59
	v_add_f32_e32 v57, v57, v58
	v_exp_f32_e32 v57, v57
	v_cvt_i32_f32_e32 v58, v59
	s_nop 0
	v_mul_f32_e32 v46, v48, v46
	v_cmp_nlt_f32_e32 vcc, s77, v56
	v_and_b32_e32 v52, 0xffff0000, v52
	v_ldexp_f32 v48, v57, v58
	v_cndmask_b32_e32 v48, 0, v48, vcc
	v_cmp_ngt_f32_e32 vcc, s78, v56
	v_mul_f32_e32 v47, v49, v47
	v_lshlrev_b32_e32 v58, 16, v53
	v_cndmask_b32_e32 v48, v97, v48, vcc
	v_add_f32_e32 v48, 1.0, v48
	v_div_scale_f32 v56, s[4:5], v48, v48, v46
	v_rcp_f32_e32 v57, v56
	v_cmp_nlt_f32_e64 s[4:5], s77, v52
	v_mul_f32_e32 v44, v50, v44
	v_and_b32_e32 v53, 0xffff0000, v53
	v_fma_f32 v59, -v56, v57, 1.0
	v_fmac_f32_e32 v57, v59, v57
	v_div_scale_f32 v59, vcc, v46, v48, v46
	v_mul_f32_e32 v60, v59, v57
	v_fma_f32 v61, -v56, v60, v59
	v_fmac_f32_e32 v60, v61, v57
	v_mul_f32_e32 v61, 0xbfb8aa3b, v52
	v_fma_f32 v62, v52, s76, -v61
	v_rndne_f32_e32 v63, v61
	v_fmac_f32_e32 v62, 0xb2a5705f, v52
	v_sub_f32_e32 v61, v61, v63
	v_add_f32_e32 v61, v61, v62
	v_exp_f32_e32 v61, v61
	v_cvt_i32_f32_e32 v62, v63
	v_fma_f32 v56, -v56, v60, v59
	v_div_fmas_f32 v56, v56, v57, v60
	v_div_fixup_f32 v46, v56, v48, v46
	v_ldexp_f32 v49, v61, v62
	v_cndmask_b32_e64 v49, 0, v49, s[4:5]
	v_cmp_ngt_f32_e64 s[4:5], s78, v52
	v_mul_f32_e32 v45, v51, v45
	s_nop 0
	v_cndmask_b32_e64 v49, v97, v49, s[4:5]
	v_add_f32_e32 v49, 1.0, v49
	v_div_scale_f32 v52, s[4:5], v49, v49, v47
	v_rcp_f32_e32 v59, v52
	v_cmp_nlt_f32_e64 s[4:5], s77, v58
	v_fma_f32 v48, -v52, v59, 1.0
; __device__ __forceinline__ unsigned cvt_pk_bf16(float lo, float hi) { unsigned r; asm volatile("v_cvt_pk_bf16_f32 %0, %1, %2" : "=v"(r) : "v"(lo), "v"(hi)); return r; }
; __device__ __forceinline__ void mlstm_D(LAS unsigned char* lds, int c, int h, const bf16_t* Z, const float* gi, const float* bcum, const float* marr, const bf16_t* CST, const float* NST,
;                                         const float* hgain, bf16_t* YCAT) {
;     ...
;         for (int n = 0; n < 2; ++n) { const int col = h * DH + 16 * (j + n) + 4 * fq;
;             const f32x4 gn = *(const f32x4*)(hgain + col); const u32x2 ov = *(const u32x2*)(Z + trow * EVN + 4096 + col);
;             const float o0 = bf_lo(ov.x), o1 = bf_hi(ov.x), o2 = bf_lo(ov.y), o3 = bf_hi(ov.y);
;             const float y0 = acc[j + n][0] * rs * gn[0] / (1.0f + expf(-o0)), y1 = acc[j + n][1] * rs * gn[1] / (1.0f + expf(-o1));
;             const float y2 = acc[j + n][2] * rs * gn[2] / (1.0f + expf(-o2)), y3 = acc[j + n][3] * rs * gn[3] / (1.0f + expf(-o3));
;             ab[n].x = cvt_pk_bf16(y0, y1); ab[n].y = cvt_pk_bf16(y2, y3); }
;         const bool odd = fq & 1; const u32x2 give = odd ? ab[0] : ab[1];
;         u32x2 got; got.x = (unsigned)__shfl_xor((int)give.x, 16); got.y = (unsigned)__shfl_xor((int)give.y, 16);
;         u32x4 w; if (odd) { w.x = got.x; w.y = got.y; w.z = ab[1].x; w.w = ab[1].y; } else { w.x = ab[0].x; w.y = ab[0].y; w.z = got.x; w.w = got.y; }
;         *(u32x4*)(YCAT + trow * D + 1024 + h * DH + 16 * (j + (odd ? 1 : 0)) + 4 * (fq & 2)) = w; if ((j & 3) == 2) asm volatile("" ::: "memory"); }
	v_fmac_f32_e32 v59, v48, v59
	v_div_scale_f32 v48, vcc, v47, v49, v47
	v_mul_f32_e32 v56, v48, v59
	v_fma_f32 v57, -v52, v56, v48
	v_fmac_f32_e32 v56, v57, v59
	v_mul_f32_e32 v57, 0xbfb8aa3b, v58
	v_fma_f32 v60, v58, s76, -v57
	v_rndne_f32_e32 v61, v57
	v_fmac_f32_e32 v60, 0xb2a5705f, v58
	v_sub_f32_e32 v57, v57, v61
	v_add_f32_e32 v57, v57, v60
	v_exp_f32_e32 v57, v57
	v_cvt_i32_f32_e32 v60, v61
	v_fma_f32 v48, -v52, v56, v48
	v_div_fmas_f32 v48, v48, v59, v56
	v_div_fixup_f32 v47, v48, v49, v47
	v_ldexp_f32 v50, v57, v60
	v_cndmask_b32_e64 v50, 0, v50, s[4:5]
	v_cmp_ngt_f32_e64 s[4:5], s78, v58
	v_cvt_pk_bf16_f32 v46, v46, v47
	s_nop 1
	v_cndmask_b32_e64 v50, v97, v50, s[4:5]
	v_add_f32_e32 v50, 1.0, v50
	v_div_scale_f32 v52, s[4:5], v50, v50, v44
	v_rcp_f32_e32 v57, v52
	v_cmp_nlt_f32_e64 s[4:5], s77, v53
	v_fma_f32 v48, -v52, v57, 1.0
	v_fmac_f32_e32 v57, v48, v57
	v_div_scale_f32 v48, vcc, v44, v50, v44
	v_mul_f32_e32 v49, v48, v57
	v_fma_f32 v56, -v52, v49, v48
	v_fmac_f32_e32 v49, v56, v57
	v_mul_f32_e32 v56, 0xbfb8aa3b, v53
	v_fma_f32 v58, v53, s76, -v56
	v_rndne_f32_e32 v59, v56
	v_fmac_f32_e32 v58, 0xb2a5705f, v53
	v_sub_f32_e32 v56, v56, v59
	v_add_f32_e32 v56, v56, v58
	v_exp_f32_e32 v56, v56
	v_cvt_i32_f32_e32 v58, v59
	v_fma_f32 v48, -v52, v49, v48
	v_div_fmas_f32 v48, v48, v57, v49
	v_div_fixup_f32 v44, v48, v50, v44
	v_ldexp_f32 v51, v56, v58
	v_cndmask_b32_e64 v51, 0, v51, s[4:5]
	v_cmp_ngt_f32_e64 s[4:5], s78, v53
	s_nop 1
	v_cndmask_b32_e64 v51, v97, v51, s[4:5]
	v_add_f32_e32 v51, 1.0, v51
	v_div_scale_f32 v52, s[4:5], v51, v51, v45
	v_rcp_f32_e32 v53, v52
	s_nop 0
	v_fma_f32 v48, -v52, v53, 1.0
	v_fmac_f32_e32 v53, v48, v53
	v_div_scale_f32 v48, vcc, v45, v51, v45
	v_mul_f32_e32 v49, v48, v53
	v_fma_f32 v50, -v52, v49, v48
	v_fmac_f32_e32 v49, v50, v53
	v_fma_f32 v48, -v52, v49, v48
	v_div_fmas_f32 v48, v48, v53, v49
	v_div_fixup_f32 v45, v48, v51, v45
	v_cvt_pk_bf16_f32 v45, v44, v45
	v_cndmask_b32_e64 v44, v54, v46, s[2:3]
	v_cndmask_b32_e64 v47, v55, v45, s[2:3]
	ds_bpermute_b32 v44, v98, v44
	ds_bpermute_b32 v48, v98, v47
	s_waitcnt lgkmcnt(1)
	v_cndmask_b32_e64 v46, v46, v44, s[2:3]
	v_cndmask_b32_e64 v44, v44, v54, s[2:3]
	s_waitcnt lgkmcnt(0)
	v_cndmask_b32_e64 v47, v45, v48, s[2:3]
	v_cndmask_b32_e64 v45, v48, v55, s[2:3]
	global_store_dwordx4 v[18:19], v[44:47], off offset:128
	s_nop 1
	v_or_b32_e32 v44, 0xc0, v66
	v_mov_b32_e32 v45, v67
	v_lshl_add_u64 v[44:45], v[72:73], 0, v[44:45]
	v_mov_b32_e32 v48, v206
	v_mov_b32_e32 v49, v207
	s_nop 0
	s_waitcnt vmcnt(12)
	v_mov_b32_e32 v44, v144
	v_mov_b32_e32 v45, v145
	v_mov_b32_e32 v46, v146
	v_mov_b32_e32 v47, v147
	s_nop 0
	v_lshlrev_b32_e32 v50, 16, v48
	v_mul_f32_e32 v51, 0xbfb8aa3b, v50
	v_fma_f32 v52, v50, s76, -v51
	v_rndne_f32_e32 v53, v51
	v_fmac_f32_e32 v52, 0xb2a5705f, v50
	v_sub_f32_e32 v51, v51, v53
	v_add_f32_e32 v51, v51, v52
	v_exp_f32_e32 v51, v51
	v_cvt_i32_f32_e32 v52, v53
	s_nop 0
	v_mul_f32_e32 v42, v42, v44
	v_cmp_nlt_f32_e32 vcc, s77, v50
	v_and_b32_e32 v48, 0xffff0000, v48
	v_ldexp_f32 v44, v51, v52
	v_cndmask_b32_e32 v44, 0, v44, vcc
	v_cmp_ngt_f32_e32 vcc, s78, v50
	v_mul_f32_e32 v43, v43, v45
	v_lshlrev_b32_e32 v52, 16, v49
	v_cndmask_b32_e32 v44, v97, v44, vcc
	v_add_f32_e32 v44, 1.0, v44
	v_div_scale_f32 v50, s[4:5], v44, v44, v42
	v_rcp_f32_e32 v51, v50
	v_cmp_nlt_f32_e64 s[4:5], s77, v48
	v_mul_f32_e32 v40, v40, v46
	v_and_b32_e32 v49, 0xffff0000, v49
	v_fma_f32 v53, -v50, v51, 1.0
	v_fmac_f32_e32 v51, v53, v51
	v_div_scale_f32 v53, vcc, v42, v44, v42
	v_mul_f32_e32 v54, v53, v51
	v_fma_f32 v55, -v50, v54, v53
	v_fmac_f32_e32 v54, v55, v51
	v_mul_f32_e32 v55, 0xbfb8aa3b, v48
	v_fma_f32 v56, v48, s76, -v55
	v_rndne_f32_e32 v57, v55
	v_fmac_f32_e32 v56, 0xb2a5705f, v48
	v_sub_f32_e32 v55, v55, v57
	v_add_f32_e32 v55, v55, v56
	v_exp_f32_e32 v55, v55
	v_cvt_i32_f32_e32 v56, v57
	v_fma_f32 v50, -v50, v54, v53
	v_div_fmas_f32 v50, v50, v51, v54
	v_div_fixup_f32 v42, v50, v44, v42
	v_ldexp_f32 v45, v55, v56
	v_cndmask_b32_e64 v45, 0, v45, s[4:5]
	v_cmp_ngt_f32_e64 s[4:5], s78, v48
	v_mul_f32_e32 v41, v41, v47
	s_nop 0
	v_cndmask_b32_e64 v45, v97, v45, s[4:5]
	v_add_f32_e32 v45, 1.0, v45
	v_div_scale_f32 v48, s[4:5], v45, v45, v43
	v_rcp_f32_e32 v53, v48
	v_cmp_nlt_f32_e64 s[4:5], s77, v52
	v_fma_f32 v44, -v48, v53, 1.0
	v_fmac_f32_e32 v53, v44, v53
	v_div_scale_f32 v44, vcc, v43, v45, v43
	v_mul_f32_e32 v50, v44, v53
	v_fma_f32 v51, -v48, v50, v44
	v_fmac_f32_e32 v50, v51, v53
	v_mul_f32_e32 v51, 0xbfb8aa3b, v52
	v_fma_f32 v54, v52, s76, -v51
	v_rndne_f32_e32 v55, v51
	v_fmac_f32_e32 v54, 0xb2a5705f, v52
	v_sub_f32_e32 v51, v51, v55
	v_add_f32_e32 v51, v51, v54
	v_exp_f32_e32 v51, v51
	v_cvt_i32_f32_e32 v54, v55
	v_fma_f32 v44, -v48, v50, v44
	v_div_fmas_f32 v44, v44, v53, v50
	v_div_fixup_f32 v43, v44, v45, v43
	v_ldexp_f32 v46, v51, v54
	v_cndmask_b32_e64 v46, 0, v46, s[4:5]
	v_cmp_ngt_f32_e64 s[4:5], s78, v52
	s_nop 1
	v_cndmask_b32_e64 v46, v97, v46, s[4:5]
	v_add_f32_e32 v46, 1.0, v46
	v_div_scale_f32 v48, s[4:5], v46, v46, v40
	v_rcp_f32_e32 v51, v48
	v_cmp_nlt_f32_e64 s[4:5], s77, v49
	v_fma_f32 v44, -v48, v51, 1.0
	v_fmac_f32_e32 v51, v44, v51
	v_div_scale_f32 v44, vcc, v40, v46, v40
	v_mul_f32_e32 v45, v44, v51
	v_fma_f32 v50, -v48, v45, v44
	v_fmac_f32_e32 v45, v50, v51
	v_mul_f32_e32 v50, 0xbfb8aa3b, v49
	v_fma_f32 v52, v49, s76, -v50
	v_rndne_f32_e32 v53, v50
	v_fmac_f32_e32 v52, 0xb2a5705f, v49
	v_sub_f32_e32 v50, v50, v53
	v_add_f32_e32 v50, v50, v52
	v_exp_f32_e32 v50, v50
	v_cvt_i32_f32_e32 v52, v53
	v_fma_f32 v44, -v48, v45, v44
	v_div_fmas_f32 v44, v44, v51, v45
	v_div_fixup_f32 v40, v44, v46, v40
	v_ldexp_f32 v47, v50, v52
	v_cndmask_b32_e64 v47, 0, v47, s[4:5]
	v_cmp_ngt_f32_e64 s[4:5], s78, v49
	s_nop 1
	v_cndmask_b32_e64 v47, v97, v47, s[4:5]
	v_add_f32_e32 v47, 1.0, v47
	v_div_scale_f32 v48, s[4:5], v47, v47, v41
	v_rcp_f32_e32 v49, v48
	s_nop 0
	v_fma_f32 v44, -v48, v49, 1.0
	v_fmac_f32_e32 v49, v44, v49
	v_div_scale_f32 v44, vcc, v41, v47, v41
	v_mul_f32_e32 v45, v44, v49
	v_fma_f32 v46, -v48, v45, v44
	v_fmac_f32_e32 v45, v46, v49
	v_fma_f32 v44, -v48, v45, v44
	v_div_fmas_f32 v44, v44, v49, v45
	v_div_fixup_f32 v41, v44, v47, v41
	v_cvt_pk_bf16_f32 v46, v42, v43
	v_cvt_pk_bf16_f32 v47, v40, v41
	v_or_b32_e32 v40, 0xe0, v66
	v_mov_b32_e32 v41, v67
	v_lshl_add_u64 v[40:41], v[72:73], 0, v[40:41]
	v_mov_b32_e32 v44, v208
	v_mov_b32_e32 v45, v209
	s_nop 0
	s_waitcnt vmcnt(11)
; __device__ __forceinline__ unsigned cvt_pk_bf16(float lo, float hi) { unsigned r; asm volatile("v_cvt_pk_bf16_f32 %0, %1, %2" : "=v"(r) : "v"(lo), "v"(hi)); return r; }
; __device__ __forceinline__ void mlstm_D(LAS unsigned char* lds, int c, int h, const bf16_t* Z, const float* gi, const float* bcum, const float* marr, const bf16_t* CST, const float* NST,
;                                         const float* hgain, bf16_t* YCAT) {
;     ...
;         for (int n = 0; n < 2; ++n) { const int col = h * DH + 16 * (j + n) + 4 * fq;
;             const f32x4 gn = *(const f32x4*)(hgain + col); const u32x2 ov = *(const u32x2*)(Z + trow * EVN + 4096 + col);
;             const float o0 = bf_lo(ov.x), o1 = bf_hi(ov.x), o2 = bf_lo(ov.y), o3 = bf_hi(ov.y);
;             const float y0 = acc[j + n][0] * rs * gn[0] / (1.0f + expf(-o0)), y1 = acc[j + n][1] * rs * gn[1] / (1.0f + expf(-o1));
;             const float y2 = acc[j + n][2] * rs * gn[2] / (1.0f + expf(-o2)), y3 = acc[j + n][3] * rs * gn[3] / (1.0f + expf(-o3));
;             ab[n].x = cvt_pk_bf16(y0, y1); ab[n].y = cvt_pk_bf16(y2, y3); }
;         const bool odd = fq & 1; const u32x2 give = odd ? ab[0] : ab[1];
;         u32x2 got; got.x = (unsigned)__shfl_xor((int)give.x, 16); got.y = (unsigned)__shfl_xor((int)give.y, 16);
;         u32x4 w; if (odd) { w.x = got.x; w.y = got.y; w.z = ab[1].x; w.w = ab[1].y; } else { w.x = ab[0].x; w.y = ab[0].y; w.z = got.x; w.w = got.y; }
;         *(u32x4*)(YCAT + trow * D + 1024 + h * DH + 16 * (j + (odd ? 1 : 0)) + 4 * (fq & 2)) = w; if ((j & 3) == 2) asm volatile("" ::: "memory"); }
	v_mov_b32_e32 v40, v148
	v_mov_b32_e32 v41, v149
	v_mov_b32_e32 v42, v150
	v_mov_b32_e32 v43, v151
	s_nop 0
	v_lshlrev_b32_e32 v48, 16, v44
	v_mul_f32_e32 v49, 0xbfb8aa3b, v48
	v_fma_f32 v50, v48, s76, -v49
	v_rndne_f32_e32 v51, v49
	v_fmac_f32_e32 v50, 0xb2a5705f, v48
	v_sub_f32_e32 v49, v49, v51
	v_add_f32_e32 v49, v49, v50
	v_exp_f32_e32 v49, v49
	v_cvt_i32_f32_e32 v50, v51
	s_nop 0
	v_mul_f32_e32 v38, v38, v40
	v_cmp_nlt_f32_e32 vcc, s77, v48
	v_and_b32_e32 v44, 0xffff0000, v44
	v_ldexp_f32 v40, v49, v50
	v_cndmask_b32_e32 v40, 0, v40, vcc
	v_cmp_ngt_f32_e32 vcc, s78, v48
	v_mul_f32_e32 v39, v39, v41
	v_lshlrev_b32_e32 v50, 16, v45
	v_cndmask_b32_e32 v40, v97, v40, vcc
	v_add_f32_e32 v40, 1.0, v40
	v_div_scale_f32 v48, s[4:5], v40, v40, v38
	v_rcp_f32_e32 v49, v48
	v_cmp_nlt_f32_e64 s[4:5], s77, v44
	v_mul_f32_e32 v36, v36, v42
	v_and_b32_e32 v45, 0xffff0000, v45
	v_fma_f32 v51, -v48, v49, 1.0
	v_fmac_f32_e32 v49, v51, v49
	v_div_scale_f32 v51, vcc, v38, v40, v38
	v_mul_f32_e32 v52, v51, v49
	v_fma_f32 v53, -v48, v52, v51
	v_fmac_f32_e32 v52, v53, v49
	v_mul_f32_e32 v53, 0xbfb8aa3b, v44
	v_fma_f32 v54, v44, s76, -v53
	v_rndne_f32_e32 v55, v53
	v_fmac_f32_e32 v54, 0xb2a5705f, v44
	v_sub_f32_e32 v53, v53, v55
	v_add_f32_e32 v53, v53, v54
	v_exp_f32_e32 v53, v53
	v_cvt_i32_f32_e32 v54, v55
	v_fma_f32 v48, -v48, v52, v51
	v_div_fmas_f32 v48, v48, v49, v52
	v_div_fixup_f32 v38, v48, v40, v38
	v_ldexp_f32 v41, v53, v54
	v_cndmask_b32_e64 v41, 0, v41, s[4:5]
	v_cmp_ngt_f32_e64 s[4:5], s78, v44
	v_mul_f32_e32 v37, v37, v43
	s_nop 0
	v_cndmask_b32_e64 v41, v97, v41, s[4:5]
	v_add_f32_e32 v41, 1.0, v41
	v_div_scale_f32 v44, s[4:5], v41, v41, v39
	v_rcp_f32_e32 v51, v44
	v_cmp_nlt_f32_e64 s[4:5], s77, v50
	v_fma_f32 v40, -v44, v51, 1.0
	v_fmac_f32_e32 v51, v40, v51
	v_div_scale_f32 v40, vcc, v39, v41, v39
	v_mul_f32_e32 v48, v40, v51
	v_fma_f32 v49, -v44, v48, v40
	v_fmac_f32_e32 v48, v49, v51
	v_mul_f32_e32 v49, 0xbfb8aa3b, v50
	v_fma_f32 v52, v50, s76, -v49
	v_rndne_f32_e32 v53, v49
	v_fmac_f32_e32 v52, 0xb2a5705f, v50
	v_sub_f32_e32 v49, v49, v53
	v_add_f32_e32 v49, v49, v52
	v_exp_f32_e32 v49, v49
	v_cvt_i32_f32_e32 v52, v53
	v_fma_f32 v40, -v44, v48, v40
	v_div_fmas_f32 v40, v40, v51, v48
	v_div_fixup_f32 v39, v40, v41, v39
	v_ldexp_f32 v42, v49, v52
	v_cndmask_b32_e64 v42, 0, v42, s[4:5]
	v_cmp_ngt_f32_e64 s[4:5], s78, v50
	v_cvt_pk_bf16_f32 v38, v38, v39
	s_nop 1
	v_cndmask_b32_e64 v42, v97, v42, s[4:5]
	v_add_f32_e32 v42, 1.0, v42
	v_div_scale_f32 v44, s[4:5], v42, v42, v36
	v_rcp_f32_e32 v49, v44
	v_cmp_nlt_f32_e64 s[4:5], s77, v45
	v_fma_f32 v40, -v44, v49, 1.0
	v_fmac_f32_e32 v49, v40, v49
	v_div_scale_f32 v40, vcc, v36, v42, v36
	v_mul_f32_e32 v41, v40, v49
	v_fma_f32 v48, -v44, v41, v40
	v_fmac_f32_e32 v41, v48, v49
	v_mul_f32_e32 v48, 0xbfb8aa3b, v45
	v_fma_f32 v50, v45, s76, -v48
	v_rndne_f32_e32 v51, v48
	v_fmac_f32_e32 v50, 0xb2a5705f, v45
	v_sub_f32_e32 v48, v48, v51
	v_add_f32_e32 v48, v48, v50
	v_exp_f32_e32 v48, v48
	v_cvt_i32_f32_e32 v50, v51
	v_fma_f32 v40, -v44, v41, v40
	v_div_fmas_f32 v40, v40, v49, v41
	v_div_fixup_f32 v36, v40, v42, v36
	v_ldexp_f32 v43, v48, v50
	v_cndmask_b32_e64 v43, 0, v43, s[4:5]
	v_cmp_ngt_f32_e64 s[4:5], s78, v45
	s_nop 1
	v_cndmask_b32_e64 v43, v97, v43, s[4:5]
	v_add_f32_e32 v43, 1.0, v43
	v_div_scale_f32 v44, s[4:5], v43, v43, v37
	v_rcp_f32_e32 v45, v44
	s_nop 0
	v_fma_f32 v40, -v44, v45, 1.0
	v_fmac_f32_e32 v45, v40, v45
	v_div_scale_f32 v40, vcc, v37, v43, v37
	v_mul_f32_e32 v41, v40, v45
	v_fma_f32 v42, -v44, v41, v40
	v_fmac_f32_e32 v41, v42, v45
	v_fma_f32 v40, -v44, v41, v40
	v_div_fmas_f32 v40, v40, v45, v41
	v_div_fixup_f32 v37, v40, v43, v37
	v_cvt_pk_bf16_f32 v37, v36, v37
	v_cndmask_b32_e64 v36, v46, v38, s[2:3]
	v_cndmask_b32_e64 v39, v47, v37, s[2:3]
	ds_bpermute_b32 v36, v98, v36
	ds_bpermute_b32 v40, v98, v39
	s_waitcnt lgkmcnt(1)
	v_cndmask_b32_e64 v38, v38, v36, s[2:3]
	v_cndmask_b32_e64 v36, v36, v46, s[2:3]
	s_waitcnt lgkmcnt(0)
	v_cndmask_b32_e64 v39, v37, v40, s[2:3]
	v_cndmask_b32_e64 v37, v40, v47, s[2:3]
	global_store_dwordx4 v[18:19], v[36:39], off offset:192
	s_nop 1
	v_or_b32_e32 v36, 0x100, v66
	v_mov_b32_e32 v37, v67
	v_lshl_add_u64 v[36:37], v[72:73], 0, v[36:37]
	v_mov_b32_e32 v40, v210
	v_mov_b32_e32 v41, v211
	s_nop 0
	s_waitcnt vmcnt(11)
; __device__ __forceinline__ unsigned cvt_pk_bf16(float lo, float hi) { unsigned r; asm volatile("v_cvt_pk_bf16_f32 %0, %1, %2" : "=v"(r) : "v"(lo), "v"(hi)); return r; }
; __device__ __forceinline__ void mlstm_D(LAS unsigned char* lds, int c, int h, const bf16_t* Z, const float* gi, const float* bcum, const float* marr, const bf16_t* CST, const float* NST,
;                                         const float* hgain, bf16_t* YCAT) {
;     ...
;         for (int n = 0; n < 2; ++n) { const int col = h * DH + 16 * (j + n) + 4 * fq;
;             const f32x4 gn = *(const f32x4*)(hgain + col); const u32x2 ov = *(const u32x2*)(Z + trow * EVN + 4096 + col);
;             const float o0 = bf_lo(ov.x), o1 = bf_hi(ov.x), o2 = bf_lo(ov.y), o3 = bf_hi(ov.y);
;             const float y0 = acc[j + n][0] * rs * gn[0] / (1.0f + expf(-o0)), y1 = acc[j + n][1] * rs * gn[1] / (1.0f + expf(-o1));
;             const float y2 = acc[j + n][2] * rs * gn[2] / (1.0f + expf(-o2)), y3 = acc[j + n][3] * rs * gn[3] / (1.0f + expf(-o3));
;             ab[n].x = cvt_pk_bf16(y0, y1); ab[n].y = cvt_pk_bf16(y2, y3); }
;         const bool odd = fq & 1; const u32x2 give = odd ? ab[0] : ab[1];
;         u32x2 got; got.x = (unsigned)__shfl_xor((int)give.x, 16); got.y = (unsigned)__shfl_xor((int)give.y, 16);
;         u32x4 w; if (odd) { w.x = got.x; w.y = got.y; w.z = ab[1].x; w.w = ab[1].y; } else { w.x = ab[0].x; w.y = ab[0].y; w.z = got.x; w.w = got.y; }
;         *(u32x4*)(YCAT + trow * D + 1024 + h * DH + 16 * (j + (odd ? 1 : 0)) + 4 * (fq & 2)) = w; if ((j & 3) == 2) asm volatile("" ::: "memory"); }
	v_mov_b32_e32 v36, v152
	v_mov_b32_e32 v37, v153
	v_mov_b32_e32 v38, v154
	v_mov_b32_e32 v39, v155
	s_nop 0
	v_lshlrev_b32_e32 v42, 16, v40
	v_mul_f32_e32 v43, 0xbfb8aa3b, v42
	v_fma_f32 v44, v42, s76, -v43
	v_rndne_f32_e32 v45, v43
	v_fmac_f32_e32 v44, 0xb2a5705f, v42
	v_sub_f32_e32 v43, v43, v45
	v_add_f32_e32 v43, v43, v44
	v_exp_f32_e32 v43, v43
	v_cvt_i32_f32_e32 v44, v45
	s_nop 0
	v_mul_f32_e32 v34, v34, v36
	v_cmp_nlt_f32_e32 vcc, s77, v42
	v_and_b32_e32 v40, 0xffff0000, v40
	v_ldexp_f32 v36, v43, v44
	v_cndmask_b32_e32 v36, 0, v36, vcc
	v_cmp_ngt_f32_e32 vcc, s78, v42
	v_mul_f32_e32 v35, v35, v37
	v_lshlrev_b32_e32 v44, 16, v41
	v_cndmask_b32_e32 v36, v97, v36, vcc
	v_add_f32_e32 v36, 1.0, v36
	v_div_scale_f32 v42, s[4:5], v36, v36, v34
	v_rcp_f32_e32 v43, v42
	v_cmp_nlt_f32_e64 s[4:5], s77, v40
	v_mul_f32_e32 v32, v32, v38
	v_and_b32_e32 v41, 0xffff0000, v41
	v_fma_f32 v45, -v42, v43, 1.0
	v_fmac_f32_e32 v43, v45, v43
	v_div_scale_f32 v45, vcc, v34, v36, v34
	v_mul_f32_e32 v46, v45, v43
	v_fma_f32 v47, -v42, v46, v45
	v_fmac_f32_e32 v46, v47, v43
	v_mul_f32_e32 v47, 0xbfb8aa3b, v40
	v_fma_f32 v48, v40, s76, -v47
	v_rndne_f32_e32 v49, v47
	v_fmac_f32_e32 v48, 0xb2a5705f, v40
	v_sub_f32_e32 v47, v47, v49
	v_add_f32_e32 v47, v47, v48
	v_exp_f32_e32 v47, v47
	v_cvt_i32_f32_e32 v48, v49
	v_fma_f32 v42, -v42, v46, v45
	v_div_fmas_f32 v42, v42, v43, v46
	v_div_fixup_f32 v34, v42, v36, v34
	v_ldexp_f32 v37, v47, v48
	v_cndmask_b32_e64 v37, 0, v37, s[4:5]
	v_cmp_ngt_f32_e64 s[4:5], s78, v40
	v_mul_f32_e32 v33, v33, v39
	s_nop 0
	v_cndmask_b32_e64 v37, v97, v37, s[4:5]
	v_add_f32_e32 v37, 1.0, v37
	v_div_scale_f32 v40, s[4:5], v37, v37, v35
	v_rcp_f32_e32 v45, v40
	v_cmp_nlt_f32_e64 s[4:5], s77, v44
	v_fma_f32 v36, -v40, v45, 1.0
	v_fmac_f32_e32 v45, v36, v45
	v_div_scale_f32 v36, vcc, v35, v37, v35
	v_mul_f32_e32 v42, v36, v45
	v_fma_f32 v43, -v40, v42, v36
	v_fmac_f32_e32 v42, v43, v45
	v_mul_f32_e32 v43, 0xbfb8aa3b, v44
	v_fma_f32 v46, v44, s76, -v43
	v_rndne_f32_e32 v47, v43
	v_fmac_f32_e32 v46, 0xb2a5705f, v44
	v_sub_f32_e32 v43, v43, v47
	v_add_f32_e32 v43, v43, v46
	v_exp_f32_e32 v43, v43
	v_cvt_i32_f32_e32 v46, v47
	v_fma_f32 v36, -v40, v42, v36
	v_div_fmas_f32 v36, v36, v45, v42
	v_div_fixup_f32 v35, v36, v37, v35
	v_ldexp_f32 v38, v43, v46
	v_cndmask_b32_e64 v38, 0, v38, s[4:5]
	v_cmp_ngt_f32_e64 s[4:5], s78, v44
	s_nop 1
	v_cndmask_b32_e64 v38, v97, v38, s[4:5]
	v_add_f32_e32 v38, 1.0, v38
	v_div_scale_f32 v40, s[4:5], v38, v38, v32
	v_rcp_f32_e32 v43, v40
	v_cmp_nlt_f32_e64 s[4:5], s77, v41
	v_fma_f32 v36, -v40, v43, 1.0
	v_fmac_f32_e32 v43, v36, v43
	v_div_scale_f32 v36, vcc, v32, v38, v32
	v_mul_f32_e32 v37, v36, v43
	v_fma_f32 v42, -v40, v37, v36
	v_fmac_f32_e32 v37, v42, v43
	v_mul_f32_e32 v42, 0xbfb8aa3b, v41
	v_fma_f32 v44, v41, s76, -v42
	v_rndne_f32_e32 v45, v42
	v_fmac_f32_e32 v44, 0xb2a5705f, v41
	v_sub_f32_e32 v42, v42, v45
	v_add_f32_e32 v42, v42, v44
	v_exp_f32_e32 v42, v42
	v_cvt_i32_f32_e32 v44, v45
	v_fma_f32 v36, -v40, v37, v36
	v_div_fmas_f32 v36, v36, v43, v37
	v_div_fixup_f32 v32, v36, v38, v32
	v_ldexp_f32 v39, v42, v44
	v_cndmask_b32_e64 v39, 0, v39, s[4:5]
	v_cmp_ngt_f32_e64 s[4:5], s78, v41
	s_nop 1
	v_cndmask_b32_e64 v39, v97, v39, s[4:5]
	v_add_f32_e32 v39, 1.0, v39
	v_div_scale_f32 v40, s[4:5], v39, v39, v33
	v_rcp_f32_e32 v41, v40
	s_nop 0
	v_fma_f32 v36, -v40, v41, 1.0
	v_fmac_f32_e32 v41, v36, v41
	v_div_scale_f32 v36, vcc, v33, v39, v33
	v_mul_f32_e32 v37, v36, v41
	v_fma_f32 v38, -v40, v37, v36
	v_fmac_f32_e32 v37, v38, v41
	v_fma_f32 v36, -v40, v37, v36
	v_div_fmas_f32 v36, v36, v41, v37
	v_div_fixup_f32 v33, v36, v39, v33
	v_cvt_pk_bf16_f32 v38, v34, v35
	v_cvt_pk_bf16_f32 v39, v32, v33
	v_or_b32_e32 v32, 0x120, v66
	v_mov_b32_e32 v33, v67
	v_lshl_add_u64 v[32:33], v[72:73], 0, v[32:33]
	v_mov_b32_e32 v36, v212
	v_mov_b32_e32 v37, v213
	s_nop 0
	s_waitcnt vmcnt(10)
	v_mov_b32_e32 v32, v156
	v_mov_b32_e32 v33, v157
	v_mov_b32_e32 v34, v158
	v_mov_b32_e32 v35, v159
	s_nop 0
	v_lshlrev_b32_e32 v40, 16, v36
	v_mul_f32_e32 v41, 0xbfb8aa3b, v40
	v_fma_f32 v42, v40, s76, -v41
	v_rndne_f32_e32 v43, v41
	v_fmac_f32_e32 v42, 0xb2a5705f, v40
	v_sub_f32_e32 v41, v41, v43
	v_add_f32_e32 v41, v41, v42
	v_exp_f32_e32 v41, v41
	v_cvt_i32_f32_e32 v42, v43
	s_nop 0
	v_mul_f32_e32 v30, v30, v32
	v_cmp_nlt_f32_e32 vcc, s77, v40
	v_and_b32_e32 v36, 0xffff0000, v36
	v_ldexp_f32 v32, v41, v42
	v_cndmask_b32_e32 v32, 0, v32, vcc
	v_cmp_ngt_f32_e32 vcc, s78, v40
	v_mul_f32_e32 v31, v31, v33
	v_lshlrev_b32_e32 v42, 16, v37
	v_cndmask_b32_e32 v32, v97, v32, vcc
	v_add_f32_e32 v32, 1.0, v32
	v_div_scale_f32 v40, s[4:5], v32, v32, v30
	v_rcp_f32_e32 v41, v40
	v_cmp_nlt_f32_e64 s[4:5], s77, v36
	v_mul_f32_e32 v28, v28, v34
	v_and_b32_e32 v37, 0xffff0000, v37
	v_fma_f32 v43, -v40, v41, 1.0
	v_fmac_f32_e32 v41, v43, v41
	v_div_scale_f32 v43, vcc, v30, v32, v30
	v_mul_f32_e32 v44, v43, v41
	v_fma_f32 v45, -v40, v44, v43
	v_fmac_f32_e32 v44, v45, v41
	v_mul_f32_e32 v45, 0xbfb8aa3b, v36
	v_fma_f32 v46, v36, s76, -v45
	v_rndne_f32_e32 v47, v45
	v_fmac_f32_e32 v46, 0xb2a5705f, v36
	v_sub_f32_e32 v45, v45, v47
	v_add_f32_e32 v45, v45, v46
	v_exp_f32_e32 v45, v45
	v_cvt_i32_f32_e32 v46, v47
	v_fma_f32 v40, -v40, v44, v43
	v_div_fmas_f32 v40, v40, v41, v44
	v_div_fixup_f32 v30, v40, v32, v30
	v_ldexp_f32 v33, v45, v46
	v_cndmask_b32_e64 v33, 0, v33, s[4:5]
	v_cmp_ngt_f32_e64 s[4:5], s78, v36
	v_mul_f32_e32 v29, v29, v35
	s_nop 0
	v_cndmask_b32_e64 v33, v97, v33, s[4:5]
	v_add_f32_e32 v33, 1.0, v33
	v_div_scale_f32 v36, s[4:5], v33, v33, v31
	v_rcp_f32_e32 v43, v36
	v_cmp_nlt_f32_e64 s[4:5], s77, v42
	v_fma_f32 v32, -v36, v43, 1.0
; __device__ __forceinline__ unsigned cvt_pk_bf16(float lo, float hi) { unsigned r; asm volatile("v_cvt_pk_bf16_f32 %0, %1, %2" : "=v"(r) : "v"(lo), "v"(hi)); return r; }
; __device__ __forceinline__ void mlstm_D(LAS unsigned char* lds, int c, int h, const bf16_t* Z, const float* gi, const float* bcum, const float* marr, const bf16_t* CST, const float* NST,
;                                         const float* hgain, bf16_t* YCAT) {
;     ...
;         for (int n = 0; n < 2; ++n) { const int col = h * DH + 16 * (j + n) + 4 * fq;
;             const f32x4 gn = *(const f32x4*)(hgain + col); const u32x2 ov = *(const u32x2*)(Z + trow * EVN + 4096 + col);
;             const float o0 = bf_lo(ov.x), o1 = bf_hi(ov.x), o2 = bf_lo(ov.y), o3 = bf_hi(ov.y);
;             const float y0 = acc[j + n][0] * rs * gn[0] / (1.0f + expf(-o0)), y1 = acc[j + n][1] * rs * gn[1] / (1.0f + expf(-o1));
;             const float y2 = acc[j + n][2] * rs * gn[2] / (1.0f + expf(-o2)), y3 = acc[j + n][3] * rs * gn[3] / (1.0f + expf(-o3));
;             ab[n].x = cvt_pk_bf16(y0, y1); ab[n].y = cvt_pk_bf16(y2, y3); }
;         const bool odd = fq & 1; const u32x2 give = odd ? ab[0] : ab[1];
;         u32x2 got; got.x = (unsigned)__shfl_xor((int)give.x, 16); got.y = (unsigned)__shfl_xor((int)give.y, 16);
;         u32x4 w; if (odd) { w.x = got.x; w.y = got.y; w.z = ab[1].x; w.w = ab[1].y; } else { w.x = ab[0].x; w.y = ab[0].y; w.z = got.x; w.w = got.y; }
;         *(u32x4*)(YCAT + trow * D + 1024 + h * DH + 16 * (j + (odd ? 1 : 0)) + 4 * (fq & 2)) = w; if ((j & 3) == 2) asm volatile("" ::: "memory"); }
	v_fmac_f32_e32 v43, v32, v43
	v_div_scale_f32 v32, vcc, v31, v33, v31
	v_mul_f32_e32 v40, v32, v43
	v_fma_f32 v41, -v36, v40, v32
	v_fmac_f32_e32 v40, v41, v43
	v_mul_f32_e32 v41, 0xbfb8aa3b, v42
	v_fma_f32 v44, v42, s76, -v41
	v_rndne_f32_e32 v45, v41
	v_fmac_f32_e32 v44, 0xb2a5705f, v42
	v_sub_f32_e32 v41, v41, v45
	v_add_f32_e32 v41, v41, v44
	v_exp_f32_e32 v41, v41
	v_cvt_i32_f32_e32 v44, v45
	v_fma_f32 v32, -v36, v40, v32
	v_div_fmas_f32 v32, v32, v43, v40
	v_div_fixup_f32 v31, v32, v33, v31
	v_ldexp_f32 v34, v41, v44
	v_cndmask_b32_e64 v34, 0, v34, s[4:5]
	v_cmp_ngt_f32_e64 s[4:5], s78, v42
	v_cvt_pk_bf16_f32 v30, v30, v31
	s_nop 1
	v_cndmask_b32_e64 v34, v97, v34, s[4:5]
	v_add_f32_e32 v34, 1.0, v34
	v_div_scale_f32 v36, s[4:5], v34, v34, v28
	v_rcp_f32_e32 v41, v36
	v_cmp_nlt_f32_e64 s[4:5], s77, v37
	v_fma_f32 v32, -v36, v41, 1.0
	v_fmac_f32_e32 v41, v32, v41
	v_div_scale_f32 v32, vcc, v28, v34, v28
	v_mul_f32_e32 v33, v32, v41
	v_fma_f32 v40, -v36, v33, v32
	v_fmac_f32_e32 v33, v40, v41
	v_mul_f32_e32 v40, 0xbfb8aa3b, v37
	v_fma_f32 v42, v37, s76, -v40
	v_rndne_f32_e32 v43, v40
	v_fmac_f32_e32 v42, 0xb2a5705f, v37
	v_sub_f32_e32 v40, v40, v43
	v_add_f32_e32 v40, v40, v42
	v_exp_f32_e32 v40, v40
	v_cvt_i32_f32_e32 v42, v43
	v_fma_f32 v32, -v36, v33, v32
	v_div_fmas_f32 v32, v32, v41, v33
	v_div_fixup_f32 v28, v32, v34, v28
	v_ldexp_f32 v35, v40, v42
	v_cndmask_b32_e64 v35, 0, v35, s[4:5]
	v_cmp_ngt_f32_e64 s[4:5], s78, v37
	s_nop 1
	v_cndmask_b32_e64 v35, v97, v35, s[4:5]
	v_add_f32_e32 v35, 1.0, v35
	v_div_scale_f32 v36, s[4:5], v35, v35, v29
	v_rcp_f32_e32 v37, v36
	s_nop 0
	v_fma_f32 v32, -v36, v37, 1.0
	v_fmac_f32_e32 v37, v32, v37
	v_div_scale_f32 v32, vcc, v29, v35, v29
	v_mul_f32_e32 v33, v32, v37
	v_fma_f32 v34, -v36, v33, v32
	v_fmac_f32_e32 v33, v34, v37
	v_fma_f32 v32, -v36, v33, v32
	v_div_fmas_f32 v32, v32, v37, v33
	v_div_fixup_f32 v29, v32, v35, v29
	v_cvt_pk_bf16_f32 v29, v28, v29
	v_cndmask_b32_e64 v28, v38, v30, s[2:3]
	v_cndmask_b32_e64 v31, v39, v29, s[2:3]
	ds_bpermute_b32 v28, v98, v28
	ds_bpermute_b32 v32, v98, v31
	s_waitcnt lgkmcnt(1)
	v_cndmask_b32_e64 v30, v30, v28, s[2:3]
	v_cndmask_b32_e64 v28, v28, v38, s[2:3]
	s_waitcnt lgkmcnt(0)
	v_cndmask_b32_e64 v31, v29, v32, s[2:3]
	v_cndmask_b32_e64 v29, v32, v39, s[2:3]
	global_store_dwordx4 v[18:19], v[28:31], off offset:256
	s_nop 1
	v_or_b32_e32 v28, 0x140, v66
	v_mov_b32_e32 v29, v67
	v_lshl_add_u64 v[28:29], v[72:73], 0, v[28:29]
	v_mov_b32_e32 v32, v214
	v_mov_b32_e32 v33, v215
	s_nop 0
	s_waitcnt vmcnt(10)
	v_mov_b32_e32 v28, v160
	v_mov_b32_e32 v29, v161
	v_mov_b32_e32 v30, v162
	v_mov_b32_e32 v31, v163
	s_nop 0
	v_lshlrev_b32_e32 v34, 16, v32
	v_mul_f32_e32 v35, 0xbfb8aa3b, v34
	v_fma_f32 v36, v34, s76, -v35
	v_rndne_f32_e32 v37, v35
	v_fmac_f32_e32 v36, 0xb2a5705f, v34
	v_sub_f32_e32 v35, v35, v37
	v_add_f32_e32 v35, v35, v36
	v_exp_f32_e32 v35, v35
	v_cvt_i32_f32_e32 v36, v37
	s_nop 0
	v_mul_f32_e32 v26, v26, v28
	v_cmp_nlt_f32_e32 vcc, s77, v34
	v_and_b32_e32 v32, 0xffff0000, v32
	v_ldexp_f32 v28, v35, v36
	v_cndmask_b32_e32 v28, 0, v28, vcc
	v_cmp_ngt_f32_e32 vcc, s78, v34
	v_mul_f32_e32 v27, v27, v29
	v_lshlrev_b32_e32 v36, 16, v33
	v_cndmask_b32_e32 v28, v97, v28, vcc
	v_add_f32_e32 v28, 1.0, v28
	v_div_scale_f32 v34, s[4:5], v28, v28, v26
	v_rcp_f32_e32 v35, v34
	v_cmp_nlt_f32_e64 s[4:5], s77, v32
	v_mul_f32_e32 v24, v24, v30
	v_and_b32_e32 v33, 0xffff0000, v33
	v_fma_f32 v37, -v34, v35, 1.0
	v_fmac_f32_e32 v35, v37, v35
	v_div_scale_f32 v37, vcc, v26, v28, v26
	v_mul_f32_e32 v38, v37, v35
	v_fma_f32 v39, -v34, v38, v37
	v_fmac_f32_e32 v38, v39, v35
	v_mul_f32_e32 v39, 0xbfb8aa3b, v32
	v_fma_f32 v40, v32, s76, -v39
	v_rndne_f32_e32 v41, v39
	v_fmac_f32_e32 v40, 0xb2a5705f, v32
	v_sub_f32_e32 v39, v39, v41
	v_add_f32_e32 v39, v39, v40
	v_exp_f32_e32 v39, v39
	v_cvt_i32_f32_e32 v40, v41
	v_fma_f32 v34, -v34, v38, v37
	v_div_fmas_f32 v34, v34, v35, v38
	v_div_fixup_f32 v26, v34, v28, v26
	v_ldexp_f32 v29, v39, v40
	v_cndmask_b32_e64 v29, 0, v29, s[4:5]
	v_cmp_ngt_f32_e64 s[4:5], s78, v32
	v_mul_f32_e32 v25, v25, v31
	s_nop 0
	v_cndmask_b32_e64 v29, v97, v29, s[4:5]
	v_add_f32_e32 v29, 1.0, v29
	v_div_scale_f32 v32, s[4:5], v29, v29, v27
	v_rcp_f32_e32 v37, v32
	v_cmp_nlt_f32_e64 s[4:5], s77, v36
	v_fma_f32 v28, -v32, v37, 1.0
	v_fmac_f32_e32 v37, v28, v37
	v_div_scale_f32 v28, vcc, v27, v29, v27
	v_mul_f32_e32 v34, v28, v37
	v_fma_f32 v35, -v32, v34, v28
	v_fmac_f32_e32 v34, v35, v37
	v_mul_f32_e32 v35, 0xbfb8aa3b, v36
	v_fma_f32 v38, v36, s76, -v35
	v_rndne_f32_e32 v39, v35
	v_fmac_f32_e32 v38, 0xb2a5705f, v36
	v_sub_f32_e32 v35, v35, v39
	v_add_f32_e32 v35, v35, v38
	v_exp_f32_e32 v35, v35
	v_cvt_i32_f32_e32 v38, v39
	v_fma_f32 v28, -v32, v34, v28
	v_div_fmas_f32 v28, v28, v37, v34
	v_div_fixup_f32 v27, v28, v29, v27
	v_ldexp_f32 v30, v35, v38
	v_cndmask_b32_e64 v30, 0, v30, s[4:5]
	v_cmp_ngt_f32_e64 s[4:5], s78, v36
	s_nop 1
	v_cndmask_b32_e64 v30, v97, v30, s[4:5]
	v_add_f32_e32 v30, 1.0, v30
	v_div_scale_f32 v32, s[4:5], v30, v30, v24
	v_rcp_f32_e32 v35, v32
	v_cmp_nlt_f32_e64 s[4:5], s77, v33
	v_fma_f32 v28, -v32, v35, 1.0
	v_fmac_f32_e32 v35, v28, v35
	v_div_scale_f32 v28, vcc, v24, v30, v24
	v_mul_f32_e32 v29, v28, v35
	v_fma_f32 v34, -v32, v29, v28
	v_fmac_f32_e32 v29, v34, v35
	v_mul_f32_e32 v34, 0xbfb8aa3b, v33
	v_fma_f32 v36, v33, s76, -v34
	v_rndne_f32_e32 v37, v34
	v_fmac_f32_e32 v36, 0xb2a5705f, v33
	v_sub_f32_e32 v34, v34, v37
	v_add_f32_e32 v34, v34, v36
	v_exp_f32_e32 v34, v34
	v_cvt_i32_f32_e32 v36, v37
	v_fma_f32 v28, -v32, v29, v28
	v_div_fmas_f32 v28, v28, v35, v29
	v_div_fixup_f32 v24, v28, v30, v24
	v_ldexp_f32 v31, v34, v36
	v_cndmask_b32_e64 v31, 0, v31, s[4:5]
	v_cmp_ngt_f32_e64 s[4:5], s78, v33
	s_nop 1
	v_cndmask_b32_e64 v31, v97, v31, s[4:5]
	v_add_f32_e32 v31, 1.0, v31
	v_div_scale_f32 v32, s[4:5], v31, v31, v25
	v_rcp_f32_e32 v33, v32
	s_nop 0
	v_fma_f32 v28, -v32, v33, 1.0
	v_fmac_f32_e32 v33, v28, v33
	v_div_scale_f32 v28, vcc, v25, v31, v25
	v_mul_f32_e32 v29, v28, v33
	v_fma_f32 v30, -v32, v29, v28
	v_fmac_f32_e32 v29, v30, v33
	v_fma_f32 v28, -v32, v29, v28
	v_div_fmas_f32 v28, v28, v33, v29
	v_div_fixup_f32 v25, v28, v31, v25
	v_cvt_pk_bf16_f32 v30, v26, v27
	v_cvt_pk_bf16_f32 v31, v24, v25
	v_or_b32_e32 v24, 0x160, v66
	v_mov_b32_e32 v25, v67
	v_lshl_add_u64 v[24:25], v[72:73], 0, v[24:25]
	v_mov_b32_e32 v28, v216
	v_mov_b32_e32 v29, v217
	s_nop 0
	s_waitcnt vmcnt(9)
; __device__ __forceinline__ unsigned cvt_pk_bf16(float lo, float hi) { unsigned r; asm volatile("v_cvt_pk_bf16_f32 %0, %1, %2" : "=v"(r) : "v"(lo), "v"(hi)); return r; }
; __device__ __forceinline__ void mlstm_D(LAS unsigned char* lds, int c, int h, const bf16_t* Z, const float* gi, const float* bcum, const float* marr, const bf16_t* CST, const float* NST,
;                                         const float* hgain, bf16_t* YCAT) {
;     ...
;         for (int n = 0; n < 2; ++n) { const int col = h * DH + 16 * (j + n) + 4 * fq;
;             const f32x4 gn = *(const f32x4*)(hgain + col); const u32x2 ov = *(const u32x2*)(Z + trow * EVN + 4096 + col);
;             const float o0 = bf_lo(ov.x), o1 = bf_hi(ov.x), o2 = bf_lo(ov.y), o3 = bf_hi(ov.y);
;             const float y0 = acc[j + n][0] * rs * gn[0] / (1.0f + expf(-o0)), y1 = acc[j + n][1] * rs * gn[1] / (1.0f + expf(-o1));
;             const float y2 = acc[j + n][2] * rs * gn[2] / (1.0f + expf(-o2)), y3 = acc[j + n][3] * rs * gn[3] / (1.0f + expf(-o3));
;             ab[n].x = cvt_pk_bf16(y0, y1); ab[n].y = cvt_pk_bf16(y2, y3); }
;         const bool odd = fq & 1; const u32x2 give = odd ? ab[0] : ab[1];
;         u32x2 got; got.x = (unsigned)__shfl_xor((int)give.x, 16); got.y = (unsigned)__shfl_xor((int)give.y, 16);
;         u32x4 w; if (odd) { w.x = got.x; w.y = got.y; w.z = ab[1].x; w.w = ab[1].y; } else { w.x = ab[0].x; w.y = ab[0].y; w.z = got.x; w.w = got.y; }
;         *(u32x4*)(YCAT + trow * D + 1024 + h * DH + 16 * (j + (odd ? 1 : 0)) + 4 * (fq & 2)) = w; if ((j & 3) == 2) asm volatile("" ::: "memory"); }
	v_mov_b32_e32 v24, v164
	v_mov_b32_e32 v25, v165
	v_mov_b32_e32 v26, v166
	v_mov_b32_e32 v27, v167
	s_nop 0
	v_lshlrev_b32_e32 v32, 16, v28
	v_mul_f32_e32 v33, 0xbfb8aa3b, v32
	v_fma_f32 v34, v32, s76, -v33
	v_rndne_f32_e32 v35, v33
	v_fmac_f32_e32 v34, 0xb2a5705f, v32
	v_sub_f32_e32 v33, v33, v35
	v_add_f32_e32 v33, v33, v34
	v_exp_f32_e32 v33, v33
	v_cvt_i32_f32_e32 v34, v35
	s_nop 0
	v_mul_f32_e32 v22, v22, v24
	v_cmp_nlt_f32_e32 vcc, s77, v32
	v_and_b32_e32 v28, 0xffff0000, v28
	v_ldexp_f32 v24, v33, v34
	v_cndmask_b32_e32 v24, 0, v24, vcc
	v_cmp_ngt_f32_e32 vcc, s78, v32
	v_mul_f32_e32 v23, v23, v25
	v_lshlrev_b32_e32 v34, 16, v29
	v_cndmask_b32_e32 v24, v97, v24, vcc
	v_add_f32_e32 v24, 1.0, v24
	v_div_scale_f32 v32, s[4:5], v24, v24, v22
	v_rcp_f32_e32 v33, v32
	v_cmp_nlt_f32_e64 s[4:5], s77, v28
	v_mul_f32_e32 v20, v20, v26
	v_and_b32_e32 v29, 0xffff0000, v29
	v_fma_f32 v35, -v32, v33, 1.0
	v_fmac_f32_e32 v33, v35, v33
	v_div_scale_f32 v35, vcc, v22, v24, v22
	v_mul_f32_e32 v36, v35, v33
	v_fma_f32 v37, -v32, v36, v35
	v_fmac_f32_e32 v36, v37, v33
	v_mul_f32_e32 v37, 0xbfb8aa3b, v28
	v_fma_f32 v38, v28, s76, -v37
	v_rndne_f32_e32 v39, v37
	v_fmac_f32_e32 v38, 0xb2a5705f, v28
	v_sub_f32_e32 v37, v37, v39
	v_add_f32_e32 v37, v37, v38
	v_exp_f32_e32 v37, v37
	v_cvt_i32_f32_e32 v38, v39
	v_fma_f32 v32, -v32, v36, v35
	v_div_fmas_f32 v32, v32, v33, v36
	v_div_fixup_f32 v22, v32, v24, v22
	v_ldexp_f32 v25, v37, v38
	v_cndmask_b32_e64 v25, 0, v25, s[4:5]
	v_cmp_ngt_f32_e64 s[4:5], s78, v28
	v_mul_f32_e32 v21, v21, v27
	s_nop 0
	v_cndmask_b32_e64 v25, v97, v25, s[4:5]
	v_add_f32_e32 v25, 1.0, v25
	v_div_scale_f32 v28, s[4:5], v25, v25, v23
	v_rcp_f32_e32 v35, v28
	v_cmp_nlt_f32_e64 s[4:5], s77, v34
	v_fma_f32 v24, -v28, v35, 1.0
	v_fmac_f32_e32 v35, v24, v35
	v_div_scale_f32 v24, vcc, v23, v25, v23
	v_mul_f32_e32 v32, v24, v35
	v_fma_f32 v33, -v28, v32, v24
	v_fmac_f32_e32 v32, v33, v35
	v_mul_f32_e32 v33, 0xbfb8aa3b, v34
	v_fma_f32 v36, v34, s76, -v33
	v_rndne_f32_e32 v37, v33
	v_fmac_f32_e32 v36, 0xb2a5705f, v34
	v_sub_f32_e32 v33, v33, v37
	v_add_f32_e32 v33, v33, v36
	v_exp_f32_e32 v33, v33
	v_cvt_i32_f32_e32 v36, v37
	v_fma_f32 v24, -v28, v32, v24
	v_div_fmas_f32 v24, v24, v35, v32
	v_div_fixup_f32 v23, v24, v25, v23
	v_ldexp_f32 v26, v33, v36
	v_cndmask_b32_e64 v26, 0, v26, s[4:5]
	v_cmp_ngt_f32_e64 s[4:5], s78, v34
	v_cvt_pk_bf16_f32 v22, v22, v23
	s_nop 1
	v_cndmask_b32_e64 v26, v97, v26, s[4:5]
	v_add_f32_e32 v26, 1.0, v26
	v_div_scale_f32 v28, s[4:5], v26, v26, v20
	v_rcp_f32_e32 v33, v28
	v_cmp_nlt_f32_e64 s[4:5], s77, v29
	v_fma_f32 v24, -v28, v33, 1.0
	v_fmac_f32_e32 v33, v24, v33
	v_div_scale_f32 v24, vcc, v20, v26, v20
	v_mul_f32_e32 v25, v24, v33
	v_fma_f32 v32, -v28, v25, v24
	v_fmac_f32_e32 v25, v32, v33
	v_mul_f32_e32 v32, 0xbfb8aa3b, v29
	v_fma_f32 v34, v29, s76, -v32
	v_rndne_f32_e32 v35, v32
	v_fmac_f32_e32 v34, 0xb2a5705f, v29
	v_sub_f32_e32 v32, v32, v35
	v_add_f32_e32 v32, v32, v34
	v_exp_f32_e32 v32, v32
	v_cvt_i32_f32_e32 v34, v35
	v_fma_f32 v24, -v28, v25, v24
	v_div_fmas_f32 v24, v24, v33, v25
	v_div_fixup_f32 v20, v24, v26, v20
	v_ldexp_f32 v27, v32, v34
	v_cndmask_b32_e64 v27, 0, v27, s[4:5]
	v_cmp_ngt_f32_e64 s[4:5], s78, v29
	s_nop 1
	v_cndmask_b32_e64 v27, v97, v27, s[4:5]
	v_add_f32_e32 v27, 1.0, v27
	v_div_scale_f32 v28, s[4:5], v27, v27, v21
	v_rcp_f32_e32 v29, v28
	s_nop 0
	v_fma_f32 v24, -v28, v29, 1.0
	v_fmac_f32_e32 v29, v24, v29
	v_div_scale_f32 v24, vcc, v21, v27, v21
	v_mul_f32_e32 v25, v24, v29
	v_fma_f32 v26, -v28, v25, v24
	v_fmac_f32_e32 v25, v26, v29
	v_fma_f32 v24, -v28, v25, v24
	v_div_fmas_f32 v24, v24, v29, v25
	v_div_fixup_f32 v21, v24, v27, v21
	v_cvt_pk_bf16_f32 v21, v20, v21
	v_cndmask_b32_e64 v20, v30, v22, s[2:3]
	v_cndmask_b32_e64 v23, v31, v21, s[2:3]
	ds_bpermute_b32 v20, v98, v20
	ds_bpermute_b32 v24, v98, v23
	s_waitcnt lgkmcnt(1)
	v_cndmask_b32_e64 v22, v22, v20, s[2:3]
	v_cndmask_b32_e64 v20, v20, v30, s[2:3]
	s_waitcnt lgkmcnt(0)
	v_cndmask_b32_e64 v23, v21, v24, s[2:3]
	v_cndmask_b32_e64 v21, v24, v31, s[2:3]
	global_store_dwordx4 v[18:19], v[20:23], off offset:320
	s_nop 1
	v_or_b32_e32 v20, 0x180, v66
	v_mov_b32_e32 v21, v67
	v_lshl_add_u64 v[20:21], v[72:73], 0, v[20:21]
	v_mov_b32_e32 v24, v218
	v_mov_b32_e32 v25, v219
	s_nop 0
	s_waitcnt vmcnt(9)
; __device__ __forceinline__ unsigned cvt_pk_bf16(float lo, float hi) { unsigned r; asm volatile("v_cvt_pk_bf16_f32 %0, %1, %2" : "=v"(r) : "v"(lo), "v"(hi)); return r; }
; __device__ __forceinline__ void mlstm_D(LAS unsigned char* lds, int c, int h, const bf16_t* Z, const float* gi, const float* bcum, const float* marr, const bf16_t* CST, const float* NST,
;                                         const float* hgain, bf16_t* YCAT) {
;     ...
;         for (int n = 0; n < 2; ++n) { const int col = h * DH + 16 * (j + n) + 4 * fq;
;             const f32x4 gn = *(const f32x4*)(hgain + col); const u32x2 ov = *(const u32x2*)(Z + trow * EVN + 4096 + col);
;             const float o0 = bf_lo(ov.x), o1 = bf_hi(ov.x), o2 = bf_lo(ov.y), o3 = bf_hi(ov.y);
;             const float y0 = acc[j + n][0] * rs * gn[0] / (1.0f + expf(-o0)), y1 = acc[j + n][1] * rs * gn[1] / (1.0f + expf(-o1));
;             const float y2 = acc[j + n][2] * rs * gn[2] / (1.0f + expf(-o2)), y3 = acc[j + n][3] * rs * gn[3] / (1.0f + expf(-o3));
;             ab[n].x = cvt_pk_bf16(y0, y1); ab[n].y = cvt_pk_bf16(y2, y3); }
;         const bool odd = fq & 1; const u32x2 give = odd ? ab[0] : ab[1];
;         u32x2 got; got.x = (unsigned)__shfl_xor((int)give.x, 16); got.y = (unsigned)__shfl_xor((int)give.y, 16);
;         u32x4 w; if (odd) { w.x = got.x; w.y = got.y; w.z = ab[1].x; w.w = ab[1].y; } else { w.x = ab[0].x; w.y = ab[0].y; w.z = got.x; w.w = got.y; }
;         *(u32x4*)(YCAT + trow * D + 1024 + h * DH + 16 * (j + (odd ? 1 : 0)) + 4 * (fq & 2)) = w; if ((j & 3) == 2) asm volatile("" ::: "memory"); }
	v_mov_b32_e32 v20, v168
	v_mov_b32_e32 v21, v169
	v_mov_b32_e32 v22, v170
	v_mov_b32_e32 v23, v171
	s_nop 0
	v_lshlrev_b32_e32 v26, 16, v24
	v_mul_f32_e32 v27, 0xbfb8aa3b, v26
	v_fma_f32 v28, v26, s76, -v27
	v_rndne_f32_e32 v29, v27
	v_fmac_f32_e32 v28, 0xb2a5705f, v26
	v_sub_f32_e32 v27, v27, v29
	v_add_f32_e32 v27, v27, v28
	v_exp_f32_e32 v27, v27
	v_cvt_i32_f32_e32 v28, v29
	s_nop 0
	v_mul_f32_e32 v14, v14, v20
	v_cmp_nlt_f32_e32 vcc, s77, v26
	v_and_b32_e32 v24, 0xffff0000, v24
	v_ldexp_f32 v20, v27, v28
	v_cndmask_b32_e32 v20, 0, v20, vcc
	v_cmp_ngt_f32_e32 vcc, s78, v26
	v_mul_f32_e32 v15, v15, v21
	v_lshlrev_b32_e32 v28, 16, v25
	v_cndmask_b32_e32 v20, v97, v20, vcc
	v_add_f32_e32 v20, 1.0, v20
	v_div_scale_f32 v26, s[4:5], v20, v20, v14
	v_rcp_f32_e32 v27, v26
	v_cmp_nlt_f32_e64 s[4:5], s77, v24
	v_mul_f32_e32 v16, v16, v22
	v_and_b32_e32 v25, 0xffff0000, v25
	v_fma_f32 v29, -v26, v27, 1.0
	v_fmac_f32_e32 v27, v29, v27
	v_div_scale_f32 v29, vcc, v14, v20, v14
	v_mul_f32_e32 v30, v29, v27
	v_fma_f32 v31, -v26, v30, v29
	v_fmac_f32_e32 v30, v31, v27
	v_mul_f32_e32 v31, 0xbfb8aa3b, v24
	v_fma_f32 v32, v24, s76, -v31
	v_rndne_f32_e32 v33, v31
	v_fmac_f32_e32 v32, 0xb2a5705f, v24
	v_sub_f32_e32 v31, v31, v33
	v_add_f32_e32 v31, v31, v32
	v_exp_f32_e32 v31, v31
	v_cvt_i32_f32_e32 v32, v33
	v_fma_f32 v26, -v26, v30, v29
	v_div_fmas_f32 v26, v26, v27, v30
	v_div_fixup_f32 v14, v26, v20, v14
	v_ldexp_f32 v21, v31, v32
	v_cndmask_b32_e64 v21, 0, v21, s[4:5]
	v_cmp_ngt_f32_e64 s[4:5], s78, v24
	v_mul_f32_e32 v17, v17, v23
	s_nop 0
	v_cndmask_b32_e64 v21, v97, v21, s[4:5]
	v_add_f32_e32 v21, 1.0, v21
	v_div_scale_f32 v24, s[4:5], v21, v21, v15
	v_rcp_f32_e32 v29, v24
	v_cmp_nlt_f32_e64 s[4:5], s77, v28
	v_fma_f32 v20, -v24, v29, 1.0
	v_fmac_f32_e32 v29, v20, v29
	v_div_scale_f32 v20, vcc, v15, v21, v15
	v_mul_f32_e32 v26, v20, v29
	v_fma_f32 v27, -v24, v26, v20
	v_fmac_f32_e32 v26, v27, v29
	v_mul_f32_e32 v27, 0xbfb8aa3b, v28
	v_fma_f32 v30, v28, s76, -v27
	v_rndne_f32_e32 v31, v27
	v_fmac_f32_e32 v30, 0xb2a5705f, v28
	v_sub_f32_e32 v27, v27, v31
	v_add_f32_e32 v27, v27, v30
	v_exp_f32_e32 v27, v27
	v_cvt_i32_f32_e32 v30, v31
	v_fma_f32 v20, -v24, v26, v20
	v_div_fmas_f32 v20, v20, v29, v26
	v_div_fixup_f32 v15, v20, v21, v15
	v_ldexp_f32 v22, v27, v30
	v_cndmask_b32_e64 v22, 0, v22, s[4:5]
	v_cmp_ngt_f32_e64 s[4:5], s78, v28
	s_nop 1
	v_cndmask_b32_e64 v22, v97, v22, s[4:5]
	v_add_f32_e32 v22, 1.0, v22
	v_div_scale_f32 v24, s[4:5], v22, v22, v16
	v_rcp_f32_e32 v27, v24
	v_cmp_nlt_f32_e64 s[4:5], s77, v25
	v_fma_f32 v20, -v24, v27, 1.0
	v_fmac_f32_e32 v27, v20, v27
	v_div_scale_f32 v20, vcc, v16, v22, v16
	v_mul_f32_e32 v21, v20, v27
	v_fma_f32 v26, -v24, v21, v20
	v_fmac_f32_e32 v21, v26, v27
	v_mul_f32_e32 v26, 0xbfb8aa3b, v25
	v_fma_f32 v28, v25, s76, -v26
	v_rndne_f32_e32 v29, v26
	v_fmac_f32_e32 v28, 0xb2a5705f, v25
	v_sub_f32_e32 v26, v26, v29
	v_add_f32_e32 v26, v26, v28
	v_exp_f32_e32 v26, v26
	v_cvt_i32_f32_e32 v28, v29
	v_fma_f32 v20, -v24, v21, v20
	v_div_fmas_f32 v20, v20, v27, v21
	v_div_fixup_f32 v16, v20, v22, v16
	v_ldexp_f32 v23, v26, v28
	v_cndmask_b32_e64 v23, 0, v23, s[4:5]
	v_cmp_ngt_f32_e64 s[4:5], s78, v25
	s_nop 1
	v_cndmask_b32_e64 v23, v97, v23, s[4:5]
	v_add_f32_e32 v23, 1.0, v23
	v_div_scale_f32 v24, s[4:5], v23, v23, v17
	v_rcp_f32_e32 v25, v24
	s_nop 0
	v_fma_f32 v20, -v24, v25, 1.0
	v_fmac_f32_e32 v25, v20, v25
	v_div_scale_f32 v20, vcc, v17, v23, v17
	v_mul_f32_e32 v21, v20, v25
	v_fma_f32 v22, -v24, v21, v20
	v_fmac_f32_e32 v21, v22, v25
	v_fma_f32 v20, -v24, v21, v20
	v_div_fmas_f32 v20, v20, v25, v21
	v_cvt_pk_bf16_f32 v22, v14, v15
	v_or_b32_e32 v14, 0x1a0, v66
	v_mov_b32_e32 v15, v67
	v_div_fixup_f32 v17, v20, v23, v17
	v_lshl_add_u64 v[14:15], v[72:73], 0, v[14:15]
	v_cvt_pk_bf16_f32 v23, v16, v17
	v_mov_b32_e32 v20, v220
	v_mov_b32_e32 v21, v221
	s_nop 0
	s_waitcnt vmcnt(8)
	v_mov_b32_e32 v14, v172
	v_mov_b32_e32 v15, v173
	v_mov_b32_e32 v16, v174
	v_mov_b32_e32 v17, v175
	s_nop 0
	v_lshlrev_b32_e32 v24, 16, v20
	v_mul_f32_e32 v25, 0xbfb8aa3b, v24
	v_fma_f32 v26, v24, s76, -v25
	v_rndne_f32_e32 v27, v25
	v_fmac_f32_e32 v26, 0xb2a5705f, v24
	v_sub_f32_e32 v25, v25, v27
	v_add_f32_e32 v25, v25, v26
	v_exp_f32_e32 v25, v25
	v_cvt_i32_f32_e32 v26, v27
	s_nop 0
	v_mul_f32_e32 v10, v10, v14
	v_cmp_nlt_f32_e32 vcc, s77, v24
	v_and_b32_e32 v20, 0xffff0000, v20
	v_ldexp_f32 v14, v25, v26
	v_cndmask_b32_e32 v14, 0, v14, vcc
	v_cmp_ngt_f32_e32 vcc, s78, v24
	v_mul_f32_e32 v11, v11, v15
	v_lshlrev_b32_e32 v26, 16, v21
	v_cndmask_b32_e32 v14, v97, v14, vcc
	v_add_f32_e32 v14, 1.0, v14
	v_div_scale_f32 v24, s[4:5], v14, v14, v10
	v_rcp_f32_e32 v25, v24
	v_cmp_nlt_f32_e64 s[4:5], s77, v20
	v_mul_f32_e32 v12, v12, v16
	v_and_b32_e32 v21, 0xffff0000, v21
	v_fma_f32 v27, -v24, v25, 1.0
	v_fmac_f32_e32 v25, v27, v25
	v_div_scale_f32 v27, vcc, v10, v14, v10
	v_mul_f32_e32 v28, v27, v25
	v_fma_f32 v29, -v24, v28, v27
	v_fmac_f32_e32 v28, v29, v25
	v_mul_f32_e32 v29, 0xbfb8aa3b, v20
	v_fma_f32 v30, v20, s76, -v29
	v_rndne_f32_e32 v31, v29
	v_fmac_f32_e32 v30, 0xb2a5705f, v20
	v_sub_f32_e32 v29, v29, v31
	v_add_f32_e32 v29, v29, v30
	v_exp_f32_e32 v29, v29
	v_cvt_i32_f32_e32 v30, v31
	v_fma_f32 v24, -v24, v28, v27
	v_div_fmas_f32 v24, v24, v25, v28
	v_div_fixup_f32 v10, v24, v14, v10
	v_ldexp_f32 v15, v29, v30
	v_cndmask_b32_e64 v15, 0, v15, s[4:5]
	v_cmp_ngt_f32_e64 s[4:5], s78, v20
	v_mul_f32_e32 v13, v13, v17
	s_nop 0
	v_cndmask_b32_e64 v15, v97, v15, s[4:5]
	v_add_f32_e32 v15, 1.0, v15
	v_div_scale_f32 v20, s[4:5], v15, v15, v11
	v_rcp_f32_e32 v27, v20
	v_cmp_nlt_f32_e64 s[4:5], s77, v26
	v_fma_f32 v14, -v20, v27, 1.0
; __device__ __forceinline__ unsigned cvt_pk_bf16(float lo, float hi) { unsigned r; asm volatile("v_cvt_pk_bf16_f32 %0, %1, %2" : "=v"(r) : "v"(lo), "v"(hi)); return r; }
; __device__ __forceinline__ void mlstm_D(LAS unsigned char* lds, int c, int h, const bf16_t* Z, const float* gi, const float* bcum, const float* marr, const bf16_t* CST, const float* NST,
;                                         const float* hgain, bf16_t* YCAT) {
;     ...
;         for (int n = 0; n < 2; ++n) { const int col = h * DH + 16 * (j + n) + 4 * fq;
;             const f32x4 gn = *(const f32x4*)(hgain + col); const u32x2 ov = *(const u32x2*)(Z + trow * EVN + 4096 + col);
;             const float o0 = bf_lo(ov.x), o1 = bf_hi(ov.x), o2 = bf_lo(ov.y), o3 = bf_hi(ov.y);
;             const float y0 = acc[j + n][0] * rs * gn[0] / (1.0f + expf(-o0)), y1 = acc[j + n][1] * rs * gn[1] / (1.0f + expf(-o1));
;             const float y2 = acc[j + n][2] * rs * gn[2] / (1.0f + expf(-o2)), y3 = acc[j + n][3] * rs * gn[3] / (1.0f + expf(-o3));
;             ab[n].x = cvt_pk_bf16(y0, y1); ab[n].y = cvt_pk_bf16(y2, y3); }
;         const bool odd = fq & 1; const u32x2 give = odd ? ab[0] : ab[1];
;         u32x2 got; got.x = (unsigned)__shfl_xor((int)give.x, 16); got.y = (unsigned)__shfl_xor((int)give.y, 16);
;         u32x4 w; if (odd) { w.x = got.x; w.y = got.y; w.z = ab[1].x; w.w = ab[1].y; } else { w.x = ab[0].x; w.y = ab[0].y; w.z = got.x; w.w = got.y; }
;         *(u32x4*)(YCAT + trow * D + 1024 + h * DH + 16 * (j + (odd ? 1 : 0)) + 4 * (fq & 2)) = w; if ((j & 3) == 2) asm volatile("" ::: "memory"); }
	v_fmac_f32_e32 v27, v14, v27
	v_div_scale_f32 v14, vcc, v11, v15, v11
	v_mul_f32_e32 v24, v14, v27
	v_fma_f32 v25, -v20, v24, v14
	v_fmac_f32_e32 v24, v25, v27
	v_mul_f32_e32 v25, 0xbfb8aa3b, v26
	v_fma_f32 v28, v26, s76, -v25
	v_rndne_f32_e32 v29, v25
	v_fmac_f32_e32 v28, 0xb2a5705f, v26
	v_sub_f32_e32 v25, v25, v29
	v_add_f32_e32 v25, v25, v28
	v_exp_f32_e32 v25, v25
	v_cvt_i32_f32_e32 v28, v29
	v_fma_f32 v14, -v20, v24, v14
	v_div_fmas_f32 v14, v14, v27, v24
	v_div_fixup_f32 v11, v14, v15, v11
	v_ldexp_f32 v16, v25, v28
	v_cndmask_b32_e64 v16, 0, v16, s[4:5]
	v_cmp_ngt_f32_e64 s[4:5], s78, v26
	v_cvt_pk_bf16_f32 v10, v10, v11
	s_nop 1
	v_cndmask_b32_e64 v16, v97, v16, s[4:5]
	v_add_f32_e32 v16, 1.0, v16
	v_div_scale_f32 v20, s[4:5], v16, v16, v12
	v_rcp_f32_e32 v25, v20
	v_cmp_nlt_f32_e64 s[4:5], s77, v21
	v_fma_f32 v14, -v20, v25, 1.0
	v_fmac_f32_e32 v25, v14, v25
	v_div_scale_f32 v14, vcc, v12, v16, v12
	v_mul_f32_e32 v15, v14, v25
	v_fma_f32 v24, -v20, v15, v14
	v_fmac_f32_e32 v15, v24, v25
	v_mul_f32_e32 v24, 0xbfb8aa3b, v21
	v_fma_f32 v26, v21, s76, -v24
	v_rndne_f32_e32 v27, v24
	v_fmac_f32_e32 v26, 0xb2a5705f, v21
	v_sub_f32_e32 v24, v24, v27
	v_add_f32_e32 v24, v24, v26
	v_exp_f32_e32 v24, v24
	v_cvt_i32_f32_e32 v26, v27
	v_fma_f32 v14, -v20, v15, v14
	v_div_fmas_f32 v14, v14, v25, v15
	v_div_fixup_f32 v12, v14, v16, v12
	v_ldexp_f32 v17, v24, v26
	v_cndmask_b32_e64 v17, 0, v17, s[4:5]
	v_cmp_ngt_f32_e64 s[4:5], s78, v21
	s_nop 1
	v_cndmask_b32_e64 v17, v97, v17, s[4:5]
	v_add_f32_e32 v17, 1.0, v17
	v_div_scale_f32 v20, s[4:5], v17, v17, v13
	v_rcp_f32_e32 v21, v20
	s_nop 0
	v_fma_f32 v14, -v20, v21, 1.0
	v_fmac_f32_e32 v21, v14, v21
	v_div_scale_f32 v14, vcc, v13, v17, v13
	v_mul_f32_e32 v15, v14, v21
	v_fma_f32 v16, -v20, v15, v14
	v_fmac_f32_e32 v15, v16, v21
	v_fma_f32 v14, -v20, v15, v14
	v_div_fmas_f32 v14, v14, v21, v15
	v_div_fixup_f32 v13, v14, v17, v13
	v_cvt_pk_bf16_f32 v11, v12, v13
	v_cndmask_b32_e64 v12, v22, v10, s[2:3]
	ds_bpermute_b32 v13, v98, v12
	v_cndmask_b32_e64 v12, v23, v11, s[2:3]
	ds_bpermute_b32 v14, v98, v12
	s_waitcnt lgkmcnt(1)
	v_cndmask_b32_e64 v12, v10, v13, s[2:3]
	v_cndmask_b32_e64 v10, v13, v22, s[2:3]
	s_waitcnt lgkmcnt(0)
	v_cndmask_b32_e64 v13, v11, v14, s[2:3]
	v_cndmask_b32_e64 v11, v14, v23, s[2:3]
	global_store_dwordx4 v[18:19], v[10:13], off offset:384
	s_nop 1
	v_or_b32_e32 v10, 0x1c0, v66
	v_mov_b32_e32 v11, v67
	v_lshl_add_u64 v[10:11], v[72:73], 0, v[10:11]
	v_mov_b32_e32 v14, v222
	v_mov_b32_e32 v15, v223
	s_nop 0
	s_waitcnt vmcnt(8)
	v_mov_b32_e32 v10, v176
	v_mov_b32_e32 v11, v177
	v_mov_b32_e32 v12, v178
	v_mov_b32_e32 v13, v179
	v_or_b32_e32 v66, 0x1e0, v66
	s_nop 0
	v_lshlrev_b32_e32 v16, 16, v14
	v_mul_f32_e32 v17, 0xbfb8aa3b, v16
	v_fma_f32 v20, v16, s76, -v17
	v_rndne_f32_e32 v21, v17
	v_fmac_f32_e32 v20, 0xb2a5705f, v16
	v_sub_f32_e32 v17, v17, v21
	v_add_f32_e32 v17, v17, v20
	v_exp_f32_e32 v17, v17
	v_cvt_i32_f32_e32 v20, v21
	s_nop 0
	v_mul_f32_e32 v6, v6, v10
	v_cmp_nlt_f32_e32 vcc, s77, v16
	v_and_b32_e32 v14, 0xffff0000, v14
	v_ldexp_f32 v10, v17, v20
	v_cndmask_b32_e32 v10, 0, v10, vcc
	v_cmp_ngt_f32_e32 vcc, s78, v16
	v_mul_f32_e32 v7, v7, v11
	v_lshlrev_b32_e32 v20, 16, v15
	v_cndmask_b32_e32 v10, v97, v10, vcc
	v_add_f32_e32 v10, 1.0, v10
	v_div_scale_f32 v16, s[4:5], v10, v10, v6
	v_rcp_f32_e32 v17, v16
	v_cmp_nlt_f32_e64 s[4:5], s77, v14
	v_mul_f32_e32 v8, v8, v12
	v_and_b32_e32 v15, 0xffff0000, v15
	v_fma_f32 v21, -v16, v17, 1.0
	v_fmac_f32_e32 v17, v21, v17
	v_div_scale_f32 v21, vcc, v6, v10, v6
	v_mul_f32_e32 v22, v21, v17
	v_fma_f32 v23, -v16, v22, v21
	v_fmac_f32_e32 v22, v23, v17
	v_mul_f32_e32 v23, 0xbfb8aa3b, v14
	v_fma_f32 v24, v14, s76, -v23
	v_rndne_f32_e32 v25, v23
	v_fmac_f32_e32 v24, 0xb2a5705f, v14
	v_sub_f32_e32 v23, v23, v25
	v_add_f32_e32 v23, v23, v24
	v_exp_f32_e32 v23, v23
	v_cvt_i32_f32_e32 v24, v25
	v_fma_f32 v16, -v16, v22, v21
	v_div_fmas_f32 v16, v16, v17, v22
	v_div_fixup_f32 v6, v16, v10, v6
	v_ldexp_f32 v11, v23, v24
	v_cndmask_b32_e64 v11, 0, v11, s[4:5]
	v_cmp_ngt_f32_e64 s[4:5], s78, v14
	v_mul_f32_e32 v9, v9, v13
	s_nop 0
	v_cndmask_b32_e64 v11, v97, v11, s[4:5]
	v_add_f32_e32 v11, 1.0, v11
	v_div_scale_f32 v14, s[4:5], v11, v11, v7
	v_rcp_f32_e32 v21, v14
	v_cmp_nlt_f32_e64 s[4:5], s77, v20
	v_fma_f32 v10, -v14, v21, 1.0
	v_fmac_f32_e32 v21, v10, v21
	v_div_scale_f32 v10, vcc, v7, v11, v7
	v_mul_f32_e32 v16, v10, v21
	v_fma_f32 v17, -v14, v16, v10
	v_fmac_f32_e32 v16, v17, v21
	v_mul_f32_e32 v17, 0xbfb8aa3b, v20
	v_fma_f32 v22, v20, s76, -v17
	v_rndne_f32_e32 v23, v17
	v_fmac_f32_e32 v22, 0xb2a5705f, v20
	v_sub_f32_e32 v17, v17, v23
	v_add_f32_e32 v17, v17, v22
	v_exp_f32_e32 v17, v17
	v_cvt_i32_f32_e32 v22, v23
	v_fma_f32 v10, -v14, v16, v10
	v_div_fmas_f32 v10, v10, v21, v16
	v_div_fixup_f32 v7, v10, v11, v7
	v_ldexp_f32 v12, v17, v22
	v_cndmask_b32_e64 v12, 0, v12, s[4:5]
	v_cmp_ngt_f32_e64 s[4:5], s78, v20
	s_nop 1
	v_cndmask_b32_e64 v12, v97, v12, s[4:5]
	v_add_f32_e32 v12, 1.0, v12
	v_div_scale_f32 v14, s[4:5], v12, v12, v8
	v_rcp_f32_e32 v17, v14
	v_cmp_nlt_f32_e64 s[4:5], s77, v15
	v_fma_f32 v10, -v14, v17, 1.0
	v_fmac_f32_e32 v17, v10, v17
	v_div_scale_f32 v10, vcc, v8, v12, v8
	v_mul_f32_e32 v11, v10, v17
	v_fma_f32 v16, -v14, v11, v10
	v_fmac_f32_e32 v11, v16, v17
	v_mul_f32_e32 v16, 0xbfb8aa3b, v15
	v_fma_f32 v20, v15, s76, -v16
	v_rndne_f32_e32 v21, v16
	v_fmac_f32_e32 v20, 0xb2a5705f, v15
	v_sub_f32_e32 v16, v16, v21
	v_add_f32_e32 v16, v16, v20
	v_exp_f32_e32 v16, v16
	v_cvt_i32_f32_e32 v20, v21
	v_fma_f32 v10, -v14, v11, v10
	v_div_fmas_f32 v10, v10, v17, v11
	v_div_fixup_f32 v8, v10, v12, v8
	v_ldexp_f32 v13, v16, v20
	v_cndmask_b32_e64 v13, 0, v13, s[4:5]
	v_cmp_ngt_f32_e64 s[4:5], s78, v15
	s_nop 1
	v_cndmask_b32_e64 v13, v97, v13, s[4:5]
	v_add_f32_e32 v13, 1.0, v13
	v_div_scale_f32 v14, s[4:5], v13, v13, v9
	v_rcp_f32_e32 v15, v14
	s_nop 0
	v_fma_f32 v10, -v14, v15, 1.0
	v_fmac_f32_e32 v15, v10, v15
	v_div_scale_f32 v10, vcc, v9, v13, v9
	v_mul_f32_e32 v11, v10, v15
	v_fma_f32 v12, -v14, v11, v10
	v_fmac_f32_e32 v11, v12, v15
	v_fma_f32 v10, -v14, v11, v10
	v_div_fmas_f32 v10, v10, v15, v11
	v_div_fixup_f32 v9, v10, v13, v9
	v_cvt_pk_bf16_f32 v12, v6, v7
	v_lshl_add_u64 v[6:7], v[72:73], 0, v[66:67]
	v_cvt_pk_bf16_f32 v13, v8, v9
	v_mov_b32_e32 v10, v224
	v_mov_b32_e32 v11, v225
	s_nop 0
	s_waitcnt vmcnt(7)
; __device__ __forceinline__ unsigned cvt_pk_bf16(float lo, float hi) { unsigned r; asm volatile("v_cvt_pk_bf16_f32 %0, %1, %2" : "=v"(r) : "v"(lo), "v"(hi)); return r; }
; __device__ __forceinline__ void mlstm_D(LAS unsigned char* lds, int c, int h, const bf16_t* Z, const float* gi, const float* bcum, const float* marr, const bf16_t* CST, const float* NST,
;                                         const float* hgain, bf16_t* YCAT) {
;     ...
;         for (int n = 0; n < 2; ++n) { const int col = h * DH + 16 * (j + n) + 4 * fq;
;             const f32x4 gn = *(const f32x4*)(hgain + col); const u32x2 ov = *(const u32x2*)(Z + trow * EVN + 4096 + col);
;             const float o0 = bf_lo(ov.x), o1 = bf_hi(ov.x), o2 = bf_lo(ov.y), o3 = bf_hi(ov.y);
;             const float y0 = acc[j + n][0] * rs * gn[0] / (1.0f + expf(-o0)), y1 = acc[j + n][1] * rs * gn[1] / (1.0f + expf(-o1));
;             const float y2 = acc[j + n][2] * rs * gn[2] / (1.0f + expf(-o2)), y3 = acc[j + n][3] * rs * gn[3] / (1.0f + expf(-o3));
;             ab[n].x = cvt_pk_bf16(y0, y1); ab[n].y = cvt_pk_bf16(y2, y3); }
;         const bool odd = fq & 1; const u32x2 give = odd ? ab[0] : ab[1];
;         u32x2 got; got.x = (unsigned)__shfl_xor((int)give.x, 16); got.y = (unsigned)__shfl_xor((int)give.y, 16);
;         u32x4 w; if (odd) { w.x = got.x; w.y = got.y; w.z = ab[1].x; w.w = ab[1].y; } else { w.x = ab[0].x; w.y = ab[0].y; w.z = got.x; w.w = got.y; }
;         *(u32x4*)(YCAT + trow * D + 1024 + h * DH + 16 * (j + (odd ? 1 : 0)) + 4 * (fq & 2)) = w; if ((j & 3) == 2) asm volatile("" ::: "memory"); }
	v_mov_b32_e32 v6, v180
	v_mov_b32_e32 v7, v181
	v_mov_b32_e32 v8, v182
	v_mov_b32_e32 v9, v183
	s_nop 0
	v_lshlrev_b32_e32 v14, 16, v10
	v_mul_f32_e32 v15, 0xbfb8aa3b, v14
	v_fma_f32 v16, v14, s76, -v15
	v_rndne_f32_e32 v17, v15
	v_fmac_f32_e32 v16, 0xb2a5705f, v14
	v_sub_f32_e32 v15, v15, v17
	v_add_f32_e32 v15, v15, v16
	v_exp_f32_e32 v15, v15
	v_cvt_i32_f32_e32 v16, v17
	s_nop 0
	v_mul_f32_e32 v2, v2, v6
	v_cmp_nlt_f32_e32 vcc, s77, v14
	v_and_b32_e32 v10, 0xffff0000, v10
	v_ldexp_f32 v6, v15, v16
	v_cndmask_b32_e32 v6, 0, v6, vcc
	v_cmp_ngt_f32_e32 vcc, s78, v14
	v_mul_f32_e32 v3, v3, v7
	v_lshlrev_b32_e32 v16, 16, v11
	v_cndmask_b32_e32 v6, v97, v6, vcc
	v_add_f32_e32 v6, 1.0, v6
	v_div_scale_f32 v14, s[4:5], v6, v6, v2
	v_rcp_f32_e32 v15, v14
	v_cmp_nlt_f32_e64 s[4:5], s77, v10
	v_mul_f32_e32 v4, v4, v8
	v_and_b32_e32 v11, 0xffff0000, v11
	v_fma_f32 v17, -v14, v15, 1.0
	v_fmac_f32_e32 v15, v17, v15
	v_div_scale_f32 v17, vcc, v2, v6, v2
	v_mul_f32_e32 v20, v17, v15
	v_fma_f32 v21, -v14, v20, v17
	v_fmac_f32_e32 v20, v21, v15
	v_mul_f32_e32 v21, 0xbfb8aa3b, v10
	v_fma_f32 v22, v10, s76, -v21
	v_rndne_f32_e32 v23, v21
	v_fmac_f32_e32 v22, 0xb2a5705f, v10
	v_sub_f32_e32 v21, v21, v23
	v_add_f32_e32 v21, v21, v22
	v_exp_f32_e32 v21, v21
	v_cvt_i32_f32_e32 v22, v23
	v_fma_f32 v14, -v14, v20, v17
	v_div_fmas_f32 v14, v14, v15, v20
	v_div_fixup_f32 v2, v14, v6, v2
	v_ldexp_f32 v7, v21, v22
	v_cndmask_b32_e64 v7, 0, v7, s[4:5]
	v_cmp_ngt_f32_e64 s[4:5], s78, v10
	v_mul_f32_e32 v5, v5, v9
	s_nop 0
	v_cndmask_b32_e64 v7, v97, v7, s[4:5]
	v_add_f32_e32 v7, 1.0, v7
	v_div_scale_f32 v10, s[4:5], v7, v7, v3
	v_rcp_f32_e32 v17, v10
	v_cmp_nlt_f32_e64 s[4:5], s77, v16
	v_fma_f32 v6, -v10, v17, 1.0
	v_fmac_f32_e32 v17, v6, v17
	v_div_scale_f32 v6, vcc, v3, v7, v3
	v_mul_f32_e32 v14, v6, v17
	v_fma_f32 v15, -v10, v14, v6
	v_fmac_f32_e32 v14, v15, v17
	v_mul_f32_e32 v15, 0xbfb8aa3b, v16
	v_fma_f32 v20, v16, s76, -v15
	v_rndne_f32_e32 v21, v15
	v_fmac_f32_e32 v20, 0xb2a5705f, v16
	v_sub_f32_e32 v15, v15, v21
	v_add_f32_e32 v15, v15, v20
	v_exp_f32_e32 v15, v15
	v_cvt_i32_f32_e32 v20, v21
	v_fma_f32 v6, -v10, v14, v6
	v_div_fmas_f32 v6, v6, v17, v14
	v_div_fixup_f32 v3, v6, v7, v3
	v_ldexp_f32 v8, v15, v20
	v_cndmask_b32_e64 v8, 0, v8, s[4:5]
	v_cmp_ngt_f32_e64 s[4:5], s78, v16
	v_cvt_pk_bf16_f32 v2, v2, v3
	s_nop 1
	v_cndmask_b32_e64 v8, v97, v8, s[4:5]
	v_add_f32_e32 v8, 1.0, v8
	v_div_scale_f32 v10, s[4:5], v8, v8, v4
	v_rcp_f32_e32 v15, v10
	v_cmp_nlt_f32_e64 s[4:5], s77, v11
	v_fma_f32 v6, -v10, v15, 1.0
	v_fmac_f32_e32 v15, v6, v15
	v_div_scale_f32 v6, vcc, v4, v8, v4
	v_mul_f32_e32 v7, v6, v15
	v_fma_f32 v14, -v10, v7, v6
	v_fmac_f32_e32 v7, v14, v15
	v_mul_f32_e32 v14, 0xbfb8aa3b, v11
	v_fma_f32 v16, v11, s76, -v14
	v_rndne_f32_e32 v17, v14
	v_fmac_f32_e32 v16, 0xb2a5705f, v11
	v_sub_f32_e32 v14, v14, v17
	v_add_f32_e32 v14, v14, v16
	v_exp_f32_e32 v14, v14
	v_cvt_i32_f32_e32 v16, v17
	v_fma_f32 v6, -v10, v7, v6
	v_div_fmas_f32 v6, v6, v15, v7
	v_div_fixup_f32 v4, v6, v8, v4
	v_ldexp_f32 v9, v14, v16
	v_cndmask_b32_e64 v9, 0, v9, s[4:5]
	v_cmp_ngt_f32_e64 s[4:5], s78, v11
	s_nop 1
	v_cndmask_b32_e64 v9, v97, v9, s[4:5]
	v_add_f32_e32 v9, 1.0, v9
	v_div_scale_f32 v10, s[4:5], v9, v9, v5
	v_rcp_f32_e32 v11, v10
	s_nop 0
	v_fma_f32 v6, -v10, v11, 1.0
	v_fmac_f32_e32 v11, v6, v11
	v_div_scale_f32 v6, vcc, v5, v9, v5
	v_mul_f32_e32 v7, v6, v11
	v_fma_f32 v8, -v10, v7, v6
	v_fmac_f32_e32 v7, v8, v11
	v_fma_f32 v6, -v10, v7, v6
	v_div_fmas_f32 v6, v6, v11, v7
	v_div_fixup_f32 v5, v6, v9, v5
	v_cvt_pk_bf16_f32 v3, v4, v5
	v_cndmask_b32_e64 v4, v12, v2, s[2:3]
	ds_bpermute_b32 v5, v98, v4
	v_cndmask_b32_e64 v4, v13, v3, s[2:3]
	ds_bpermute_b32 v6, v98, v4
	s_waitcnt lgkmcnt(1)
	v_cndmask_b32_e64 v4, v2, v5, s[2:3]
	v_cndmask_b32_e64 v2, v5, v12, s[2:3]
	s_waitcnt lgkmcnt(0)
	v_cndmask_b32_e64 v5, v3, v6, s[2:3]
	v_cndmask_b32_e64 v3, v6, v13, s[2:3]
	global_store_dwordx4 v[18:19], v[2:5], off offset:448
	s_cbranch_scc0 .LBB0_558

; __device__ __forceinline__ unsigned cvt_pk_bf16(float lo, float hi) { unsigned r; asm volatile("v_cvt_pk_bf16_f32 %0, %1, %2" : "=v"(r) : "v"(lo), "v"(hi)); return r; }
;     __device__ __forceinline__ void operator()(const f32x4 (&acc)[2][2][4][2], const Unit& u, int wr, int wc, int fr, int fq) const {
;     ...
;         for (int ai = 0; ai < 2; ++ai)
; #pragma unroll
;             for (int m = 0; m < 4; ++m) { const int row = row0 + ai * HALF + m * 16; const size_t ro = (size_t)row * u.ldc + col0;
;                 f32x4 rv[2][2];
; #pragma unroll
;                 for (int bj = 0; bj < 2; ++bj) { rv[bj][0] = *(const f32x4*)((const float*)res + ro + bj * HALF); rv[bj][1] = *(const f32x4*)((const float*)res + ro + bj * HALF + 4); }
;                 float s = 0.f;
; #pragma unroll
;                 for (int bj = 0; bj < 2; ++bj) { const f32x4 v0 = acc[ai][bj][m][0] + rv[bj][0], v1 = acc[ai][bj][m][1] + rv[bj][1];
;                     u32x4 w; w.x = cvt_pk_bf16(v0[0], v0[1]); w.y = cvt_pk_bf16(v0[2], v0[3]); w.z = cvt_pk_bf16(v1[0], v1[1]); w.w = cvt_pk_bf16(v1[2], v1[3]);
;                     *(u32x4*)(base + ro + bj * HALF) = w;
;                     s += ((v0[0] * v0[0] + v0[1] * v0[1]) + (v0[2] * v0[2] + v0[3] * v0[3])) + ((v1[0] * v1[0] + v1[1] * v1[1]) + (v1[2] * v1[2] + v1[3] * v1[3])); }
;                 if (ssq) { s += __shfl_xor(s, 16); s += __shfl_xor(s, 32);
;                     if (fq == 0) ssq[(size_t)row * 32 + u.pn * 4 + wc] = s; } }
.LBB0_841:
	v_lshl_add_u32 v136, s20, 8, v141
	v_lshl_or_b32 v134, s67, 8, v142
	v_ashrrev_i32_e32 v137, 31, v136
	v_ashrrev_i32_e32 v135, 31, v134
	v_lshlrev_b64 v[150:151], 11, v[136:137]
	v_lshl_add_u64 v[166:167], v[150:151], 0, v[134:135]
	v_lshl_add_u64 v[162:163], v[166:167], 2, s[8:9]
	v_mov_b32_e32 v131, 0
	v_mov_b32_e32 v130, 0x20000
	v_lshl_add_u64 v[132:133], v[162:163], 0, v[130:131]
	global_load_dwordx4 v[170:173], v[132:133], off
	global_load_dwordx4 v[174:177], v[132:133], off offset:16
	global_load_dwordx4 v[178:181], v[132:133], off offset:512
	global_load_dwordx4 v[182:185], v[132:133], off offset:528
	v_mov_b32_e32 v130, 0x40000
	v_lshl_add_u64 v[132:133], v[162:163], 0, v[130:131]
	global_load_dwordx4 v[186:189], v[132:133], off
	global_load_dwordx4 v[190:193], v[132:133], off offset:16
	global_load_dwordx4 v[194:197], v[132:133], off offset:512
	global_load_dwordx4 v[198:201], v[132:133], off offset:528
	v_mov_b32_e32 v130, 0x60000
	v_lshl_add_u64 v[132:133], v[162:163], 0, v[130:131]
	global_load_dwordx4 v[202:205], v[132:133], off
	global_load_dwordx4 v[206:209], v[132:133], off offset:16
	global_load_dwordx4 v[210:213], v[132:133], off offset:512
	global_load_dwordx4 v[214:217], v[132:133], off offset:528
	v_mov_b32_e32 v130, 0x100000
	v_lshl_add_u64 v[132:133], v[162:163], 0, v[130:131]
	global_load_dwordx4 v[218:221], v[132:133], off
	global_load_dwordx4 v[222:225], v[132:133], off offset:16
	global_load_dwordx4 v[226:229], v[132:133], off offset:512
	global_load_dwordx4 v[230:233], v[132:133], off offset:528
	v_mov_b32_e32 v130, 0x120000
	v_lshl_add_u64 v[132:133], v[162:163], 0, v[130:131]
	global_load_dwordx4 v[234:237], v[132:133], off
	global_load_dwordx4 v[238:241], v[132:133], off offset:16
	global_load_dwordx4 v[242:245], v[132:133], off offset:512
	global_load_dwordx4 v[246:249], v[132:133], off offset:528
	global_load_dwordx4 v[150:153], v[162:163], off
	global_load_dwordx4 v[154:157], v[162:163], off offset:16
	global_load_dwordx4 v[158:161], v[162:163], off offset:512
	s_nop 0
	global_load_dwordx4 v[162:165], v[162:163], off offset:528
	v_and_b32_e32 v168, 64, v148
	v_xor_b32_e32 v149, 16, v148
	v_add_u32_e32 v168, 64, v168
	v_cmp_lt_i32_e32 vcc, v149, v168
	v_xor_b32_e32 v169, 32, v148
	v_lshl_add_u64 v[166:167], v[166:167], 1, s[10:11]
	v_cndmask_b32_e32 v149, v148, v149, vcc
	v_lshlrev_b32_e32 v149, 2, v149
	v_cmp_lt_i32_e32 vcc, v169, v168
	s_waitcnt vmcnt(3)
	v_pk_add_f32 v[128:129], v[128:129], v[152:153]
	v_pk_add_f32 v[126:127], v[126:127], v[150:151]
	s_waitcnt vmcnt(2)
	v_pk_add_f32 v[124:125], v[124:125], v[156:157]
	v_pk_add_f32 v[122:123], v[122:123], v[154:155]
	s_waitcnt vmcnt(1)
	v_pk_add_f32 v[120:121], v[120:121], v[160:161]
	v_pk_add_f32 v[118:119], v[118:119], v[158:159]
	s_waitcnt vmcnt(0)
	v_pk_add_f32 v[150:151], v[116:117], v[164:165]
	v_pk_add_f32 v[152:153], v[114:115], v[162:163]
	v_cvt_pk_bf16_f32 v114, v126, v127
	v_cvt_pk_bf16_f32 v115, v128, v129
	v_mul_f32_e32 v116, v127, v127
	v_mul_f32_e32 v117, v129, v129
	v_mul_f32_e32 v127, v123, v123
	v_mul_f32_e32 v129, v125, v125
	v_mul_f32_e32 v154, v119, v119
	v_mul_f32_e32 v155, v121, v121
	v_mul_f32_e32 v156, v153, v153
	v_mul_f32_e32 v157, v151, v151
	v_fmac_f32_e32 v116, v126, v126
	v_fmac_f32_e32 v117, v128, v128
	v_fmac_f32_e32 v127, v122, v122
	v_fmac_f32_e32 v129, v124, v124
	v_fmac_f32_e32 v154, v118, v118
	v_fmac_f32_e32 v155, v120, v120
	v_fmac_f32_e32 v156, v152, v152
	v_fmac_f32_e32 v157, v150, v150
	v_add_f32_e32 v116, v116, v117
	v_add_f32_e32 v117, v127, v129
	v_add_f32_e32 v126, v154, v155
	v_add_f32_e32 v127, v156, v157
	v_add_f32_e32 v116, v116, v117
	v_add_f32_e32 v117, v126, v127
	v_add_f32_e32 v126, v116, v117
	ds_bpermute_b32 v127, v149, v126
	v_cndmask_b32_e32 v168, v148, v169, vcc
	v_cvt_pk_bf16_f32 v116, v122, v123
	v_cvt_pk_bf16_f32 v117, v124, v125
	global_store_dwordx4 v[166:167], v[114:117], off
	v_cvt_pk_bf16_f32 v118, v118, v119
	v_cvt_pk_bf16_f32 v119, v120, v121
	v_cvt_pk_bf16_f32 v120, v152, v153
	v_cvt_pk_bf16_f32 v121, v150, v151
	global_store_dwordx4 v[166:167], v[118:121], off offset:256
	s_waitcnt lgkmcnt(0)
	v_add_f32_e32 v114, v126, v127
	v_lshlrev_b32_e32 v116, 2, v168
	ds_bpermute_b32 v115, v116, v114
	s_and_saveexec_b64 s[34:35], s[2:3]
	s_cbranch_execz .LBB0_843
	s_waitcnt lgkmcnt(0)
	v_add_f32_e32 v117, v114, v115
	s_lshl_b32 s42, s67, 2
	v_lshlrev_b64 v[114:115], 7, v[136:137]
	s_ashr_i32 s43, s42, 31
	v_lshl_add_u64 v[114:115], s[14:15], 0, v[114:115]
	v_lshl_add_u64 v[114:115], s[42:43], 2, v[114:115]
	s_lshl_b32 s20, s76, 2
	v_lshl_add_u64 v[114:115], v[114:115], 0, s[20:21]
	global_store_dword v[114:115], v117, off
; __device__ __forceinline__ unsigned cvt_pk_bf16(float lo, float hi) { unsigned r; asm volatile("v_cvt_pk_bf16_f32 %0, %1, %2" : "=v"(r) : "v"(lo), "v"(hi)); return r; }
;     __device__ __forceinline__ void operator()(const f32x4 (&acc)[2][2][4][2], const Unit& u, int wr, int wc, int fr, int fq) const {
;     ...
;         for (int ai = 0; ai < 2; ++ai)
; #pragma unroll
;             for (int m = 0; m < 4; ++m) { const int row = row0 + ai * HALF + m * 16; const size_t ro = (size_t)row * u.ldc + col0;
;                 f32x4 rv[2][2];
; #pragma unroll
;                 for (int bj = 0; bj < 2; ++bj) { rv[bj][0] = *(const f32x4*)((const float*)res + ro + bj * HALF); rv[bj][1] = *(const f32x4*)((const float*)res + ro + bj * HALF + 4); }
;                 float s = 0.f;
; #pragma unroll
;                 for (int bj = 0; bj < 2; ++bj) { const f32x4 v0 = acc[ai][bj][m][0] + rv[bj][0], v1 = acc[ai][bj][m][1] + rv[bj][1];
;                     u32x4 w; w.x = cvt_pk_bf16(v0[0], v0[1]); w.y = cvt_pk_bf16(v0[2], v0[3]); w.z = cvt_pk_bf16(v1[0], v1[1]); w.w = cvt_pk_bf16(v1[2], v1[3]);
;                     *(u32x4*)(base + ro + bj * HALF) = w;
;                     s += ((v0[0] * v0[0] + v0[1] * v0[1]) + (v0[2] * v0[2] + v0[3] * v0[3])) + ((v1[0] * v1[0] + v1[1] * v1[1]) + (v1[2] * v1[2] + v1[3] * v1[3])); }
;                 if (ssq) { s += __shfl_xor(s, 16); s += __shfl_xor(s, 32);
;                     if (fq == 0) ssq[(size_t)row * 32 + u.pn * 4 + wc] = s; } }
.LBB0_843:
	s_or_b64 exec, exec, s[34:35]
	v_or_b32_e32 v114, 16, v136
	s_waitcnt lgkmcnt(0)
	v_ashrrev_i32_e32 v115, 31, v114
	v_lshlrev_b64 v[118:119], 11, v[114:115]
	v_lshl_add_u64 v[154:155], v[118:119], 0, v[134:135]
	v_lshl_add_u64 v[150:151], v[154:155], 2, s[8:9]
	v_mov_b32_e32 v118, v170
	v_mov_b32_e32 v119, v171
	v_mov_b32_e32 v120, v172
	v_mov_b32_e32 v121, v173
	v_mov_b32_e32 v122, v174
	v_mov_b32_e32 v123, v175
	v_mov_b32_e32 v124, v176
	v_mov_b32_e32 v125, v177
	v_mov_b32_e32 v126, v178
	v_mov_b32_e32 v127, v179
	v_mov_b32_e32 v128, v180
	v_mov_b32_e32 v129, v181
	s_nop 0
	v_mov_b32_e32 v150, v182
	v_mov_b32_e32 v151, v183
	v_mov_b32_e32 v152, v184
	v_mov_b32_e32 v153, v185
	v_lshl_add_u64 v[154:155], v[154:155], 1, s[10:11]
	s_nop 0
	v_pk_add_f32 v[112:113], v[112:113], v[120:121]
	v_pk_add_f32 v[110:111], v[110:111], v[118:119]
	s_nop 0
	v_pk_add_f32 v[108:109], v[108:109], v[124:125]
	v_pk_add_f32 v[106:107], v[106:107], v[122:123]
	s_nop 0
	v_pk_add_f32 v[104:105], v[104:105], v[128:129]
	v_pk_add_f32 v[102:103], v[102:103], v[126:127]
	s_nop 0
	v_pk_add_f32 v[118:119], v[100:101], v[152:153]
	v_pk_add_f32 v[120:121], v[98:99], v[150:151]
	v_cvt_pk_bf16_f32 v98, v110, v111
	v_cvt_pk_bf16_f32 v99, v112, v113
	v_mul_f32_e32 v100, v111, v111
	v_mul_f32_e32 v101, v113, v113
	v_mul_f32_e32 v111, v107, v107
	v_mul_f32_e32 v113, v109, v109
	v_mul_f32_e32 v117, v103, v103
	v_mul_f32_e32 v122, v105, v105
	v_mul_f32_e32 v123, v121, v121
	v_mul_f32_e32 v124, v119, v119
	v_fmac_f32_e32 v100, v110, v110
	v_fmac_f32_e32 v101, v112, v112
	v_fmac_f32_e32 v111, v106, v106
	v_fmac_f32_e32 v113, v108, v108
	v_fmac_f32_e32 v117, v102, v102
	v_fmac_f32_e32 v122, v104, v104
	v_fmac_f32_e32 v123, v120, v120
	v_fmac_f32_e32 v124, v118, v118
	v_add_f32_e32 v100, v100, v101
	v_add_f32_e32 v101, v111, v113
	v_add_f32_e32 v110, v117, v122
	v_add_f32_e32 v111, v123, v124
	v_add_f32_e32 v100, v100, v101
	v_add_f32_e32 v101, v110, v111
	v_add_f32_e32 v110, v100, v101
	ds_bpermute_b32 v111, v149, v110
	v_cvt_pk_bf16_f32 v100, v106, v107
	v_cvt_pk_bf16_f32 v101, v108, v109
	global_store_dwordx4 v[154:155], v[98:101], off
	s_waitcnt lgkmcnt(0)
	s_nop 0
	v_add_f32_e32 v98, v110, v111
	ds_bpermute_b32 v99, v116, v98
	v_cvt_pk_bf16_f32 v100, v102, v103
	v_cvt_pk_bf16_f32 v101, v104, v105
	v_cvt_pk_bf16_f32 v102, v120, v121
	v_cvt_pk_bf16_f32 v103, v118, v119
	global_store_dwordx4 v[154:155], v[100:103], off offset:256
	s_and_saveexec_b64 s[34:35], s[2:3]
	s_cbranch_execz .LBB0_845
	s_waitcnt lgkmcnt(0)
	v_add_f32_e32 v100, v98, v99
	s_lshl_b32 s42, s67, 2
	v_lshlrev_b64 v[98:99], 7, v[114:115]
	s_ashr_i32 s43, s42, 31
	v_lshl_add_u64 v[98:99], s[14:15], 0, v[98:99]
	v_lshl_add_u64 v[98:99], s[42:43], 2, v[98:99]
	s_lshl_b32 s20, s76, 2
	v_lshl_add_u64 v[98:99], v[98:99], 0, s[20:21]
	global_store_dword v[98:99], v100, off
.LBB0_845:
	s_or_b64 exec, exec, s[34:35]
	v_or_b32_e32 v98, 32, v136
	s_waitcnt lgkmcnt(0)
	v_ashrrev_i32_e32 v99, 31, v98
	v_lshlrev_b64 v[100:101], 11, v[98:99]
	v_lshl_add_u64 v[118:119], v[100:101], 0, v[134:135]
	v_lshl_add_u64 v[112:113], v[118:119], 2, s[8:9]
	v_mov_b32_e32 v100, v186
	v_mov_b32_e32 v101, v187
	v_mov_b32_e32 v102, v188
	v_mov_b32_e32 v103, v189
	v_mov_b32_e32 v104, v190
	v_mov_b32_e32 v105, v191
	v_mov_b32_e32 v106, v192
	v_mov_b32_e32 v107, v193
	v_mov_b32_e32 v108, v194
	v_mov_b32_e32 v109, v195
	v_mov_b32_e32 v110, v196
	v_mov_b32_e32 v111, v197
	s_nop 0
	v_mov_b32_e32 v112, v198
	v_mov_b32_e32 v113, v199
	v_mov_b32_e32 v114, v200
	v_mov_b32_e32 v115, v201
	v_lshl_add_u64 v[118:119], v[118:119], 1, s[10:11]
	s_nop 0
	v_pk_add_f32 v[96:97], v[96:97], v[102:103]
	v_pk_add_f32 v[94:95], v[94:95], v[100:101]
	s_nop 0
	v_pk_add_f32 v[92:93], v[92:93], v[106:107]
	v_pk_add_f32 v[90:91], v[90:91], v[104:105]
	s_nop 0
	v_pk_add_f32 v[88:89], v[88:89], v[110:111]
	v_pk_add_f32 v[86:87], v[86:87], v[108:109]
	s_nop 0
	v_pk_add_f32 v[100:101], v[84:85], v[114:115]
	v_pk_add_f32 v[102:103], v[82:83], v[112:113]
	v_cvt_pk_bf16_f32 v82, v94, v95
	v_cvt_pk_bf16_f32 v83, v96, v97
	v_mul_f32_e32 v84, v95, v95
	v_mul_f32_e32 v85, v97, v97
	v_mul_f32_e32 v95, v91, v91
	v_mul_f32_e32 v97, v93, v93
	v_mul_f32_e32 v104, v87, v87
	v_mul_f32_e32 v105, v89, v89
	v_mul_f32_e32 v106, v103, v103
	v_mul_f32_e32 v107, v101, v101
	v_fmac_f32_e32 v84, v94, v94
	v_fmac_f32_e32 v85, v96, v96
	v_fmac_f32_e32 v95, v90, v90
	v_fmac_f32_e32 v97, v92, v92
	v_fmac_f32_e32 v104, v86, v86
	v_fmac_f32_e32 v105, v88, v88
	v_fmac_f32_e32 v106, v102, v102
	v_fmac_f32_e32 v107, v100, v100
	v_add_f32_e32 v84, v84, v85
	v_add_f32_e32 v85, v95, v97
	v_add_f32_e32 v94, v104, v105
	v_add_f32_e32 v95, v106, v107
	v_add_f32_e32 v84, v84, v85
	v_add_f32_e32 v85, v94, v95
	v_add_f32_e32 v94, v84, v85
	ds_bpermute_b32 v95, v149, v94
	v_cvt_pk_bf16_f32 v84, v90, v91
	v_cvt_pk_bf16_f32 v85, v92, v93
	global_store_dwordx4 v[118:119], v[82:85], off
	s_waitcnt lgkmcnt(0)
	s_nop 0
	v_add_f32_e32 v82, v94, v95
	ds_bpermute_b32 v83, v116, v82
	v_cvt_pk_bf16_f32 v84, v86, v87
	v_cvt_pk_bf16_f32 v85, v88, v89
	v_cvt_pk_bf16_f32 v86, v102, v103
	v_cvt_pk_bf16_f32 v87, v100, v101
	global_store_dwordx4 v[118:119], v[84:87], off offset:256
	s_and_saveexec_b64 s[34:35], s[2:3]
	s_cbranch_execz .LBB0_847
	s_waitcnt lgkmcnt(0)
	v_add_f32_e32 v84, v82, v83
	s_lshl_b32 s42, s67, 2
	v_lshlrev_b64 v[82:83], 7, v[98:99]
	s_ashr_i32 s43, s42, 31
	v_lshl_add_u64 v[82:83], s[14:15], 0, v[82:83]
	v_lshl_add_u64 v[82:83], s[42:43], 2, v[82:83]
	s_lshl_b32 s20, s76, 2
	v_lshl_add_u64 v[82:83], v[82:83], 0, s[20:21]
	global_store_dword v[82:83], v84, off
; __device__ __forceinline__ unsigned cvt_pk_bf16(float lo, float hi) { unsigned r; asm volatile("v_cvt_pk_bf16_f32 %0, %1, %2" : "=v"(r) : "v"(lo), "v"(hi)); return r; }
;     __device__ __forceinline__ void operator()(const f32x4 (&acc)[2][2][4][2], const Unit& u, int wr, int wc, int fr, int fq) const {
;     ...
;         for (int ai = 0; ai < 2; ++ai)
; #pragma unroll
;             for (int m = 0; m < 4; ++m) { const int row = row0 + ai * HALF + m * 16; const size_t ro = (size_t)row * u.ldc + col0;
;                 f32x4 rv[2][2];
; #pragma unroll
;                 for (int bj = 0; bj < 2; ++bj) { rv[bj][0] = *(const f32x4*)((const float*)res + ro + bj * HALF); rv[bj][1] = *(const f32x4*)((const float*)res + ro + bj * HALF + 4); }
;                 float s = 0.f;
; #pragma unroll
;                 for (int bj = 0; bj < 2; ++bj) { const f32x4 v0 = acc[ai][bj][m][0] + rv[bj][0], v1 = acc[ai][bj][m][1] + rv[bj][1];
;                     u32x4 w; w.x = cvt_pk_bf16(v0[0], v0[1]); w.y = cvt_pk_bf16(v0[2], v0[3]); w.z = cvt_pk_bf16(v1[0], v1[1]); w.w = cvt_pk_bf16(v1[2], v1[3]);
;                     *(u32x4*)(base + ro + bj * HALF) = w;
;                     s += ((v0[0] * v0[0] + v0[1] * v0[1]) + (v0[2] * v0[2] + v0[3] * v0[3])) + ((v1[0] * v1[0] + v1[1] * v1[1]) + (v1[2] * v1[2] + v1[3] * v1[3])); }
;                 if (ssq) { s += __shfl_xor(s, 16); s += __shfl_xor(s, 32);
;                     if (fq == 0) ssq[(size_t)row * 32 + u.pn * 4 + wc] = s; } }
.LBB0_847:
	s_or_b64 exec, exec, s[34:35]
	v_or_b32_e32 v82, 48, v136
	s_waitcnt lgkmcnt(0)
	v_ashrrev_i32_e32 v83, 31, v82
	v_lshlrev_b64 v[84:85], 11, v[82:83]
	v_lshl_add_u64 v[100:101], v[84:85], 0, v[134:135]
	v_lshl_add_u64 v[96:97], v[100:101], 2, s[8:9]
	v_mov_b32_e32 v84, v202
	v_mov_b32_e32 v85, v203
	v_mov_b32_e32 v86, v204
	v_mov_b32_e32 v87, v205
	v_mov_b32_e32 v88, v206
	v_mov_b32_e32 v89, v207
	v_mov_b32_e32 v90, v208
	v_mov_b32_e32 v91, v209
	v_mov_b32_e32 v92, v210
	v_mov_b32_e32 v93, v211
	v_mov_b32_e32 v94, v212
	v_mov_b32_e32 v95, v213
	s_nop 0
	v_mov_b32_e32 v96, v214
	v_mov_b32_e32 v97, v215
	v_mov_b32_e32 v98, v216
	v_mov_b32_e32 v99, v217
	v_lshl_add_u64 v[100:101], v[100:101], 1, s[10:11]
	s_nop 0
	v_pk_add_f32 v[80:81], v[80:81], v[86:87]
	v_pk_add_f32 v[78:79], v[78:79], v[84:85]
	s_nop 0
	v_pk_add_f32 v[76:77], v[76:77], v[90:91]
	v_pk_add_f32 v[74:75], v[74:75], v[88:89]
	s_nop 0
	v_pk_add_f32 v[72:73], v[72:73], v[94:95]
	v_pk_add_f32 v[70:71], v[70:71], v[92:93]
	s_nop 0
	v_pk_add_f32 v[84:85], v[68:69], v[98:99]
	v_pk_add_f32 v[86:87], v[66:67], v[96:97]
	v_cvt_pk_bf16_f32 v66, v78, v79
	v_cvt_pk_bf16_f32 v67, v80, v81
	v_mul_f32_e32 v68, v79, v79
	v_mul_f32_e32 v69, v81, v81
	v_mul_f32_e32 v79, v75, v75
	v_mul_f32_e32 v81, v77, v77
	v_mul_f32_e32 v88, v71, v71
	v_mul_f32_e32 v89, v73, v73
	v_mul_f32_e32 v90, v87, v87
	v_mul_f32_e32 v91, v85, v85
	v_fmac_f32_e32 v68, v78, v78
	v_fmac_f32_e32 v69, v80, v80
	v_fmac_f32_e32 v79, v74, v74
	v_fmac_f32_e32 v81, v76, v76
	v_fmac_f32_e32 v88, v70, v70
	v_fmac_f32_e32 v89, v72, v72
	v_fmac_f32_e32 v90, v86, v86
	v_fmac_f32_e32 v91, v84, v84
	v_add_f32_e32 v68, v68, v69
	v_add_f32_e32 v69, v79, v81
	v_add_f32_e32 v78, v88, v89
	v_add_f32_e32 v79, v90, v91
	v_add_f32_e32 v68, v68, v69
	v_add_f32_e32 v69, v78, v79
	v_add_f32_e32 v78, v68, v69
	ds_bpermute_b32 v79, v149, v78
	v_cvt_pk_bf16_f32 v68, v74, v75
	v_cvt_pk_bf16_f32 v69, v76, v77
	global_store_dwordx4 v[100:101], v[66:69], off
	s_waitcnt lgkmcnt(0)
	s_nop 0
	v_add_f32_e32 v66, v78, v79
	ds_bpermute_b32 v67, v116, v66
	v_cvt_pk_bf16_f32 v68, v70, v71
	v_cvt_pk_bf16_f32 v69, v72, v73
	v_cvt_pk_bf16_f32 v70, v86, v87
	v_cvt_pk_bf16_f32 v71, v84, v85
	global_store_dwordx4 v[100:101], v[68:71], off offset:256
	s_and_saveexec_b64 s[34:35], s[2:3]
	s_cbranch_execz .LBB0_849
	s_waitcnt lgkmcnt(0)
	v_add_f32_e32 v68, v66, v67
	s_lshl_b32 s42, s67, 2
	v_lshlrev_b64 v[66:67], 7, v[82:83]
	s_ashr_i32 s43, s42, 31
	v_lshl_add_u64 v[66:67], s[14:15], 0, v[66:67]
	v_lshl_add_u64 v[66:67], s[42:43], 2, v[66:67]
	s_lshl_b32 s20, s76, 2
	v_lshl_add_u64 v[66:67], v[66:67], 0, s[20:21]
	global_store_dword v[66:67], v68, off
; __device__ __forceinline__ unsigned cvt_pk_bf16(float lo, float hi) { unsigned r; asm volatile("v_cvt_pk_bf16_f32 %0, %1, %2" : "=v"(r) : "v"(lo), "v"(hi)); return r; }
;     __device__ __forceinline__ void operator()(const f32x4 (&acc)[2][2][4][2], const Unit& u, int wr, int wc, int fr, int fq) const {
;     ...
;         for (int ai = 0; ai < 2; ++ai)
; #pragma unroll
;             for (int m = 0; m < 4; ++m) { const int row = row0 + ai * HALF + m * 16; const size_t ro = (size_t)row * u.ldc + col0;
;                 f32x4 rv[2][2];
; #pragma unroll
;                 for (int bj = 0; bj < 2; ++bj) { rv[bj][0] = *(const f32x4*)((const float*)res + ro + bj * HALF); rv[bj][1] = *(const f32x4*)((const float*)res + ro + bj * HALF + 4); }
;                 float s = 0.f;
; #pragma unroll
;                 for (int bj = 0; bj < 2; ++bj) { const f32x4 v0 = acc[ai][bj][m][0] + rv[bj][0], v1 = acc[ai][bj][m][1] + rv[bj][1];
;                     u32x4 w; w.x = cvt_pk_bf16(v0[0], v0[1]); w.y = cvt_pk_bf16(v0[2], v0[3]); w.z = cvt_pk_bf16(v1[0], v1[1]); w.w = cvt_pk_bf16(v1[2], v1[3]);
;                     *(u32x4*)(base + ro + bj * HALF) = w;
;                     s += ((v0[0] * v0[0] + v0[1] * v0[1]) + (v0[2] * v0[2] + v0[3] * v0[3])) + ((v1[0] * v1[0] + v1[1] * v1[1]) + (v1[2] * v1[2] + v1[3] * v1[3])); }
;                 if (ssq) { s += __shfl_xor(s, 16); s += __shfl_xor(s, 32);
;                     if (fq == 0) ssq[(size_t)row * 32 + u.pn * 4 + wc] = s; } }
.LBB0_849:
	s_or_b64 exec, exec, s[34:35]
	v_add_u32_e32 v66, 0x80, v136
	s_waitcnt lgkmcnt(0)
	v_ashrrev_i32_e32 v67, 31, v66
	v_lshlrev_b64 v[68:69], 11, v[66:67]
	v_lshl_add_u64 v[84:85], v[68:69], 0, v[134:135]
	v_lshl_add_u64 v[80:81], v[84:85], 2, s[8:9]
	v_mov_b32_e32 v68, v218
	v_mov_b32_e32 v69, v219
	v_mov_b32_e32 v70, v220
	v_mov_b32_e32 v71, v221
	v_mov_b32_e32 v72, v222
	v_mov_b32_e32 v73, v223
	v_mov_b32_e32 v74, v224
	v_mov_b32_e32 v75, v225
	v_mov_b32_e32 v76, v226
	v_mov_b32_e32 v77, v227
	v_mov_b32_e32 v78, v228
	v_mov_b32_e32 v79, v229
	s_nop 0
	v_mov_b32_e32 v80, v230
	v_mov_b32_e32 v81, v231
	v_mov_b32_e32 v82, v232
	v_mov_b32_e32 v83, v233
	v_lshl_add_u64 v[84:85], v[84:85], 1, s[10:11]
	s_nop 0
	v_pk_add_f32 v[64:65], v[64:65], v[70:71]
	v_pk_add_f32 v[62:63], v[62:63], v[68:69]
	s_nop 0
	v_pk_add_f32 v[60:61], v[60:61], v[74:75]
	v_pk_add_f32 v[58:59], v[58:59], v[72:73]
	s_nop 0
	v_pk_add_f32 v[56:57], v[56:57], v[78:79]
	v_pk_add_f32 v[54:55], v[54:55], v[76:77]
	s_nop 0
	v_pk_add_f32 v[68:69], v[52:53], v[82:83]
	v_pk_add_f32 v[70:71], v[50:51], v[80:81]
	v_cvt_pk_bf16_f32 v50, v62, v63
	v_cvt_pk_bf16_f32 v51, v64, v65
	v_mul_f32_e32 v52, v63, v63
	v_mul_f32_e32 v53, v65, v65
	v_mul_f32_e32 v63, v59, v59
	v_mul_f32_e32 v65, v61, v61
	v_mul_f32_e32 v72, v55, v55
	v_mul_f32_e32 v73, v57, v57
	v_mul_f32_e32 v74, v71, v71
	v_mul_f32_e32 v75, v69, v69
	v_fmac_f32_e32 v52, v62, v62
	v_fmac_f32_e32 v53, v64, v64
	v_fmac_f32_e32 v63, v58, v58
	v_fmac_f32_e32 v65, v60, v60
	v_fmac_f32_e32 v72, v54, v54
	v_fmac_f32_e32 v73, v56, v56
	v_fmac_f32_e32 v74, v70, v70
	v_fmac_f32_e32 v75, v68, v68
	v_add_f32_e32 v52, v52, v53
	v_add_f32_e32 v53, v63, v65
	v_add_f32_e32 v62, v72, v73
	v_add_f32_e32 v63, v74, v75
	v_add_f32_e32 v52, v52, v53
	v_add_f32_e32 v53, v62, v63
	v_add_f32_e32 v62, v52, v53
	ds_bpermute_b32 v63, v149, v62
	v_cvt_pk_bf16_f32 v52, v58, v59
	v_cvt_pk_bf16_f32 v53, v60, v61
	global_store_dwordx4 v[84:85], v[50:53], off
	s_waitcnt lgkmcnt(0)
	s_nop 0
	v_add_f32_e32 v50, v62, v63
	ds_bpermute_b32 v51, v116, v50
	v_cvt_pk_bf16_f32 v52, v54, v55
	v_cvt_pk_bf16_f32 v53, v56, v57
	v_cvt_pk_bf16_f32 v54, v70, v71
	v_cvt_pk_bf16_f32 v55, v68, v69
	global_store_dwordx4 v[84:85], v[52:55], off offset:256
	s_and_saveexec_b64 s[34:35], s[2:3]
	s_cbranch_execz .LBB0_851
	s_waitcnt lgkmcnt(0)
	v_add_f32_e32 v52, v50, v51
	s_lshl_b32 s42, s67, 2
	v_lshlrev_b64 v[50:51], 7, v[66:67]
	s_ashr_i32 s43, s42, 31
	v_lshl_add_u64 v[50:51], s[14:15], 0, v[50:51]
	v_lshl_add_u64 v[50:51], s[42:43], 2, v[50:51]
	s_lshl_b32 s20, s76, 2
	v_lshl_add_u64 v[50:51], v[50:51], 0, s[20:21]
	global_store_dword v[50:51], v52, off
.LBB0_851:
	s_or_b64 exec, exec, s[34:35]
	v_add_u32_e32 v50, 0x90, v136
	s_waitcnt lgkmcnt(0)
	v_ashrrev_i32_e32 v51, 31, v50
	v_lshlrev_b64 v[52:53], 11, v[50:51]
	v_lshl_add_u64 v[68:69], v[52:53], 0, v[134:135]
	v_lshl_add_u64 v[64:65], v[68:69], 2, s[8:9]
	v_mov_b32_e32 v52, v234
	v_mov_b32_e32 v53, v235
	v_mov_b32_e32 v54, v236
	v_mov_b32_e32 v55, v237
	v_mov_b32_e32 v56, v238
	v_mov_b32_e32 v57, v239
	v_mov_b32_e32 v58, v240
	v_mov_b32_e32 v59, v241
	v_mov_b32_e32 v60, v242
	v_mov_b32_e32 v61, v243
	v_mov_b32_e32 v62, v244
	v_mov_b32_e32 v63, v245
	s_nop 0
	v_mov_b32_e32 v64, v246
	v_mov_b32_e32 v65, v247
	v_mov_b32_e32 v66, v248
	v_mov_b32_e32 v67, v249
	v_lshl_add_u64 v[68:69], v[68:69], 1, s[10:11]
	s_nop 0
	v_pk_add_f32 v[48:49], v[48:49], v[54:55]
	v_pk_add_f32 v[46:47], v[46:47], v[52:53]
	s_nop 0
	v_pk_add_f32 v[44:45], v[44:45], v[58:59]
	v_pk_add_f32 v[42:43], v[42:43], v[56:57]
	s_nop 0
	v_pk_add_f32 v[40:41], v[40:41], v[62:63]
	v_pk_add_f32 v[38:39], v[38:39], v[60:61]
	s_nop 0
	v_pk_add_f32 v[52:53], v[36:37], v[66:67]
	v_pk_add_f32 v[54:55], v[34:35], v[64:65]
	v_cvt_pk_bf16_f32 v34, v46, v47
	v_cvt_pk_bf16_f32 v35, v48, v49
	v_mul_f32_e32 v36, v47, v47
	v_mul_f32_e32 v37, v49, v49
	v_mul_f32_e32 v47, v43, v43
	v_mul_f32_e32 v49, v45, v45
	v_mul_f32_e32 v56, v39, v39
	v_mul_f32_e32 v57, v41, v41
	v_mul_f32_e32 v58, v55, v55
	v_mul_f32_e32 v59, v53, v53
	v_fmac_f32_e32 v36, v46, v46
	v_fmac_f32_e32 v37, v48, v48
	v_fmac_f32_e32 v47, v42, v42
	v_fmac_f32_e32 v49, v44, v44
	v_fmac_f32_e32 v56, v38, v38
	v_fmac_f32_e32 v57, v40, v40
	v_fmac_f32_e32 v58, v54, v54
	v_fmac_f32_e32 v59, v52, v52
	v_add_f32_e32 v36, v36, v37
	v_add_f32_e32 v37, v47, v49
	v_add_f32_e32 v46, v56, v57
	v_add_f32_e32 v47, v58, v59
	v_add_f32_e32 v36, v36, v37
	v_add_f32_e32 v37, v46, v47
	v_add_f32_e32 v46, v36, v37
	ds_bpermute_b32 v47, v149, v46
	v_cvt_pk_bf16_f32 v36, v42, v43
	v_cvt_pk_bf16_f32 v37, v44, v45
	global_store_dwordx4 v[68:69], v[34:37], off
	s_waitcnt lgkmcnt(0)
	s_nop 0
	v_add_f32_e32 v34, v46, v47
	ds_bpermute_b32 v35, v116, v34
	v_cvt_pk_bf16_f32 v36, v38, v39
	v_cvt_pk_bf16_f32 v37, v40, v41
	v_cvt_pk_bf16_f32 v38, v54, v55
	v_cvt_pk_bf16_f32 v39, v52, v53
	global_store_dwordx4 v[68:69], v[36:39], off offset:256
	s_and_saveexec_b64 s[34:35], s[2:3]
	s_cbranch_execz .LBB0_853
	s_waitcnt lgkmcnt(0)
	v_add_f32_e32 v36, v34, v35
	s_lshl_b32 s42, s67, 2
	v_lshlrev_b64 v[34:35], 7, v[50:51]
	s_ashr_i32 s43, s42, 31
	v_lshl_add_u64 v[34:35], s[14:15], 0, v[34:35]
	v_lshl_add_u64 v[34:35], s[42:43], 2, v[34:35]
	s_lshl_b32 s20, s76, 2
	v_lshl_add_u64 v[34:35], v[34:35], 0, s[20:21]
	global_store_dword v[34:35], v36, off

; #define LAS __attribute__((address_space(3)))
; __device__ __forceinline__ unsigned cvt_pk_bf16(float lo, float hi) { unsigned r; asm volatile("v_cvt_pk_bf16_f32 %0, %1, %2" : "=v"(r) : "v"(lo), "v"(hi)); return r; }
; __device__ __forceinline__ void xattn_unit(LAS unsigned char* lds, int hd, int qt, const bf16_t* QX, const bf16_t* KX, const bf16_t* VX, bf16_t* O) {
;     ...
;     float mx = -INFINITY;
; #pragma unroll
;     for (int j = 0; j < 16; ++j) mx = fmaxf(mx, fmaxf(fmaxf(S[j][0], S[j][1]), fmaxf(S[j][2], S[j][3])));
;     mx = fmaxf(mx, __shfl_xor(mx, 16)); mx = fmaxf(mx, __shfl_xor(mx, 32));
;     const float SC = 0.044194173824159216f;
;     float sum = 0.f;
; #pragma unroll
;     for (int j = 0; j < 16; ++j) { float pv[4];
; #pragma unroll
;         for (int i = 0; i < 4; ++i) { pv[i] = __expf((S[j][i] - mx) * SC); sum += pv[i]; }
;         u32x2 w; w.x = cvt_pk_bf16(pv[0], pv[1]); w.y = cvt_pk_bf16(pv[2], pv[3]);
;         *(LAS u32x2*)(Pw + fr * PRS + (16 * j + 4 * fq) * 2) = w; }
.LBB0_982:
	s_nop 2
	v_max_f32_e32 v2, v97, v97
	v_max_f32_e32 v3, v96, v96
	v_max_f32_e32 v2, v3, v2
	v_max_f32_e32 v3, v93, v93
	v_max_f32_e32 v4, v92, v92
	v_max_f32_e32 v3, v4, v3
	v_max3_f32 v2, v94, v95, v2
	v_max3_f32 v3, v90, v91, v3
	v_max3_f32 v2, v2, s35, v3
	v_max_f32_e32 v3, v89, v89
	v_max_f32_e32 v4, v88, v88
	v_max_f32_e32 v3, v4, v3
	v_max_f32_e32 v4, v85, v85
	v_max_f32_e32 v5, v84, v84
	v_max_f32_e32 v4, v5, v4
	v_max3_f32 v3, v86, v87, v3
	v_max3_f32 v4, v82, v83, v4
	v_max3_f32 v2, v2, v3, v4
	v_max_f32_e32 v3, v81, v81
	v_max_f32_e32 v4, v80, v80
	v_max_f32_e32 v3, v4, v3
	v_max_f32_e32 v4, v77, v77
	v_max_f32_e32 v5, v76, v76
	v_max_f32_e32 v4, v5, v4
	v_max3_f32 v3, v78, v79, v3
	v_max3_f32 v4, v74, v75, v4
	v_max3_f32 v2, v2, v3, v4
	v_max_f32_e32 v3, v73, v73
	v_max_f32_e32 v4, v72, v72
	v_max_f32_e32 v3, v4, v3
	v_max_f32_e32 v4, v69, v69
	v_max_f32_e32 v5, v68, v68
	v_max_f32_e32 v4, v5, v4
	v_max3_f32 v3, v70, v71, v3
	v_max3_f32 v4, v66, v67, v4
	v_max3_f32 v2, v2, v3, v4
	v_max_f32_e32 v3, v65, v65
	v_max_f32_e32 v4, v64, v64
	v_max_f32_e32 v3, v4, v3
	v_max_f32_e32 v4, v61, v61
	v_max_f32_e32 v5, v60, v60
	v_max_f32_e32 v4, v5, v4
	v_max3_f32 v3, v62, v63, v3
	v_max3_f32 v4, v58, v59, v4
	v_max3_f32 v2, v2, v3, v4
	v_max_f32_e32 v3, v57, v57
	v_max_f32_e32 v4, v56, v56
	v_max_f32_e32 v3, v4, v3
	v_max_f32_e32 v4, v53, v53
	v_max_f32_e32 v5, v52, v52
	v_max_f32_e32 v4, v5, v4
	v_max3_f32 v3, v54, v55, v3
	v_max3_f32 v4, v50, v51, v4
	v_max3_f32 v2, v2, v3, v4
	v_max_f32_e32 v3, v49, v49
	v_max_f32_e32 v4, v48, v48
	v_max_f32_e32 v3, v4, v3
	v_max_f32_e32 v4, v45, v45
	v_max_f32_e32 v5, v44, v44
	v_max_f32_e32 v4, v5, v4
	v_max3_f32 v3, v46, v47, v3
	v_max3_f32 v4, v42, v43, v4
	v_max3_f32 v2, v2, v3, v4
	v_max_f32_e32 v3, v41, v41
	v_max_f32_e32 v4, v40, v40
	v_max_f32_e32 v3, v4, v3
	v_max_f32_e32 v4, v37, v37
	v_max_f32_e32 v5, v36, v36
	v_max_f32_e32 v4, v5, v4
	v_max3_f32 v3, v38, v39, v3
	v_max3_f32 v4, v34, v35, v4
	v_max3_f32 v4, v2, v3, v4
	v_and_b32_e32 v3, 64, v1
	v_xor_b32_e32 v2, 16, v1
	v_add_u32_e32 v5, 64, v3
	v_cmp_lt_i32_e32 vcc, v2, v5
	v_mov_b32_e32 v3, s15
	s_mulk_i32 s13, 0x210
	v_cndmask_b32_e32 v2, v1, v2, vcc
	v_lshlrev_b32_e32 v100, 2, v2
	ds_bpermute_b32 v6, v100, v4
	v_or_b32_e32 v2, s14, v114
	v_lshlrev_b64 v[98:99], 12, v[2:3]
	s_add_i32 s10, s28, s13
	v_lshrrev_b32_e32 v2, 1, v199
	s_waitcnt lgkmcnt(0)
	v_max_f32_e32 v6, v6, v6
	v_max_f32_e32 v4, v4, v6
	v_xor_b32_e32 v6, 32, v1
	v_cmp_lt_i32_e32 vcc, v6, v5
	s_lshl_b32 s12, s12, 1
	s_nop 0
	v_cndmask_b32_e32 v5, v1, v6, vcc
	v_lshlrev_b32_e32 v5, 2, v5
	ds_bpermute_b32 v6, v5, v4
	s_waitcnt lgkmcnt(0)
	v_max_f32_e32 v3, v6, v6
	v_max_f32_e32 v4, v4, v3
	v_mov_b32_e32 v3, s10
	v_mad_u32_u24 v22, v114, s34, v3
	v_add_u32_e32 v6, v22, v2
	v_sub_f32_e32 v2, v94, v4
	v_mul_f32_e32 v2, 0x3d3504f3, v2
	v_sub_f32_e32 v3, v95, v4
	v_mul_f32_e32 v2, 0x3fb8aa3b, v2
	v_mul_f32_e32 v3, 0x3d3504f3, v3
	v_exp_f32_e32 v2, v2
	v_mul_f32_e32 v3, 0x3fb8aa3b, v3
	v_exp_f32_e32 v3, v3
	v_sub_f32_e32 v7, v96, v4
	v_sub_f32_e32 v8, v97, v4
	v_mul_f32_e32 v7, 0x3d3504f3, v7
	v_mul_f32_e32 v8, 0x3d3504f3, v8
	v_mul_f32_e32 v7, 0x3fb8aa3b, v7
	v_mul_f32_e32 v8, 0x3fb8aa3b, v8
	v_add_f32_e32 v9, 0, v2
	v_cvt_pk_bf16_f32 v2, v2, v3
	v_exp_f32_e32 v7, v7
	v_exp_f32_e32 v8, v8
	v_add_f32_e32 v9, v3, v9
	v_cvt_pk_bf16_f32 v3, v7, v8
	ds_write_b64 v6, v[2:3]
	v_sub_f32_e32 v2, v90, v4
	v_mul_f32_e32 v2, 0x3d3504f3, v2
	v_sub_f32_e32 v3, v91, v4
	v_mul_f32_e32 v2, 0x3fb8aa3b, v2
	v_mul_f32_e32 v3, 0x3d3504f3, v3
	v_exp_f32_e32 v2, v2
	v_mul_f32_e32 v3, 0x3fb8aa3b, v3
	v_add_f32_e32 v9, v7, v9
	v_exp_f32_e32 v3, v3
	v_add_f32_e32 v9, v8, v9
	v_sub_f32_e32 v7, v92, v4
	v_sub_f32_e32 v8, v93, v4
	v_mul_f32_e32 v7, 0x3d3504f3, v7
	v_mul_f32_e32 v8, 0x3d3504f3, v8
	v_mul_f32_e32 v7, 0x3fb8aa3b, v7
	v_mul_f32_e32 v8, 0x3fb8aa3b, v8
	v_add_f32_e32 v9, v2, v9
	v_cvt_pk_bf16_f32 v2, v2, v3
	v_exp_f32_e32 v7, v7
	v_exp_f32_e32 v8, v8
	v_add_f32_e32 v9, v3, v9
	v_cvt_pk_bf16_f32 v3, v7, v8
	ds_write_b64 v6, v[2:3] offset:32
	v_sub_f32_e32 v2, v86, v4
	v_mul_f32_e32 v2, 0x3d3504f3, v2
	v_sub_f32_e32 v3, v87, v4
	v_mul_f32_e32 v2, 0x3fb8aa3b, v2
	v_mul_f32_e32 v3, 0x3d3504f3, v3
	v_exp_f32_e32 v2, v2
	v_mul_f32_e32 v3, 0x3fb8aa3b, v3
	v_add_f32_e32 v9, v7, v9
	v_exp_f32_e32 v3, v3
	v_add_f32_e32 v9, v8, v9
	v_sub_f32_e32 v7, v88, v4
	v_sub_f32_e32 v8, v89, v4
	v_mul_f32_e32 v7, 0x3d3504f3, v7
	v_mul_f32_e32 v8, 0x3d3504f3, v8
	v_mul_f32_e32 v7, 0x3fb8aa3b, v7
	v_mul_f32_e32 v8, 0x3fb8aa3b, v8
	v_add_f32_e32 v9, v2, v9
	v_cvt_pk_bf16_f32 v2, v2, v3
	v_exp_f32_e32 v7, v7
	v_exp_f32_e32 v8, v8
	v_add_f32_e32 v9, v3, v9
	v_cvt_pk_bf16_f32 v3, v7, v8
	ds_write_b64 v6, v[2:3] offset:64
	v_sub_f32_e32 v2, v82, v4
	v_mul_f32_e32 v2, 0x3d3504f3, v2
	v_sub_f32_e32 v3, v83, v4
	v_mul_f32_e32 v2, 0x3fb8aa3b, v2
	v_mul_f32_e32 v3, 0x3d3504f3, v3
	v_exp_f32_e32 v2, v2
	v_mul_f32_e32 v3, 0x3fb8aa3b, v3
	v_add_f32_e32 v9, v7, v9
	v_exp_f32_e32 v3, v3
	v_add_f32_e32 v9, v8, v9
	v_sub_f32_e32 v7, v84, v4
	v_sub_f32_e32 v8, v85, v4
	v_mul_f32_e32 v7, 0x3d3504f3, v7
	v_mul_f32_e32 v8, 0x3d3504f3, v8
	v_mul_f32_e32 v7, 0x3fb8aa3b, v7
	v_mul_f32_e32 v8, 0x3fb8aa3b, v8
	v_add_f32_e32 v9, v2, v9
	v_cvt_pk_bf16_f32 v2, v2, v3
	v_exp_f32_e32 v7, v7
	v_exp_f32_e32 v8, v8
	v_add_f32_e32 v9, v3, v9
	v_cvt_pk_bf16_f32 v3, v7, v8
	ds_write_b64 v6, v[2:3] offset:96
	v_sub_f32_e32 v2, v78, v4
	v_mul_f32_e32 v2, 0x3d3504f3, v2
	v_sub_f32_e32 v3, v79, v4
	v_mul_f32_e32 v2, 0x3fb8aa3b, v2
	v_mul_f32_e32 v3, 0x3d3504f3, v3
	v_exp_f32_e32 v2, v2
	v_mul_f32_e32 v3, 0x3fb8aa3b, v3
	v_add_f32_e32 v9, v7, v9
; #define LAS __attribute__((address_space(3)))
; __device__ __forceinline__ unsigned cvt_pk_bf16(float lo, float hi) { unsigned r; asm volatile("v_cvt_pk_bf16_f32 %0, %1, %2" : "=v"(r) : "v"(lo), "v"(hi)); return r; }
; __device__ __forceinline__ void xattn_unit(LAS unsigned char* lds, int hd, int qt, const bf16_t* QX, const bf16_t* KX, const bf16_t* VX, bf16_t* O) {
;     ...
;     for (int j = 0; j < 16; ++j) { float pv[4];
; #pragma unroll
;         for (int i = 0; i < 4; ++i) { pv[i] = __expf((S[j][i] - mx) * SC); sum += pv[i]; }
;         u32x2 w; w.x = cvt_pk_bf16(pv[0], pv[1]); w.y = cvt_pk_bf16(pv[2], pv[3]);
;         *(LAS u32x2*)(Pw + fr * PRS + (16 * j + 4 * fq) * 2) = w; }
	v_exp_f32_e32 v3, v3
	v_add_f32_e32 v9, v8, v9
	v_sub_f32_e32 v7, v80, v4
	v_sub_f32_e32 v8, v81, v4
	v_mul_f32_e32 v7, 0x3d3504f3, v7
	v_mul_f32_e32 v8, 0x3d3504f3, v8
	v_mul_f32_e32 v7, 0x3fb8aa3b, v7
	v_mul_f32_e32 v8, 0x3fb8aa3b, v8
	v_add_f32_e32 v9, v2, v9
	v_cvt_pk_bf16_f32 v2, v2, v3
	v_exp_f32_e32 v7, v7
	v_exp_f32_e32 v8, v8
	v_add_f32_e32 v9, v3, v9
	v_cvt_pk_bf16_f32 v3, v7, v8
	ds_write_b64 v6, v[2:3] offset:128
	v_sub_f32_e32 v2, v74, v4
	v_mul_f32_e32 v2, 0x3d3504f3, v2
	v_sub_f32_e32 v3, v75, v4
	v_mul_f32_e32 v2, 0x3fb8aa3b, v2
	v_mul_f32_e32 v3, 0x3d3504f3, v3
	v_exp_f32_e32 v2, v2
	v_mul_f32_e32 v3, 0x3fb8aa3b, v3
	v_add_f32_e32 v9, v7, v9
	v_exp_f32_e32 v3, v3
	v_add_f32_e32 v9, v8, v9
	v_sub_f32_e32 v7, v76, v4
	v_sub_f32_e32 v8, v77, v4
	v_mul_f32_e32 v7, 0x3d3504f3, v7
	v_mul_f32_e32 v8, 0x3d3504f3, v8
	v_mul_f32_e32 v7, 0x3fb8aa3b, v7
	v_mul_f32_e32 v8, 0x3fb8aa3b, v8
	v_add_f32_e32 v9, v2, v9
	v_cvt_pk_bf16_f32 v2, v2, v3
	v_exp_f32_e32 v7, v7
	v_exp_f32_e32 v8, v8
	v_add_f32_e32 v9, v3, v9
	v_cvt_pk_bf16_f32 v3, v7, v8
	ds_write_b64 v6, v[2:3] offset:160
	v_sub_f32_e32 v2, v70, v4
	v_mul_f32_e32 v2, 0x3d3504f3, v2
	v_sub_f32_e32 v3, v71, v4
	v_mul_f32_e32 v2, 0x3fb8aa3b, v2
	v_mul_f32_e32 v3, 0x3d3504f3, v3
	v_exp_f32_e32 v2, v2
	v_mul_f32_e32 v3, 0x3fb8aa3b, v3
	v_add_f32_e32 v9, v7, v9
	v_exp_f32_e32 v3, v3
	v_add_f32_e32 v9, v8, v9
	v_sub_f32_e32 v7, v72, v4
	v_sub_f32_e32 v8, v73, v4
	v_mul_f32_e32 v7, 0x3d3504f3, v7
	v_mul_f32_e32 v8, 0x3d3504f3, v8
	v_mul_f32_e32 v7, 0x3fb8aa3b, v7
	v_mul_f32_e32 v8, 0x3fb8aa3b, v8
	v_add_f32_e32 v9, v2, v9
	v_cvt_pk_bf16_f32 v2, v2, v3
	v_exp_f32_e32 v7, v7
	v_exp_f32_e32 v8, v8
	v_add_f32_e32 v9, v3, v9
	v_cvt_pk_bf16_f32 v3, v7, v8
	ds_write_b64 v6, v[2:3] offset:192
	v_sub_f32_e32 v2, v66, v4
	v_mul_f32_e32 v2, 0x3d3504f3, v2
	v_sub_f32_e32 v3, v67, v4
	v_mul_f32_e32 v2, 0x3fb8aa3b, v2
	v_mul_f32_e32 v3, 0x3d3504f3, v3
	v_exp_f32_e32 v2, v2
	v_mul_f32_e32 v3, 0x3fb8aa3b, v3
	v_add_f32_e32 v9, v7, v9
	v_exp_f32_e32 v3, v3
	v_add_f32_e32 v9, v8, v9
	v_sub_f32_e32 v7, v68, v4
	v_sub_f32_e32 v8, v69, v4
	v_mul_f32_e32 v7, 0x3d3504f3, v7
	v_mul_f32_e32 v8, 0x3d3504f3, v8
	v_mul_f32_e32 v7, 0x3fb8aa3b, v7
	v_mul_f32_e32 v8, 0x3fb8aa3b, v8
	v_add_f32_e32 v9, v2, v9
	v_cvt_pk_bf16_f32 v2, v2, v3
	v_exp_f32_e32 v7, v7
	v_exp_f32_e32 v8, v8
	v_add_f32_e32 v9, v3, v9
	v_cvt_pk_bf16_f32 v3, v7, v8
	ds_write_b64 v6, v[2:3] offset:224
	v_sub_f32_e32 v2, v62, v4
	v_mul_f32_e32 v2, 0x3d3504f3, v2
	v_sub_f32_e32 v3, v63, v4
	v_mul_f32_e32 v2, 0x3fb8aa3b, v2
	v_mul_f32_e32 v3, 0x3d3504f3, v3
	v_exp_f32_e32 v2, v2
	v_mul_f32_e32 v3, 0x3fb8aa3b, v3
	v_add_f32_e32 v9, v7, v9
	v_exp_f32_e32 v3, v3
	v_add_f32_e32 v9, v8, v9
	v_sub_f32_e32 v7, v64, v4
	v_sub_f32_e32 v8, v65, v4
	v_mul_f32_e32 v7, 0x3d3504f3, v7
	v_mul_f32_e32 v8, 0x3d3504f3, v8
	v_mul_f32_e32 v7, 0x3fb8aa3b, v7
	v_mul_f32_e32 v8, 0x3fb8aa3b, v8
	v_add_f32_e32 v9, v2, v9
	v_cvt_pk_bf16_f32 v2, v2, v3
	v_exp_f32_e32 v7, v7
	v_exp_f32_e32 v8, v8
	v_add_f32_e32 v9, v3, v9
	v_cvt_pk_bf16_f32 v3, v7, v8
	ds_write_b64 v6, v[2:3] offset:256
	v_sub_f32_e32 v2, v58, v4
	v_mul_f32_e32 v2, 0x3d3504f3, v2
	v_sub_f32_e32 v3, v59, v4
	v_mul_f32_e32 v2, 0x3fb8aa3b, v2
	v_mul_f32_e32 v3, 0x3d3504f3, v3
	v_exp_f32_e32 v2, v2
	v_mul_f32_e32 v3, 0x3fb8aa3b, v3
	v_add_f32_e32 v9, v7, v9
	v_exp_f32_e32 v3, v3
	v_add_f32_e32 v9, v8, v9
	v_sub_f32_e32 v7, v60, v4
	v_sub_f32_e32 v8, v61, v4
	v_mul_f32_e32 v7, 0x3d3504f3, v7
	v_mul_f32_e32 v8, 0x3d3504f3, v8
	v_mul_f32_e32 v7, 0x3fb8aa3b, v7
	v_mul_f32_e32 v8, 0x3fb8aa3b, v8
	v_add_f32_e32 v9, v2, v9
	v_cvt_pk_bf16_f32 v2, v2, v3
	v_exp_f32_e32 v7, v7
	v_exp_f32_e32 v8, v8
	v_add_f32_e32 v9, v3, v9
	v_cvt_pk_bf16_f32 v3, v7, v8
	ds_write_b64 v6, v[2:3] offset:288
	v_sub_f32_e32 v2, v54, v4
	v_mul_f32_e32 v2, 0x3d3504f3, v2
	v_sub_f32_e32 v3, v55, v4
	v_mul_f32_e32 v2, 0x3fb8aa3b, v2
	v_mul_f32_e32 v3, 0x3d3504f3, v3
	v_exp_f32_e32 v2, v2
	v_mul_f32_e32 v3, 0x3fb8aa3b, v3
	v_add_f32_e32 v9, v7, v9
	v_exp_f32_e32 v3, v3
	v_add_f32_e32 v9, v8, v9
	v_sub_f32_e32 v7, v56, v4
	v_sub_f32_e32 v8, v57, v4
	v_mul_f32_e32 v7, 0x3d3504f3, v7
	v_mul_f32_e32 v8, 0x3d3504f3, v8
	v_mul_f32_e32 v7, 0x3fb8aa3b, v7
	v_mul_f32_e32 v8, 0x3fb8aa3b, v8
	v_add_f32_e32 v9, v2, v9
	v_cvt_pk_bf16_f32 v2, v2, v3
	v_exp_f32_e32 v7, v7
	v_exp_f32_e32 v8, v8
	v_add_f32_e32 v9, v3, v9
	v_cvt_pk_bf16_f32 v3, v7, v8
	ds_write_b64 v6, v[2:3] offset:320
	v_sub_f32_e32 v2, v50, v4
	v_mul_f32_e32 v2, 0x3d3504f3, v2
	v_sub_f32_e32 v3, v51, v4
	v_mul_f32_e32 v2, 0x3fb8aa3b, v2
	v_mul_f32_e32 v3, 0x3d3504f3, v3
	v_exp_f32_e32 v2, v2
	v_mul_f32_e32 v3, 0x3fb8aa3b, v3
	v_add_f32_e32 v9, v7, v9
	v_exp_f32_e32 v3, v3
	v_add_f32_e32 v9, v8, v9
	v_sub_f32_e32 v7, v52, v4
	v_sub_f32_e32 v8, v53, v4
	v_mul_f32_e32 v7, 0x3d3504f3, v7
	v_mul_f32_e32 v8, 0x3d3504f3, v8
	v_mul_f32_e32 v7, 0x3fb8aa3b, v7
	v_mul_f32_e32 v8, 0x3fb8aa3b, v8
	v_add_f32_e32 v9, v2, v9
	v_cvt_pk_bf16_f32 v2, v2, v3
	v_exp_f32_e32 v7, v7
	v_exp_f32_e32 v8, v8
	v_add_f32_e32 v9, v3, v9
	v_cvt_pk_bf16_f32 v3, v7, v8
	ds_write_b64 v6, v[2:3] offset:352
	v_sub_f32_e32 v2, v46, v4
	v_mul_f32_e32 v2, 0x3d3504f3, v2
	v_sub_f32_e32 v3, v47, v4
	v_mul_f32_e32 v2, 0x3fb8aa3b, v2
	v_mul_f32_e32 v3, 0x3d3504f3, v3
	v_exp_f32_e32 v2, v2
	v_mul_f32_e32 v3, 0x3fb8aa3b, v3
	v_add_f32_e32 v9, v7, v9
	v_exp_f32_e32 v3, v3
	v_add_f32_e32 v9, v8, v9
	v_sub_f32_e32 v7, v48, v4
	v_sub_f32_e32 v8, v49, v4
	v_mul_f32_e32 v7, 0x3d3504f3, v7
	v_mul_f32_e32 v8, 0x3d3504f3, v8
	v_mul_f32_e32 v7, 0x3fb8aa3b, v7
	v_mul_f32_e32 v8, 0x3fb8aa3b, v8
	v_add_f32_e32 v9, v2, v9
	v_cvt_pk_bf16_f32 v2, v2, v3
; #define LAS __attribute__((address_space(3)))
; __device__ __forceinline__ unsigned cvt_pk_bf16(float lo, float hi) { unsigned r; asm volatile("v_cvt_pk_bf16_f32 %0, %1, %2" : "=v"(r) : "v"(lo), "v"(hi)); return r; }
; __device__ __forceinline__ void xattn_unit(LAS unsigned char* lds, int hd, int qt, const bf16_t* QX, const bf16_t* KX, const bf16_t* VX, bf16_t* O) {
;     ...
;     for (int j = 0; j < 16; ++j) { float pv[4];
; #pragma unroll
;         for (int i = 0; i < 4; ++i) { pv[i] = __expf((S[j][i] - mx) * SC); sum += pv[i]; }
;         u32x2 w; w.x = cvt_pk_bf16(pv[0], pv[1]); w.y = cvt_pk_bf16(pv[2], pv[3]);
;         *(LAS u32x2*)(Pw + fr * PRS + (16 * j + 4 * fq) * 2) = w; }
;     sum += __shfl_xor(sum, 16); sum += __shfl_xor(sum, 32);
;     const float inv = 1.0f / sum;
;     asm volatile("s_waitcnt lgkmcnt(0)" ::: "memory");
;     stage_load<NMEM, 128>(pf, VX + hd * XD, D, tid);
;     bf16x8 ap[8];
; #pragma unroll
;     for (int ks = 0; ks < 8; ++ks) ap[ks] = *(const LAS bf16x8*)(Pw + fr * PRS + (32 * ks + 8 * fq) * 2);
	v_exp_f32_e32 v7, v7
	v_exp_f32_e32 v8, v8
	v_add_f32_e32 v9, v3, v9
	v_cvt_pk_bf16_f32 v3, v7, v8
	ds_write_b64 v6, v[2:3] offset:384
	v_sub_f32_e32 v2, v42, v4
	v_mul_f32_e32 v2, 0x3d3504f3, v2
	v_sub_f32_e32 v3, v43, v4
	v_mul_f32_e32 v2, 0x3fb8aa3b, v2
	v_mul_f32_e32 v3, 0x3d3504f3, v3
	v_exp_f32_e32 v2, v2
	v_mul_f32_e32 v3, 0x3fb8aa3b, v3
	v_exp_f32_e32 v3, v3
	v_add_f32_e32 v9, v7, v9
	v_add_f32_e32 v9, v8, v9
	v_add_f32_e32 v9, v2, v9
	v_add_f32_e32 v9, v3, v9
	v_cvt_pk_bf16_f32 v2, v2, v3
	v_sub_f32_e32 v3, v38, v4
	v_mul_f32_e32 v3, 0x3d3504f3, v3
	v_mul_f32_e32 v3, 0x3fb8aa3b, v3
	v_sub_f32_e32 v7, v44, v4
	v_exp_f32_e32 v10, v3
	v_sub_f32_e32 v3, v39, v4
	v_mul_f32_e32 v7, 0x3d3504f3, v7
	v_sub_f32_e32 v8, v45, v4
	v_mul_f32_e32 v3, 0x3d3504f3, v3
	v_mul_f32_e32 v7, 0x3fb8aa3b, v7
	v_mul_f32_e32 v8, 0x3d3504f3, v8
	v_mul_f32_e32 v3, 0x3fb8aa3b, v3
	v_exp_f32_e32 v7, v7
	v_mul_f32_e32 v8, 0x3fb8aa3b, v8
	v_exp_f32_e32 v11, v3
	v_sub_f32_e32 v3, v40, v4
	v_exp_f32_e32 v8, v8
	v_mul_f32_e32 v3, 0x3d3504f3, v3
	v_mul_f32_e32 v3, 0x3fb8aa3b, v3
	v_exp_f32_e32 v12, v3
	v_sub_f32_e32 v3, v41, v4
	v_add_f32_e32 v9, v7, v9
	v_mul_f32_e32 v3, 0x3d3504f3, v3
	v_add_f32_e32 v9, v8, v9
	v_mul_f32_e32 v3, 0x3fb8aa3b, v3
	v_exp_f32_e32 v13, v3
	v_add_f32_e32 v3, v10, v9
	v_sub_f32_e32 v9, v34, v4
	v_mul_f32_e32 v9, 0x3d3504f3, v9
	v_sub_f32_e32 v14, v35, v4
	v_mul_f32_e32 v9, 0x3fb8aa3b, v9
	v_mul_f32_e32 v14, 0x3d3504f3, v14
	v_sub_f32_e32 v15, v36, v4
	v_exp_f32_e32 v9, v9
	v_mul_f32_e32 v14, 0x3fb8aa3b, v14
	v_mul_f32_e32 v15, 0x3d3504f3, v15
	v_sub_f32_e32 v4, v37, v4
	v_add_f32_e32 v3, v11, v3
	v_exp_f32_e32 v14, v14
	v_mul_f32_e32 v15, 0x3fb8aa3b, v15
	v_mul_f32_e32 v4, 0x3d3504f3, v4
	v_add_f32_e32 v3, v12, v3
	v_exp_f32_e32 v15, v15
	v_mul_f32_e32 v4, 0x3fb8aa3b, v4
	v_add_f32_e32 v3, v13, v3
	v_exp_f32_e32 v4, v4
	v_add_f32_e32 v3, v9, v3
	v_add_f32_e32 v3, v14, v3
	v_add_f32_e32 v3, v15, v3
	v_add_f32_e32 v16, v4, v3
	ds_bpermute_b32 v17, v100, v16
	v_cvt_pk_bf16_f32 v3, v7, v8
	ds_write_b64 v6, v[2:3] offset:416
	v_cvt_pk_bf16_f32 v2, v10, v11
	v_cvt_pk_bf16_f32 v3, v12, v13
	s_waitcnt lgkmcnt(1)
	v_add_f32_e32 v7, v16, v17
	ds_bpermute_b32 v5, v5, v7
	s_add_u32 s10, s24, s12
	ds_write_b64 v6, v[2:3] offset:448
	v_cvt_pk_bf16_f32 v2, v9, v14
	v_cvt_pk_bf16_f32 v3, v15, v4
	s_addc_u32 s11, s25, 0
	ds_write_b64 v6, v[2:3] offset:480
	v_lshl_add_u64 v[2:3], s[10:11], 0, v[124:125]
	s_waitcnt lgkmcnt(0)
	v_lshl_add_u64 v[10:11], v[126:127], 1, v[2:3]
	v_lshl_add_u64 v[2:3], s[10:11], 0, v[130:131]
	s_waitcnt lgkmcnt(2)
	v_add_f32_e32 v66, v7, v5
	v_lshl_add_u64 v[12:13], v[132:133], 1, v[2:3]
	global_load_dwordx4 v[2:5], v[10:11], off
	global_load_dwordx4 v[6:9], v[12:13], off
	v_lshl_add_u64 v[10:11], s[10:11], 0, v[136:137]
	v_lshl_add_u64 v[18:19], v[138:139], 1, v[10:11]
	v_lshl_add_u64 v[10:11], s[10:11], 0, v[142:143]
	v_lshl_add_u64 v[20:21], v[144:145], 1, v[10:11]
	global_load_dwordx4 v[10:13], v[18:19], off
	global_load_dwordx4 v[14:17], v[20:21], off
	v_lshl_add_u64 v[18:19], s[10:11], 0, v[148:149]
	v_lshl_add_u64 v[18:19], v[150:151], 1, v[18:19]
	v_lshl_add_u64 v[20:21], s[10:11], 0, v[156:157]
	v_lshl_add_u64 v[20:21], v[158:159], 1, v[20:21]
	global_load_dwordx4 v[34:37], v[18:19], off
	global_load_dwordx4 v[38:41], v[20:21], off
	v_lshl_add_u64 v[18:19], s[10:11], 0, v[162:163]
	v_lshl_add_u64 v[18:19], v[164:165], 1, v[18:19]
	v_lshl_add_u64 v[20:21], s[10:11], 0, v[174:175]
	v_lshl_add_u64 v[20:21], v[176:177], 1, v[20:21]
	global_load_dwordx4 v[58:61], v[18:19], off
	global_load_dwordx4 v[62:65], v[20:21], off
	global_load_dword v240, v[20:21], off
	global_load_dword v241, v[20:21], off
	global_load_dword v242, v[20:21], off
	global_load_dword v243, v[20:21], off
	v_div_scale_f32 v67, s[10:11], v66, v66, 1.0
	v_rcp_f32_e32 v68, v67
	v_add_u32_e32 v54, v22, v199
	ds_read_b128 v[18:21], v54
	ds_read_b128 v[22:25], v54 offset:64
	ds_read_b128 v[26:29], v54 offset:128
	ds_read_b128 v[30:33], v54 offset:192
	ds_read_b128 v[42:45], v54 offset:256
	ds_read_b128 v[46:49], v54 offset:320
	ds_read_b128 v[50:53], v54 offset:384
	ds_read_b128 v[54:57], v54 offset:448
	v_fma_f32 v69, -v67, v68, 1.0
	v_fmac_f32_e32 v68, v69, v68
	v_div_scale_f32 v69, vcc, 1.0, v66, 1.0
	v_mul_f32_e32 v70, v69, v68
	v_fma_f32 v71, -v67, v70, v69
	v_fmac_f32_e32 v70, v71, v68
	v_fma_f32 v67, -v67, v70, v69
	v_div_fmas_f32 v67, v67, v68, v70
	v_div_fixup_f32 v84, v67, v66, 1.0
	v_mul_lo_u32 v66, v116, s36
	v_add_u32_e32 v94, s17, v66
	v_mul_lo_u32 v66, v118, s36
	v_add_u32_e32 v95, s17, v66
	v_mul_lo_u32 v66, v120, s36
	v_add_u32_e32 v96, s17, v66
	v_mul_lo_u32 v66, v122, s36
	v_add_u32_e32 v97, s17, v66
	v_mul_lo_u32 v66, v128, s36
	v_add_u32_e32 v101, s17, v66
	v_mul_lo_u32 v66, v134, s36
	v_add_u32_e32 v102, s17, v66
	v_mul_lo_u32 v66, v140, s36
	v_add_u32_e32 v103, s17, v66
	v_mul_lo_u32 v66, v146, s36
	v_add_u32_e32 v104, s17, v66
	v_bfe_u32 v66, v198, 2, 2
	v_lshrrev_b32_e32 v68, 1, v198
	s_add_u32 s10, s26, s12
	v_and_or_b32 v69, v68, 24, v66
	v_lshlrev_b32_e32 v66, 3, v198
	s_addc_u32 s11, s27, 0
	v_and_b32_e32 v70, 24, v66
	v_and_b32_e32 v71, 16, v198
	v_lshl_add_u64 v[66:67], s[10:11], 0, v[98:99]
	v_and_b32_e32 v114, 16, v68
	v_mul_u32_u24_e32 v68, 0x120, v69
	v_lshl_add_u64 v[66:67], v[66:67], 0, v[114:115]
	v_add3_u32 v85, s17, v70, v68
	v_lshlrev_b32_e32 v114, 1, v71
	v_cmp_eq_u32_e32 vcc, 0, v71
	v_add_u32_e32 v86, 0x10080, v85
	v_add_u32_e32 v87, 0x100a0, v85
	v_add_u32_e32 v88, 0x100c0, v85
	v_add_u32_e32 v89, 0x100e0, v85
	v_add_u32_e32 v90, 0x10100, v85
	v_add_u32_e32 v91, 0x10120, v85
	v_add_u32_e32 v92, 0x10140, v85
	v_add_u32_e32 v93, 0x10160, v85
	v_lshl_add_u64 v[66:67], v[66:67], 0, v[114:115]
	v_lshl_add_u64 v[68:69], s[8:9], 0, v[166:167]
	v_lshl_add_u64 v[70:71], s[8:9], 0, v[168:169]
	v_lshl_add_u64 v[72:73], s[8:9], 0, v[170:171]
	v_lshl_add_u64 v[74:75], s[8:9], 0, v[172:173]
	v_lshl_add_u64 v[76:77], s[8:9], 0, v[178:179]
	v_lshl_add_u64 v[78:79], s[8:9], 0, v[160:161]
	v_lshl_add_u64 v[80:81], s[8:9], 0, v[154:155]
	v_lshl_add_u64 v[82:83], s[8:9], 0, v[152:153]
	s_mov_b64 s[10:11], 0
	v_add_u32_e32 v94, v94, v117
	v_add_u32_e32 v95, v95, v119
	v_add_u32_e32 v96, v96, v121
	v_add_u32_e32 v97, v97, v123
	v_add_u32_e32 v98, v101, v129
	v_add_u32_e32 v99, v102, v135
	v_add_u32_e32 v101, v103, v141
	v_add_u32_e32 v102, v104, v147
	s_mov_b64 s[12:13], 0
	s_branch .LBB0_984

; __device__ __forceinline__ void xattn_unit(LAS unsigned char* lds, int hd, int qt, const bf16_t* QX, const bf16_t* KX, const bf16_t* VX, bf16_t* O) {
;     ...
;     for (int vc = 0; vc < 4; ++vc) {
;         __syncthreads();
;         stage_store<NMEM, 128, 16>(X, pf, tid);
;         if (vc < 3) stage_load<NMEM, 128>(pf, VX + hd * XD + (vc + 1) * 128, D, tid);
.LBB0_984:
	s_cmpk_eq_i32 s12, 0x300
	s_mov_b64 s[14:15], 0x180
	s_waitcnt lgkmcnt(0)
	s_barrier
	s_waitcnt vmcnt(11)
	ds_write_b128 v94, v[2:5]
	s_waitcnt vmcnt(10)
	ds_write_b128 v95, v[6:9]
	s_waitcnt vmcnt(9)
	ds_write_b128 v96, v[10:13]
	s_waitcnt vmcnt(8)
	ds_write_b128 v97, v[14:17]
	s_waitcnt vmcnt(7)
	ds_write_b128 v98, v[34:37]
	s_waitcnt vmcnt(6)
	ds_write_b128 v99, v[38:41]
	s_waitcnt vmcnt(5)
	ds_write_b128 v101, v[58:61]
	s_waitcnt vmcnt(4)
	ds_write_b128 v102, v[62:65]
	s_cbranch_scc1 .LBB0_983
	v_lshl_add_u64 v[10:11], v[82:83], 0, s[12:13]
	v_lshl_add_u64 v[12:13], v[80:81], 0, s[12:13]
	v_lshl_add_u64 v[34:35], v[78:79], 0, s[12:13]
	v_lshl_add_u64 v[36:37], v[76:77], 0, s[12:13]
	v_lshl_add_u64 v[58:59], v[74:75], 0, s[12:13]
	v_lshl_add_u64 v[60:61], v[72:73], 0, s[12:13]
	v_lshl_add_u64 v[104:105], v[70:71], 0, s[12:13]
	global_load_dwordx4 v[2:5], v[10:11], off
	global_load_dwordx4 v[6:9], v[12:13], off
	s_nop 0
	global_load_dwordx4 v[10:13], v[34:35], off
	global_load_dwordx4 v[14:17], v[36:37], off
	s_nop 0
	global_load_dwordx4 v[34:37], v[58:59], off
	global_load_dwordx4 v[38:41], v[60:61], off
	v_lshl_add_u64 v[106:107], v[68:69], 0, s[12:13]
	global_load_dwordx4 v[58:61], v[104:105], off
	global_load_dwordx4 v[62:65], v[106:107], off
	s_mov_b64 s[14:15], s[10:11]
	s_branch .LBB0_983

; #define LAS __attribute__((address_space(3)))
; __device__ __forceinline__ unsigned cvt_pk_bf16(float lo, float hi) { unsigned r; asm volatile("v_cvt_pk_bf16_f32 %0, %1, %2" : "=v"(r) : "v"(lo), "v"(hi)); return r; }
; __device__ __forceinline__ void xattn_unit(LAS unsigned char* lds, int hd, int qt, const bf16_t* QX, const bf16_t* KX, const bf16_t* VX, bf16_t* O) {
;     ...
;     float mx = -INFINITY;
; #pragma unroll
;     for (int j = 0; j < 16; ++j) mx = fmaxf(mx, fmaxf(fmaxf(S[j][0], S[j][1]), fmaxf(S[j][2], S[j][3])));
;     mx = fmaxf(mx, __shfl_xor(mx, 16)); mx = fmaxf(mx, __shfl_xor(mx, 32));
;     const float SC = 0.044194173824159216f;
;     float sum = 0.f;
; #pragma unroll
;     for (int j = 0; j < 16; ++j) { float pv[4];
; #pragma unroll
;         for (int i = 0; i < 4; ++i) { pv[i] = __expf((S[j][i] - mx) * SC); sum += pv[i]; }
;         u32x2 w; w.x = cvt_pk_bf16(pv[0], pv[1]); w.y = cvt_pk_bf16(pv[2], pv[3]);
;         *(LAS u32x2*)(Pw + fr * PRS + (16 * j + 4 * fq) * 2) = w; }
.LBB0_1817:
	s_nop 2
	v_max_f32_e32 v2, v97, v97
	v_max_f32_e32 v3, v96, v96
	v_max_f32_e32 v2, v3, v2
	v_max_f32_e32 v3, v93, v93
	v_max_f32_e32 v4, v92, v92
	v_max_f32_e32 v3, v4, v3
	v_max3_f32 v2, v94, v95, v2
	v_max3_f32 v3, v90, v91, v3
	v_max3_f32 v2, v2, s35, v3
	v_max_f32_e32 v3, v89, v89
	v_max_f32_e32 v4, v88, v88
	v_max_f32_e32 v3, v4, v3
	v_max_f32_e32 v4, v85, v85
	v_max_f32_e32 v5, v84, v84
	v_max_f32_e32 v4, v5, v4
	v_max3_f32 v3, v86, v87, v3
	v_max3_f32 v4, v82, v83, v4
	v_max3_f32 v2, v2, v3, v4
	v_max_f32_e32 v3, v81, v81
	v_max_f32_e32 v4, v80, v80
	v_max_f32_e32 v3, v4, v3
	v_max_f32_e32 v4, v77, v77
	v_max_f32_e32 v5, v76, v76
	v_max_f32_e32 v4, v5, v4
	v_max3_f32 v3, v78, v79, v3
	v_max3_f32 v4, v74, v75, v4
	v_max3_f32 v2, v2, v3, v4
	v_max_f32_e32 v3, v73, v73
	v_max_f32_e32 v4, v72, v72
	v_max_f32_e32 v3, v4, v3
	v_max_f32_e32 v4, v69, v69
	v_max_f32_e32 v5, v68, v68
	v_max_f32_e32 v4, v5, v4
	v_max3_f32 v3, v70, v71, v3
	v_max3_f32 v4, v66, v67, v4
	v_max3_f32 v2, v2, v3, v4
	v_max_f32_e32 v3, v65, v65
	v_max_f32_e32 v4, v64, v64
	v_max_f32_e32 v3, v4, v3
	v_max_f32_e32 v4, v61, v61
	v_max_f32_e32 v5, v60, v60
	v_max_f32_e32 v4, v5, v4
	v_max3_f32 v3, v62, v63, v3
	v_max3_f32 v4, v58, v59, v4
	v_max3_f32 v2, v2, v3, v4
	v_max_f32_e32 v3, v57, v57
	v_max_f32_e32 v4, v56, v56
	v_max_f32_e32 v3, v4, v3
	v_max_f32_e32 v4, v53, v53
	v_max_f32_e32 v5, v52, v52
	v_max_f32_e32 v4, v5, v4
	v_max3_f32 v3, v54, v55, v3
	v_max3_f32 v4, v50, v51, v4
	v_max3_f32 v2, v2, v3, v4
	v_max_f32_e32 v3, v49, v49
	v_max_f32_e32 v4, v48, v48
	v_max_f32_e32 v3, v4, v3
	v_max_f32_e32 v4, v45, v45
	v_max_f32_e32 v5, v44, v44
	v_max_f32_e32 v4, v5, v4
	v_max3_f32 v3, v46, v47, v3
	v_max3_f32 v4, v42, v43, v4
	v_max3_f32 v2, v2, v3, v4
	v_max_f32_e32 v3, v41, v41
	v_max_f32_e32 v4, v40, v40
	v_max_f32_e32 v3, v4, v3
	v_max_f32_e32 v4, v37, v37
	v_max_f32_e32 v5, v36, v36
	v_max_f32_e32 v4, v5, v4
	v_max3_f32 v3, v38, v39, v3
	v_max3_f32 v4, v34, v35, v4
	v_max3_f32 v4, v2, v3, v4
	v_and_b32_e32 v3, 64, v1
	v_xor_b32_e32 v2, 16, v1
	v_add_u32_e32 v5, 64, v3
	v_cmp_lt_i32_e32 vcc, v2, v5
	v_mov_b32_e32 v3, s17
	s_mulk_i32 s15, 0x210
	v_cndmask_b32_e32 v2, v1, v2, vcc
	v_lshlrev_b32_e32 v100, 2, v2
	ds_bpermute_b32 v6, v100, v4
	v_or_b32_e32 v2, s16, v114
	v_lshlrev_b64 v[98:99], 12, v[2:3]
	s_add_i32 s12, s28, s15
	v_lshrrev_b32_e32 v2, 1, v199
	s_waitcnt lgkmcnt(0)
	v_max_f32_e32 v6, v6, v6
	v_max_f32_e32 v4, v4, v6
	v_xor_b32_e32 v6, 32, v1
	v_cmp_lt_i32_e32 vcc, v6, v5
	s_lshl_b32 s14, s14, 1
	s_nop 0
	v_cndmask_b32_e32 v5, v1, v6, vcc
	v_lshlrev_b32_e32 v5, 2, v5
	ds_bpermute_b32 v6, v5, v4
	s_waitcnt lgkmcnt(0)
	v_max_f32_e32 v3, v6, v6
	v_max_f32_e32 v4, v4, v3
	v_mov_b32_e32 v3, s12
	v_mad_u32_u24 v22, v114, s34, v3
	v_add_u32_e32 v6, v22, v2
	v_sub_f32_e32 v2, v94, v4
	v_mul_f32_e32 v2, 0x3d3504f3, v2
	v_sub_f32_e32 v3, v95, v4
	v_mul_f32_e32 v2, 0x3fb8aa3b, v2
	v_mul_f32_e32 v3, 0x3d3504f3, v3
	v_exp_f32_e32 v2, v2
	v_mul_f32_e32 v3, 0x3fb8aa3b, v3
	v_exp_f32_e32 v3, v3
	v_sub_f32_e32 v7, v96, v4
	v_sub_f32_e32 v8, v97, v4
	v_mul_f32_e32 v7, 0x3d3504f3, v7
	v_mul_f32_e32 v8, 0x3d3504f3, v8
	v_mul_f32_e32 v7, 0x3fb8aa3b, v7
	v_mul_f32_e32 v8, 0x3fb8aa3b, v8
	v_add_f32_e32 v9, 0, v2
	v_cvt_pk_bf16_f32 v2, v2, v3
	v_exp_f32_e32 v7, v7
	v_exp_f32_e32 v8, v8
	v_add_f32_e32 v9, v3, v9
	v_cvt_pk_bf16_f32 v3, v7, v8
	ds_write_b64 v6, v[2:3]
	v_sub_f32_e32 v2, v90, v4
	v_mul_f32_e32 v2, 0x3d3504f3, v2
	v_sub_f32_e32 v3, v91, v4
	v_mul_f32_e32 v2, 0x3fb8aa3b, v2
	v_mul_f32_e32 v3, 0x3d3504f3, v3
	v_exp_f32_e32 v2, v2
	v_mul_f32_e32 v3, 0x3fb8aa3b, v3
	v_add_f32_e32 v9, v7, v9
	v_exp_f32_e32 v3, v3
	v_add_f32_e32 v9, v8, v9
	v_sub_f32_e32 v7, v92, v4
	v_sub_f32_e32 v8, v93, v4
	v_mul_f32_e32 v7, 0x3d3504f3, v7
	v_mul_f32_e32 v8, 0x3d3504f3, v8
	v_mul_f32_e32 v7, 0x3fb8aa3b, v7
	v_mul_f32_e32 v8, 0x3fb8aa3b, v8
	v_add_f32_e32 v9, v2, v9
	v_cvt_pk_bf16_f32 v2, v2, v3
	v_exp_f32_e32 v7, v7
	v_exp_f32_e32 v8, v8
	v_add_f32_e32 v9, v3, v9
	v_cvt_pk_bf16_f32 v3, v7, v8
	ds_write_b64 v6, v[2:3] offset:32
	v_sub_f32_e32 v2, v86, v4
	v_mul_f32_e32 v2, 0x3d3504f3, v2
	v_sub_f32_e32 v3, v87, v4
	v_mul_f32_e32 v2, 0x3fb8aa3b, v2
	v_mul_f32_e32 v3, 0x3d3504f3, v3
	v_exp_f32_e32 v2, v2
	v_mul_f32_e32 v3, 0x3fb8aa3b, v3
	v_add_f32_e32 v9, v7, v9
	v_exp_f32_e32 v3, v3
	v_add_f32_e32 v9, v8, v9
	v_sub_f32_e32 v7, v88, v4
	v_sub_f32_e32 v8, v89, v4
	v_mul_f32_e32 v7, 0x3d3504f3, v7
	v_mul_f32_e32 v8, 0x3d3504f3, v8
	v_mul_f32_e32 v7, 0x3fb8aa3b, v7
	v_mul_f32_e32 v8, 0x3fb8aa3b, v8
	v_add_f32_e32 v9, v2, v9
	v_cvt_pk_bf16_f32 v2, v2, v3
	v_exp_f32_e32 v7, v7
	v_exp_f32_e32 v8, v8
	v_add_f32_e32 v9, v3, v9
	v_cvt_pk_bf16_f32 v3, v7, v8
	ds_write_b64 v6, v[2:3] offset:64
	v_sub_f32_e32 v2, v82, v4
	v_mul_f32_e32 v2, 0x3d3504f3, v2
	v_sub_f32_e32 v3, v83, v4
	v_mul_f32_e32 v2, 0x3fb8aa3b, v2
	v_mul_f32_e32 v3, 0x3d3504f3, v3
	v_exp_f32_e32 v2, v2
	v_mul_f32_e32 v3, 0x3fb8aa3b, v3
	v_add_f32_e32 v9, v7, v9
	v_exp_f32_e32 v3, v3
	v_add_f32_e32 v9, v8, v9
	v_sub_f32_e32 v7, v84, v4
	v_sub_f32_e32 v8, v85, v4
	v_mul_f32_e32 v7, 0x3d3504f3, v7
	v_mul_f32_e32 v8, 0x3d3504f3, v8
	v_mul_f32_e32 v7, 0x3fb8aa3b, v7
	v_mul_f32_e32 v8, 0x3fb8aa3b, v8
	v_add_f32_e32 v9, v2, v9
	v_cvt_pk_bf16_f32 v2, v2, v3
	v_exp_f32_e32 v7, v7
	v_exp_f32_e32 v8, v8
	v_add_f32_e32 v9, v3, v9
	v_cvt_pk_bf16_f32 v3, v7, v8
	ds_write_b64 v6, v[2:3] offset:96
	v_sub_f32_e32 v2, v78, v4
	v_mul_f32_e32 v2, 0x3d3504f3, v2
	v_sub_f32_e32 v3, v79, v4
	v_mul_f32_e32 v2, 0x3fb8aa3b, v2
	v_mul_f32_e32 v3, 0x3d3504f3, v3
	v_exp_f32_e32 v2, v2
	v_mul_f32_e32 v3, 0x3fb8aa3b, v3
	v_add_f32_e32 v9, v7, v9
; #define LAS __attribute__((address_space(3)))
; __device__ __forceinline__ unsigned cvt_pk_bf16(float lo, float hi) { unsigned r; asm volatile("v_cvt_pk_bf16_f32 %0, %1, %2" : "=v"(r) : "v"(lo), "v"(hi)); return r; }
; __device__ __forceinline__ void xattn_unit(LAS unsigned char* lds, int hd, int qt, const bf16_t* QX, const bf16_t* KX, const bf16_t* VX, bf16_t* O) {
;     ...
;     for (int j = 0; j < 16; ++j) { float pv[4];
; #pragma unroll
;         for (int i = 0; i < 4; ++i) { pv[i] = __expf((S[j][i] - mx) * SC); sum += pv[i]; }
;         u32x2 w; w.x = cvt_pk_bf16(pv[0], pv[1]); w.y = cvt_pk_bf16(pv[2], pv[3]);
;         *(LAS u32x2*)(Pw + fr * PRS + (16 * j + 4 * fq) * 2) = w; }
	v_exp_f32_e32 v3, v3
	v_add_f32_e32 v9, v8, v9
	v_sub_f32_e32 v7, v80, v4
	v_sub_f32_e32 v8, v81, v4
	v_mul_f32_e32 v7, 0x3d3504f3, v7
	v_mul_f32_e32 v8, 0x3d3504f3, v8
	v_mul_f32_e32 v7, 0x3fb8aa3b, v7
	v_mul_f32_e32 v8, 0x3fb8aa3b, v8
	v_add_f32_e32 v9, v2, v9
	v_cvt_pk_bf16_f32 v2, v2, v3
	v_exp_f32_e32 v7, v7
	v_exp_f32_e32 v8, v8
	v_add_f32_e32 v9, v3, v9
	v_cvt_pk_bf16_f32 v3, v7, v8
	ds_write_b64 v6, v[2:3] offset:128
	v_sub_f32_e32 v2, v74, v4
	v_mul_f32_e32 v2, 0x3d3504f3, v2
	v_sub_f32_e32 v3, v75, v4
	v_mul_f32_e32 v2, 0x3fb8aa3b, v2
	v_mul_f32_e32 v3, 0x3d3504f3, v3
	v_exp_f32_e32 v2, v2
	v_mul_f32_e32 v3, 0x3fb8aa3b, v3
	v_add_f32_e32 v9, v7, v9
	v_exp_f32_e32 v3, v3
	v_add_f32_e32 v9, v8, v9
	v_sub_f32_e32 v7, v76, v4
	v_sub_f32_e32 v8, v77, v4
	v_mul_f32_e32 v7, 0x3d3504f3, v7
	v_mul_f32_e32 v8, 0x3d3504f3, v8
	v_mul_f32_e32 v7, 0x3fb8aa3b, v7
	v_mul_f32_e32 v8, 0x3fb8aa3b, v8
	v_add_f32_e32 v9, v2, v9
	v_cvt_pk_bf16_f32 v2, v2, v3
	v_exp_f32_e32 v7, v7
	v_exp_f32_e32 v8, v8
	v_add_f32_e32 v9, v3, v9
	v_cvt_pk_bf16_f32 v3, v7, v8
	ds_write_b64 v6, v[2:3] offset:160
	v_sub_f32_e32 v2, v70, v4
	v_mul_f32_e32 v2, 0x3d3504f3, v2
	v_sub_f32_e32 v3, v71, v4
	v_mul_f32_e32 v2, 0x3fb8aa3b, v2
	v_mul_f32_e32 v3, 0x3d3504f3, v3
	v_exp_f32_e32 v2, v2
	v_mul_f32_e32 v3, 0x3fb8aa3b, v3
	v_add_f32_e32 v9, v7, v9
	v_exp_f32_e32 v3, v3
	v_add_f32_e32 v9, v8, v9
	v_sub_f32_e32 v7, v72, v4
	v_sub_f32_e32 v8, v73, v4
	v_mul_f32_e32 v7, 0x3d3504f3, v7
	v_mul_f32_e32 v8, 0x3d3504f3, v8
	v_mul_f32_e32 v7, 0x3fb8aa3b, v7
	v_mul_f32_e32 v8, 0x3fb8aa3b, v8
	v_add_f32_e32 v9, v2, v9
	v_cvt_pk_bf16_f32 v2, v2, v3
	v_exp_f32_e32 v7, v7
	v_exp_f32_e32 v8, v8
	v_add_f32_e32 v9, v3, v9
	v_cvt_pk_bf16_f32 v3, v7, v8
	ds_write_b64 v6, v[2:3] offset:192
	v_sub_f32_e32 v2, v66, v4
	v_mul_f32_e32 v2, 0x3d3504f3, v2
	v_sub_f32_e32 v3, v67, v4
	v_mul_f32_e32 v2, 0x3fb8aa3b, v2
	v_mul_f32_e32 v3, 0x3d3504f3, v3
	v_exp_f32_e32 v2, v2
	v_mul_f32_e32 v3, 0x3fb8aa3b, v3
	v_add_f32_e32 v9, v7, v9
	v_exp_f32_e32 v3, v3
	v_add_f32_e32 v9, v8, v9
	v_sub_f32_e32 v7, v68, v4
	v_sub_f32_e32 v8, v69, v4
	v_mul_f32_e32 v7, 0x3d3504f3, v7
	v_mul_f32_e32 v8, 0x3d3504f3, v8
	v_mul_f32_e32 v7, 0x3fb8aa3b, v7
	v_mul_f32_e32 v8, 0x3fb8aa3b, v8
	v_add_f32_e32 v9, v2, v9
	v_cvt_pk_bf16_f32 v2, v2, v3
	v_exp_f32_e32 v7, v7
	v_exp_f32_e32 v8, v8
	v_add_f32_e32 v9, v3, v9
	v_cvt_pk_bf16_f32 v3, v7, v8
	ds_write_b64 v6, v[2:3] offset:224
	v_sub_f32_e32 v2, v62, v4
	v_mul_f32_e32 v2, 0x3d3504f3, v2
	v_sub_f32_e32 v3, v63, v4
	v_mul_f32_e32 v2, 0x3fb8aa3b, v2
	v_mul_f32_e32 v3, 0x3d3504f3, v3
	v_exp_f32_e32 v2, v2
	v_mul_f32_e32 v3, 0x3fb8aa3b, v3
	v_add_f32_e32 v9, v7, v9
	v_exp_f32_e32 v3, v3
	v_add_f32_e32 v9, v8, v9
	v_sub_f32_e32 v7, v64, v4
	v_sub_f32_e32 v8, v65, v4
	v_mul_f32_e32 v7, 0x3d3504f3, v7
	v_mul_f32_e32 v8, 0x3d3504f3, v8
	v_mul_f32_e32 v7, 0x3fb8aa3b, v7
	v_mul_f32_e32 v8, 0x3fb8aa3b, v8
	v_add_f32_e32 v9, v2, v9
	v_cvt_pk_bf16_f32 v2, v2, v3
	v_exp_f32_e32 v7, v7
	v_exp_f32_e32 v8, v8
	v_add_f32_e32 v9, v3, v9
	v_cvt_pk_bf16_f32 v3, v7, v8
	ds_write_b64 v6, v[2:3] offset:256
	v_sub_f32_e32 v2, v58, v4
	v_mul_f32_e32 v2, 0x3d3504f3, v2
	v_sub_f32_e32 v3, v59, v4
	v_mul_f32_e32 v2, 0x3fb8aa3b, v2
	v_mul_f32_e32 v3, 0x3d3504f3, v3
	v_exp_f32_e32 v2, v2
	v_mul_f32_e32 v3, 0x3fb8aa3b, v3
	v_add_f32_e32 v9, v7, v9
	v_exp_f32_e32 v3, v3
	v_add_f32_e32 v9, v8, v9
	v_sub_f32_e32 v7, v60, v4
	v_sub_f32_e32 v8, v61, v4
	v_mul_f32_e32 v7, 0x3d3504f3, v7
	v_mul_f32_e32 v8, 0x3d3504f3, v8
	v_mul_f32_e32 v7, 0x3fb8aa3b, v7
	v_mul_f32_e32 v8, 0x3fb8aa3b, v8
	v_add_f32_e32 v9, v2, v9
	v_cvt_pk_bf16_f32 v2, v2, v3
	v_exp_f32_e32 v7, v7
	v_exp_f32_e32 v8, v8
	v_add_f32_e32 v9, v3, v9
	v_cvt_pk_bf16_f32 v3, v7, v8
	ds_write_b64 v6, v[2:3] offset:288
	v_sub_f32_e32 v2, v54, v4
	v_mul_f32_e32 v2, 0x3d3504f3, v2
	v_sub_f32_e32 v3, v55, v4
	v_mul_f32_e32 v2, 0x3fb8aa3b, v2
	v_mul_f32_e32 v3, 0x3d3504f3, v3
	v_exp_f32_e32 v2, v2
	v_mul_f32_e32 v3, 0x3fb8aa3b, v3
	v_add_f32_e32 v9, v7, v9
	v_exp_f32_e32 v3, v3
	v_add_f32_e32 v9, v8, v9
	v_sub_f32_e32 v7, v56, v4
	v_sub_f32_e32 v8, v57, v4
	v_mul_f32_e32 v7, 0x3d3504f3, v7
	v_mul_f32_e32 v8, 0x3d3504f3, v8
	v_mul_f32_e32 v7, 0x3fb8aa3b, v7
	v_mul_f32_e32 v8, 0x3fb8aa3b, v8
	v_add_f32_e32 v9, v2, v9
	v_cvt_pk_bf16_f32 v2, v2, v3
	v_exp_f32_e32 v7, v7
	v_exp_f32_e32 v8, v8
	v_add_f32_e32 v9, v3, v9
	v_cvt_pk_bf16_f32 v3, v7, v8
	ds_write_b64 v6, v[2:3] offset:320
	v_sub_f32_e32 v2, v50, v4
	v_mul_f32_e32 v2, 0x3d3504f3, v2
	v_sub_f32_e32 v3, v51, v4
	v_mul_f32_e32 v2, 0x3fb8aa3b, v2
	v_mul_f32_e32 v3, 0x3d3504f3, v3
	v_exp_f32_e32 v2, v2
	v_mul_f32_e32 v3, 0x3fb8aa3b, v3
	v_add_f32_e32 v9, v7, v9
	v_exp_f32_e32 v3, v3
	v_add_f32_e32 v9, v8, v9
	v_sub_f32_e32 v7, v52, v4
	v_sub_f32_e32 v8, v53, v4
	v_mul_f32_e32 v7, 0x3d3504f3, v7
	v_mul_f32_e32 v8, 0x3d3504f3, v8
	v_mul_f32_e32 v7, 0x3fb8aa3b, v7
	v_mul_f32_e32 v8, 0x3fb8aa3b, v8
	v_add_f32_e32 v9, v2, v9
	v_cvt_pk_bf16_f32 v2, v2, v3
	v_exp_f32_e32 v7, v7
	v_exp_f32_e32 v8, v8
	v_add_f32_e32 v9, v3, v9
	v_cvt_pk_bf16_f32 v3, v7, v8
	ds_write_b64 v6, v[2:3] offset:352
	v_sub_f32_e32 v2, v46, v4
	v_mul_f32_e32 v2, 0x3d3504f3, v2
	v_sub_f32_e32 v3, v47, v4
	v_mul_f32_e32 v2, 0x3fb8aa3b, v2
	v_mul_f32_e32 v3, 0x3d3504f3, v3
	v_exp_f32_e32 v2, v2
	v_mul_f32_e32 v3, 0x3fb8aa3b, v3
	v_add_f32_e32 v9, v7, v9
	v_exp_f32_e32 v3, v3
	v_add_f32_e32 v9, v8, v9
	v_sub_f32_e32 v7, v48, v4
	v_sub_f32_e32 v8, v49, v4
	v_mul_f32_e32 v7, 0x3d3504f3, v7
	v_mul_f32_e32 v8, 0x3d3504f3, v8
	v_mul_f32_e32 v7, 0x3fb8aa3b, v7
	v_mul_f32_e32 v8, 0x3fb8aa3b, v8
	v_add_f32_e32 v9, v2, v9
	v_cvt_pk_bf16_f32 v2, v2, v3
; #define LAS __attribute__((address_space(3)))
; __device__ __forceinline__ unsigned cvt_pk_bf16(float lo, float hi) { unsigned r; asm volatile("v_cvt_pk_bf16_f32 %0, %1, %2" : "=v"(r) : "v"(lo), "v"(hi)); return r; }
; __device__ __forceinline__ void xattn_unit(LAS unsigned char* lds, int hd, int qt, const bf16_t* QX, const bf16_t* KX, const bf16_t* VX, bf16_t* O) {
;     ...
;     for (int j = 0; j < 16; ++j) { float pv[4];
; #pragma unroll
;         for (int i = 0; i < 4; ++i) { pv[i] = __expf((S[j][i] - mx) * SC); sum += pv[i]; }
;         u32x2 w; w.x = cvt_pk_bf16(pv[0], pv[1]); w.y = cvt_pk_bf16(pv[2], pv[3]);
;         *(LAS u32x2*)(Pw + fr * PRS + (16 * j + 4 * fq) * 2) = w; }
;     sum += __shfl_xor(sum, 16); sum += __shfl_xor(sum, 32);
;     const float inv = 1.0f / sum;
;     asm volatile("s_waitcnt lgkmcnt(0)" ::: "memory");
;     stage_load<NMEM, 128>(pf, VX + hd * XD, D, tid);
;     bf16x8 ap[8];
; #pragma unroll
;     for (int ks = 0; ks < 8; ++ks) ap[ks] = *(const LAS bf16x8*)(Pw + fr * PRS + (32 * ks + 8 * fq) * 2);
	v_exp_f32_e32 v7, v7
	v_exp_f32_e32 v8, v8
	v_add_f32_e32 v9, v3, v9
	v_cvt_pk_bf16_f32 v3, v7, v8
	ds_write_b64 v6, v[2:3] offset:384
	v_sub_f32_e32 v2, v42, v4
	v_mul_f32_e32 v2, 0x3d3504f3, v2
	v_sub_f32_e32 v3, v43, v4
	v_mul_f32_e32 v2, 0x3fb8aa3b, v2
	v_mul_f32_e32 v3, 0x3d3504f3, v3
	v_exp_f32_e32 v2, v2
	v_mul_f32_e32 v3, 0x3fb8aa3b, v3
	v_exp_f32_e32 v3, v3
	v_add_f32_e32 v9, v7, v9
	v_add_f32_e32 v9, v8, v9
	v_add_f32_e32 v9, v2, v9
	v_add_f32_e32 v9, v3, v9
	v_cvt_pk_bf16_f32 v2, v2, v3
	v_sub_f32_e32 v3, v38, v4
	v_mul_f32_e32 v3, 0x3d3504f3, v3
	v_mul_f32_e32 v3, 0x3fb8aa3b, v3
	v_sub_f32_e32 v7, v44, v4
	v_exp_f32_e32 v10, v3
	v_sub_f32_e32 v3, v39, v4
	v_mul_f32_e32 v7, 0x3d3504f3, v7
	v_sub_f32_e32 v8, v45, v4
	v_mul_f32_e32 v3, 0x3d3504f3, v3
	v_mul_f32_e32 v7, 0x3fb8aa3b, v7
	v_mul_f32_e32 v8, 0x3d3504f3, v8
	v_mul_f32_e32 v3, 0x3fb8aa3b, v3
	v_exp_f32_e32 v7, v7
	v_mul_f32_e32 v8, 0x3fb8aa3b, v8
	v_exp_f32_e32 v11, v3
	v_sub_f32_e32 v3, v40, v4
	v_exp_f32_e32 v8, v8
	v_mul_f32_e32 v3, 0x3d3504f3, v3
	v_mul_f32_e32 v3, 0x3fb8aa3b, v3
	v_exp_f32_e32 v12, v3
	v_sub_f32_e32 v3, v41, v4
	v_add_f32_e32 v9, v7, v9
	v_mul_f32_e32 v3, 0x3d3504f3, v3
	v_add_f32_e32 v9, v8, v9
	v_mul_f32_e32 v3, 0x3fb8aa3b, v3
	v_exp_f32_e32 v13, v3
	v_add_f32_e32 v3, v10, v9
	v_sub_f32_e32 v9, v34, v4
	v_mul_f32_e32 v9, 0x3d3504f3, v9
	v_sub_f32_e32 v14, v35, v4
	v_mul_f32_e32 v9, 0x3fb8aa3b, v9
	v_mul_f32_e32 v14, 0x3d3504f3, v14
	v_sub_f32_e32 v15, v36, v4
	v_exp_f32_e32 v9, v9
	v_mul_f32_e32 v14, 0x3fb8aa3b, v14
	v_mul_f32_e32 v15, 0x3d3504f3, v15
	v_sub_f32_e32 v4, v37, v4
	v_add_f32_e32 v3, v11, v3
	v_exp_f32_e32 v14, v14
	v_mul_f32_e32 v15, 0x3fb8aa3b, v15
	v_mul_f32_e32 v4, 0x3d3504f3, v4
	v_add_f32_e32 v3, v12, v3
	v_exp_f32_e32 v15, v15
	v_mul_f32_e32 v4, 0x3fb8aa3b, v4
	v_add_f32_e32 v3, v13, v3
	v_exp_f32_e32 v4, v4
	v_add_f32_e32 v3, v9, v3
	v_add_f32_e32 v3, v14, v3
	v_add_f32_e32 v3, v15, v3
	v_add_f32_e32 v16, v4, v3
	ds_bpermute_b32 v17, v100, v16
	v_cvt_pk_bf16_f32 v3, v7, v8
	ds_write_b64 v6, v[2:3] offset:416
	v_cvt_pk_bf16_f32 v2, v10, v11
	v_cvt_pk_bf16_f32 v3, v12, v13
	s_waitcnt lgkmcnt(1)
	v_add_f32_e32 v7, v16, v17
	ds_bpermute_b32 v5, v5, v7
	s_add_u32 s12, s24, s14
	ds_write_b64 v6, v[2:3] offset:448
	v_cvt_pk_bf16_f32 v2, v9, v14
	v_cvt_pk_bf16_f32 v3, v15, v4
	s_addc_u32 s13, s25, 0
	ds_write_b64 v6, v[2:3] offset:480
	v_lshl_add_u64 v[2:3], s[12:13], 0, v[124:125]
	s_waitcnt lgkmcnt(0)
	v_lshl_add_u64 v[10:11], v[126:127], 1, v[2:3]
	v_lshl_add_u64 v[2:3], s[12:13], 0, v[130:131]
	s_waitcnt lgkmcnt(2)
	v_add_f32_e32 v66, v7, v5
	v_lshl_add_u64 v[12:13], v[132:133], 1, v[2:3]
	global_load_dwordx4 v[2:5], v[10:11], off
	global_load_dwordx4 v[6:9], v[12:13], off
	v_lshl_add_u64 v[10:11], s[12:13], 0, v[136:137]
	v_lshl_add_u64 v[18:19], v[138:139], 1, v[10:11]
	v_lshl_add_u64 v[10:11], s[12:13], 0, v[142:143]
	v_lshl_add_u64 v[20:21], v[144:145], 1, v[10:11]
	global_load_dwordx4 v[10:13], v[18:19], off
	global_load_dwordx4 v[14:17], v[20:21], off
	v_lshl_add_u64 v[18:19], s[12:13], 0, v[148:149]
	v_lshl_add_u64 v[18:19], v[150:151], 1, v[18:19]
	v_lshl_add_u64 v[20:21], s[12:13], 0, v[156:157]
	v_lshl_add_u64 v[20:21], v[158:159], 1, v[20:21]
	global_load_dwordx4 v[34:37], v[18:19], off
	global_load_dwordx4 v[38:41], v[20:21], off
	v_lshl_add_u64 v[18:19], s[12:13], 0, v[162:163]
	v_lshl_add_u64 v[18:19], v[164:165], 1, v[18:19]
	v_lshl_add_u64 v[20:21], s[12:13], 0, v[174:175]
	v_lshl_add_u64 v[20:21], v[176:177], 1, v[20:21]
	global_load_dwordx4 v[58:61], v[18:19], off
	global_load_dwordx4 v[62:65], v[20:21], off
	global_load_dword v240, v[20:21], off
	global_load_dword v241, v[20:21], off
	global_load_dword v242, v[20:21], off
	global_load_dword v243, v[20:21], off
	v_div_scale_f32 v67, s[12:13], v66, v66, 1.0
	v_rcp_f32_e32 v68, v67
	v_add_u32_e32 v54, v22, v199
	ds_read_b128 v[18:21], v54
	ds_read_b128 v[22:25], v54 offset:64
	ds_read_b128 v[26:29], v54 offset:128
	ds_read_b128 v[30:33], v54 offset:192
	ds_read_b128 v[42:45], v54 offset:256
	ds_read_b128 v[46:49], v54 offset:320
	ds_read_b128 v[50:53], v54 offset:384
	ds_read_b128 v[54:57], v54 offset:448
	v_fma_f32 v69, -v67, v68, 1.0
	v_fmac_f32_e32 v68, v69, v68
	v_div_scale_f32 v69, vcc, 1.0, v66, 1.0
	v_mul_f32_e32 v70, v69, v68
	v_fma_f32 v71, -v67, v70, v69
	v_fmac_f32_e32 v70, v71, v68
	v_fma_f32 v67, -v67, v70, v69
	v_div_fmas_f32 v67, v67, v68, v70
	v_div_fixup_f32 v84, v67, v66, 1.0
	v_mul_lo_u32 v66, v116, s36
	v_add_u32_e32 v94, s3, v66
	v_mul_lo_u32 v66, v118, s36
	v_add_u32_e32 v95, s3, v66
	v_mul_lo_u32 v66, v120, s36
	v_add_u32_e32 v96, s3, v66
	v_mul_lo_u32 v66, v122, s36
	v_add_u32_e32 v97, s3, v66
	v_mul_lo_u32 v66, v128, s36
	v_add_u32_e32 v101, s3, v66
	v_mul_lo_u32 v66, v134, s36
	v_add_u32_e32 v102, s3, v66
	v_mul_lo_u32 v66, v140, s36
	v_add_u32_e32 v103, s3, v66
	v_mul_lo_u32 v66, v146, s36
	v_add_u32_e32 v104, s3, v66
	v_bfe_u32 v66, v198, 2, 2
	v_lshrrev_b32_e32 v68, 1, v198
	s_add_u32 s12, s26, s14
	v_and_or_b32 v69, v68, 24, v66
	v_lshlrev_b32_e32 v66, 3, v198
	s_addc_u32 s13, s27, 0
	v_and_b32_e32 v70, 24, v66
	v_and_b32_e32 v71, 16, v198
	v_lshl_add_u64 v[66:67], s[12:13], 0, v[98:99]
	v_and_b32_e32 v114, 16, v68
	v_mul_u32_u24_e32 v68, 0x120, v69
	v_lshl_add_u64 v[66:67], v[66:67], 0, v[114:115]
	v_add3_u32 v85, s3, v70, v68
	v_lshlrev_b32_e32 v114, 1, v71
	v_cmp_eq_u32_e32 vcc, 0, v71
	v_add_u32_e32 v86, 0x10080, v85
	v_add_u32_e32 v87, 0x100a0, v85
	v_add_u32_e32 v88, 0x100c0, v85
	v_add_u32_e32 v89, 0x100e0, v85
	v_add_u32_e32 v90, 0x10100, v85
	v_add_u32_e32 v91, 0x10120, v85
	v_add_u32_e32 v92, 0x10140, v85
	v_add_u32_e32 v93, 0x10160, v85
	v_lshl_add_u64 v[66:67], v[66:67], 0, v[114:115]
	v_lshl_add_u64 v[68:69], s[10:11], 0, v[166:167]
	v_lshl_add_u64 v[70:71], s[10:11], 0, v[168:169]
	v_lshl_add_u64 v[72:73], s[10:11], 0, v[170:171]
	v_lshl_add_u64 v[74:75], s[10:11], 0, v[172:173]
	v_lshl_add_u64 v[76:77], s[10:11], 0, v[178:179]
	v_lshl_add_u64 v[78:79], s[10:11], 0, v[160:161]
	v_lshl_add_u64 v[80:81], s[10:11], 0, v[154:155]
	v_lshl_add_u64 v[82:83], s[10:11], 0, v[152:153]
	s_mov_b64 s[12:13], 0
	v_add_u32_e32 v94, v94, v117
	v_add_u32_e32 v95, v95, v119
	v_add_u32_e32 v96, v96, v121
	v_add_u32_e32 v97, v97, v123
	v_add_u32_e32 v98, v101, v129
	v_add_u32_e32 v99, v102, v135
	v_add_u32_e32 v101, v103, v141
	v_add_u32_e32 v102, v104, v147
	s_mov_b64 s[14:15], 0
	s_branch .LBB0_1819

; __device__ __forceinline__ void xattn_unit(LAS unsigned char* lds, int hd, int qt, const bf16_t* QX, const bf16_t* KX, const bf16_t* VX, bf16_t* O) {
;     ...
;     for (int vc = 0; vc < 4; ++vc) {
;         __syncthreads();
;         stage_store<NMEM, 128, 16>(X, pf, tid);
;         if (vc < 3) stage_load<NMEM, 128>(pf, VX + hd * XD + (vc + 1) * 128, D, tid);
.LBB0_1819:
	s_cmpk_eq_i32 s14, 0x300
	s_mov_b64 s[16:17], 0x180
	s_waitcnt lgkmcnt(0)
	s_barrier
	s_waitcnt vmcnt(11)
	ds_write_b128 v94, v[2:5]
	s_waitcnt vmcnt(10)
	ds_write_b128 v95, v[6:9]
	s_waitcnt vmcnt(9)
	ds_write_b128 v96, v[10:13]
	s_waitcnt vmcnt(8)
	ds_write_b128 v97, v[14:17]
	s_waitcnt vmcnt(7)
	ds_write_b128 v98, v[34:37]
	s_waitcnt vmcnt(6)
	ds_write_b128 v99, v[38:41]
	s_waitcnt vmcnt(5)
	ds_write_b128 v101, v[58:61]
	s_waitcnt vmcnt(4)
	ds_write_b128 v102, v[62:65]
	s_cbranch_scc1 .LBB0_1818
	v_lshl_add_u64 v[10:11], v[82:83], 0, s[14:15]
	v_lshl_add_u64 v[12:13], v[80:81], 0, s[14:15]
	v_lshl_add_u64 v[34:35], v[78:79], 0, s[14:15]
	v_lshl_add_u64 v[36:37], v[76:77], 0, s[14:15]
	v_lshl_add_u64 v[58:59], v[74:75], 0, s[14:15]
	v_lshl_add_u64 v[60:61], v[72:73], 0, s[14:15]
	v_lshl_add_u64 v[104:105], v[70:71], 0, s[14:15]
	global_load_dwordx4 v[2:5], v[10:11], off
	global_load_dwordx4 v[6:9], v[12:13], off
	s_nop 0
	global_load_dwordx4 v[10:13], v[34:35], off
	global_load_dwordx4 v[14:17], v[36:37], off
	s_nop 0
	global_load_dwordx4 v[34:37], v[58:59], off
	global_load_dwordx4 v[38:41], v[60:61], off
	v_lshl_add_u64 v[106:107], v[68:69], 0, s[14:15]
	global_load_dwordx4 v[58:61], v[104:105], off
	global_load_dwordx4 v[62:65], v[106:107], off
	s_mov_b64 s[16:17], s[12:13]
	s_branch .LBB0_1818
